# first K-loop iteration of every GEMM unit peeled: its first MFMA per accumulator takes SrcC=0, so the accumulator-clearing block before the K loop is gone
# speedup vs baseline: 1.0210x; 1.0069x over previous
.LBB0_177:
	s_ashr_i32 s17, s16, 31
	s_lshl_b64 s[18:19], s[16:17], 20
	s_add_u32 s18, s50, s18
	s_addc_u32 s19, s51, s19
	s_and_b64 s[20:21], s[4:5], exec
	s_cselect_b32 s17, s19, s25
	s_cselect_b32 s54, s18, s24
	s_ashr_i32 s15, s14, 31
	s_lshl_b64 s[20:21], s[14:15], 20
	s_add_u32 s20, s3, s20
	s_addc_u32 s21, s30, s21
	s_and_b64 s[28:29], s[4:5], exec
	s_cselect_b32 s15, s21, s27
	s_cselect_b32 s55, s20, s26
	s_add_u32 s24, s24, 0x80080
	s_addc_u32 s25, s25, 0
	s_add_u32 s56, s26, 0x100
	v_mov_b32_e32 v2, 0
	s_addc_u32 s57, s27, 0
	s_mov_b32 s58, -2
	ds_read_b128 v[148:151], v155
	ds_read_b128 v[160:163], v155 offset:1024
	ds_read_b128 v[164:167], v155 offset:2048
	ds_read_b128 v[168:171], v155 offset:3072
	ds_read_b128 v[172:175], v156
	ds_read_b128 v[176:179], v156 offset:1024
	ds_read_b128 v[180:183], v156 offset:2048
	ds_read_b128 v[184:187], v156 offset:3072
	s_add_u32 s26, s24, 0xfff80080
	s_addc_u32 s27, s25, -1
	s_cmp_eq_u32 s58, 28
	s_cselect_b32 s29, s17, s27
	s_cselect_b32 s28, s54, s26
	s_cselect_b32 s27, s15, s57
	s_cselect_b32 s26, s55, s56
	v_lshl_add_u64 v[220:221], s[24:25], 0, v[138:139]
	s_add_i32 m0, s23, 0xc000
	ds_read_b128 v[188:191], v157
	ds_read_b128 v[192:195], v157 offset:1024
	ds_read_b128 v[196:199], v157 offset:2048
	ds_read_b128 v[200:203], v157 offset:3072
	ds_read_b128 v[204:207], v157 offset:4096
	ds_read_b128 v[208:211], v157 offset:5120
	ds_read_b128 v[212:215], v157 offset:6144
	ds_read_b128 v[216:219], v157 offset:7168
	global_load_lds_dwordx4 v[220:221], off
	v_lshl_add_u64 v[220:221], s[24:25], 0, v[140:141]
	s_add_i32 m0, s23, 0xe000
	s_nop 0
	global_load_lds_dwordx4 v[220:221], off
	s_waitcnt vmcnt(8)
	s_waitcnt lgkmcnt(0)
	s_barrier
	s_setprio 1
	s_waitcnt lgkmcnt(0)
	v_mfma_f32_16x16x32_bf16 v[126:129], v[148:151], v[188:191], 0
	v_mfma_f32_16x16x32_bf16 v[122:125], v[164:167], v[188:191], 0
	v_mfma_f32_16x16x32_bf16 v[118:121], v[148:151], v[196:199], 0
	v_mfma_f32_16x16x32_bf16 v[110:113], v[164:167], v[196:199], 0
	v_mfma_f32_16x16x32_bf16 v[102:105], v[148:151], v[204:207], 0
	v_mfma_f32_16x16x32_bf16 v[94:97], v[164:167], v[204:207], 0
	v_mfma_f32_16x16x32_bf16 v[86:89], v[148:151], v[212:215], 0
	v_mfma_f32_16x16x32_bf16 v[78:81], v[164:167], v[212:215], 0
	v_mfma_f32_16x16x32_bf16 v[126:129], v[160:163], v[192:195], v[126:129]
	v_mfma_f32_16x16x32_bf16 v[122:125], v[168:171], v[192:195], v[122:125]
	v_mfma_f32_16x16x32_bf16 v[118:121], v[160:163], v[200:203], v[118:121]
	v_mfma_f32_16x16x32_bf16 v[110:113], v[168:171], v[200:203], v[110:113]
	v_mfma_f32_16x16x32_bf16 v[102:105], v[160:163], v[208:211], v[102:105]
	v_mfma_f32_16x16x32_bf16 v[94:97], v[168:171], v[208:211], v[94:97]
	v_mfma_f32_16x16x32_bf16 v[86:89], v[160:163], v[216:219], v[86:89]
	v_mfma_f32_16x16x32_bf16 v[78:81], v[168:171], v[216:219], v[78:81]
	s_setprio 0
	s_setprio 1
	v_mfma_f32_16x16x32_bf16 v[114:117], v[172:175], v[188:191], 0
	v_mfma_f32_16x16x32_bf16 v[106:109], v[180:183], v[188:191], 0
	v_mfma_f32_16x16x32_bf16 v[98:101], v[172:175], v[196:199], 0
	v_mfma_f32_16x16x32_bf16 v[90:93], v[180:183], v[196:199], 0
	v_mfma_f32_16x16x32_bf16 v[82:85], v[172:175], v[204:207], 0
	v_mfma_f32_16x16x32_bf16 v[74:77], v[180:183], v[204:207], 0
	v_mfma_f32_16x16x32_bf16 v[70:73], v[172:175], v[212:215], 0
	v_mfma_f32_16x16x32_bf16 v[66:69], v[180:183], v[212:215], 0
	v_mfma_f32_16x16x32_bf16 v[114:117], v[176:179], v[192:195], v[114:117]
	v_mfma_f32_16x16x32_bf16 v[106:109], v[184:187], v[192:195], v[106:109]
	v_mfma_f32_16x16x32_bf16 v[98:101], v[176:179], v[200:203], v[98:101]
	v_mfma_f32_16x16x32_bf16 v[90:93], v[184:187], v[200:203], v[90:93]
	v_mfma_f32_16x16x32_bf16 v[82:85], v[176:179], v[208:211], v[82:85]
	v_mfma_f32_16x16x32_bf16 v[74:77], v[184:187], v[208:211], v[74:77]
	v_mfma_f32_16x16x32_bf16 v[70:73], v[176:179], v[216:219], v[70:73]
	v_mfma_f32_16x16x32_bf16 v[66:69], v[184:187], v[216:219], v[66:69]
	s_setprio 0
	s_barrier
	s_add_i32 s59, s42, s31
	v_lshl_add_u64 v[220:221], s[26:27], 0, v[134:135]
	s_mov_b32 m0, s59
	ds_read_b128 v[188:191], v157 offset:16384
	ds_read_b128 v[192:195], v157 offset:17408
	ds_read_b128 v[196:199], v157 offset:18432
	ds_read_b128 v[200:203], v157 offset:19456
	ds_read_b128 v[204:207], v157 offset:20480
	ds_read_b128 v[208:211], v157 offset:21504
	ds_read_b128 v[212:215], v157 offset:22528
	ds_read_b128 v[216:219], v157 offset:23552
	global_load_lds_dwordx4 v[220:221], off
	s_add_i32 m0, s59, 0x2000
	s_add_u32 s60, s26, 0x80000
	v_lshl_add_u64 v[222:223], s[26:27], 0, v[130:131]
	s_addc_u32 s61, s27, 0
	s_add_i32 s59, s43, s31
	global_load_lds_dwordx4 v[222:223], off
	v_lshl_add_u64 v[224:225], s[60:61], 0, v[134:135]
	s_mov_b32 m0, s59
	v_lshl_add_u64 v[226:227], s[28:29], 0, v[132:133]
	global_load_lds_dwordx4 v[224:225], off
	v_lshl_add_u64 v[224:225], s[60:61], 0, v[130:131]
	s_add_i32 m0, s59, 0x2000
	s_nop 0
	global_load_lds_dwordx4 v[224:225], off
	v_lshl_add_u64 v[224:225], s[28:29], 0, v[136:137]
	s_mov_b32 m0, s23
	s_nop 0
	global_load_lds_dwordx4 v[224:225], off
	s_mov_b32 m0, s35
	s_nop 0
	global_load_lds_dwordx4 v[226:227], off
	s_waitcnt vmcnt(8)
	s_waitcnt lgkmcnt(0)
	s_barrier
	s_setprio 1
	s_waitcnt lgkmcnt(0)
	v_mfma_f32_16x16x32_bf16 v[62:65], v[148:151], v[188:191], 0
	v_mfma_f32_16x16x32_bf16 v[58:61], v[164:167], v[188:191], 0
	v_mfma_f32_16x16x32_bf16 v[54:57], v[148:151], v[196:199], 0
	v_mfma_f32_16x16x32_bf16 v[46:49], v[164:167], v[196:199], 0
	v_mfma_f32_16x16x32_bf16 v[38:41], v[148:151], v[204:207], 0
	v_mfma_f32_16x16x32_bf16 v[30:33], v[164:167], v[204:207], 0
	v_mfma_f32_16x16x32_bf16 v[22:25], v[148:151], v[212:215], 0
	v_mfma_f32_16x16x32_bf16 v[14:17], v[164:167], v[212:215], 0
	v_mfma_f32_16x16x32_bf16 v[62:65], v[160:163], v[192:195], v[62:65]
	v_mfma_f32_16x16x32_bf16 v[58:61], v[168:171], v[192:195], v[58:61]
	v_mfma_f32_16x16x32_bf16 v[54:57], v[160:163], v[200:203], v[54:57]
	v_mfma_f32_16x16x32_bf16 v[46:49], v[168:171], v[200:203], v[46:49]
	v_mfma_f32_16x16x32_bf16 v[38:41], v[160:163], v[208:211], v[38:41]
	v_mfma_f32_16x16x32_bf16 v[30:33], v[168:171], v[208:211], v[30:33]
	v_mfma_f32_16x16x32_bf16 v[22:25], v[160:163], v[216:219], v[22:25]
	v_mfma_f32_16x16x32_bf16 v[14:17], v[168:171], v[216:219], v[14:17]
	s_setprio 0
	s_setprio 1
	v_mfma_f32_16x16x32_bf16 v[50:53], v[172:175], v[188:191], 0
	v_mfma_f32_16x16x32_bf16 v[42:45], v[180:183], v[188:191], 0
	v_mfma_f32_16x16x32_bf16 v[34:37], v[172:175], v[196:199], 0
	v_mfma_f32_16x16x32_bf16 v[26:29], v[180:183], v[196:199], 0
	v_mfma_f32_16x16x32_bf16 v[18:21], v[172:175], v[204:207], 0
	v_mfma_f32_16x16x32_bf16 v[10:13], v[180:183], v[204:207], 0
	v_mfma_f32_16x16x32_bf16 v[6:9], v[172:175], v[212:215], 0
	v_mfma_f32_16x16x32_bf16 v[2:5], v[180:183], v[212:215], 0
	v_mfma_f32_16x16x32_bf16 v[50:53], v[176:179], v[192:195], v[50:53]
	v_mfma_f32_16x16x32_bf16 v[42:45], v[184:187], v[192:195], v[42:45]
	v_mfma_f32_16x16x32_bf16 v[34:37], v[176:179], v[200:203], v[34:37]
	v_mfma_f32_16x16x32_bf16 v[26:29], v[184:187], v[200:203], v[26:29]
	v_mfma_f32_16x16x32_bf16 v[18:21], v[176:179], v[208:211], v[18:21]
	v_mfma_f32_16x16x32_bf16 v[10:13], v[184:187], v[208:211], v[10:13]
	v_mfma_f32_16x16x32_bf16 v[6:9], v[176:179], v[216:219], v[6:9]
	v_mfma_f32_16x16x32_bf16 v[2:5], v[184:187], v[216:219], v[2:5]
	s_setprio 0
	s_barrier
	s_add_i32 s59, 0, 0x18000
	v_add_u32_e32 v159, s59, v153
	s_add_i32 s60, 0, 0x1c000
	ds_read_b128 v[148:151], v159
	ds_read_b128 v[160:163], v159 offset:1024
	ds_read_b128 v[164:167], v159 offset:2048
	ds_read_b128 v[168:171], v159 offset:3072
	v_add_u32_e32 v159, s60, v153
	ds_read_b128 v[172:175], v159
	ds_read_b128 v[176:179], v159 offset:1024
	ds_read_b128 v[180:183], v159 offset:2048
	ds_read_b128 v[184:187], v159 offset:3072
	s_add_u32 s28, s28, 0x80000
	s_addc_u32 s29, s29, 0
	s_mov_b32 m0, s36
	v_lshl_add_u64 v[228:229], s[28:29], 0, v[136:137]
	ds_read_b128 v[188:191], v157 offset:32768
	ds_read_b128 v[192:195], v157 offset:33792
	ds_read_b128 v[196:199], v157 offset:34816
	ds_read_b128 v[200:203], v157 offset:35840
	ds_read_b128 v[204:207], v157 offset:36864
	ds_read_b128 v[208:211], v157 offset:37888
	ds_read_b128 v[212:215], v157 offset:38912
	ds_read_b128 v[216:219], v157 offset:39936
	global_load_lds_dwordx4 v[228:229], off
	v_lshl_add_u64 v[228:229], s[28:29], 0, v[132:133]
	s_mov_b32 m0, s37
	s_nop 0
	global_load_lds_dwordx4 v[228:229], off
	s_waitcnt vmcnt(8)
	s_waitcnt lgkmcnt(0)
	s_barrier
	s_setprio 1
	s_waitcnt lgkmcnt(0)
	v_mfma_f32_16x16x32_bf16 v[126:129], v[148:151], v[188:191], v[126:129]
	v_mfma_f32_16x16x32_bf16 v[122:125], v[164:167], v[188:191], v[122:125]
	v_mfma_f32_16x16x32_bf16 v[118:121], v[148:151], v[196:199], v[118:121]
	v_mfma_f32_16x16x32_bf16 v[110:113], v[164:167], v[196:199], v[110:113]
	v_mfma_f32_16x16x32_bf16 v[102:105], v[148:151], v[204:207], v[102:105]
	v_mfma_f32_16x16x32_bf16 v[94:97], v[164:167], v[204:207], v[94:97]
	v_mfma_f32_16x16x32_bf16 v[86:89], v[148:151], v[212:215], v[86:89]
	v_mfma_f32_16x16x32_bf16 v[78:81], v[164:167], v[212:215], v[78:81]
	v_mfma_f32_16x16x32_bf16 v[126:129], v[160:163], v[192:195], v[126:129]
	v_mfma_f32_16x16x32_bf16 v[122:125], v[168:171], v[192:195], v[122:125]
	v_mfma_f32_16x16x32_bf16 v[118:121], v[160:163], v[200:203], v[118:121]
	v_mfma_f32_16x16x32_bf16 v[110:113], v[168:171], v[200:203], v[110:113]
	v_mfma_f32_16x16x32_bf16 v[102:105], v[160:163], v[208:211], v[102:105]
	v_mfma_f32_16x16x32_bf16 v[94:97], v[168:171], v[208:211], v[94:97]
	v_mfma_f32_16x16x32_bf16 v[86:89], v[160:163], v[216:219], v[86:89]
	v_mfma_f32_16x16x32_bf16 v[78:81], v[168:171], v[216:219], v[78:81]
	s_setprio 0
	s_setprio 1
	v_mfma_f32_16x16x32_bf16 v[114:117], v[172:175], v[188:191], v[114:117]
	v_mfma_f32_16x16x32_bf16 v[106:109], v[180:183], v[188:191], v[106:109]
	v_mfma_f32_16x16x32_bf16 v[98:101], v[172:175], v[196:199], v[98:101]
	v_mfma_f32_16x16x32_bf16 v[90:93], v[180:183], v[196:199], v[90:93]
	v_mfma_f32_16x16x32_bf16 v[82:85], v[172:175], v[204:207], v[82:85]
	v_mfma_f32_16x16x32_bf16 v[74:77], v[180:183], v[204:207], v[74:77]
	v_mfma_f32_16x16x32_bf16 v[70:73], v[172:175], v[212:215], v[70:73]
	v_mfma_f32_16x16x32_bf16 v[66:69], v[180:183], v[212:215], v[66:69]
	v_mfma_f32_16x16x32_bf16 v[114:117], v[176:179], v[192:195], v[114:117]
	v_mfma_f32_16x16x32_bf16 v[106:109], v[184:187], v[192:195], v[106:109]
	v_mfma_f32_16x16x32_bf16 v[98:101], v[176:179], v[200:203], v[98:101]
	v_mfma_f32_16x16x32_bf16 v[90:93], v[184:187], v[200:203], v[90:93]
	v_mfma_f32_16x16x32_bf16 v[82:85], v[176:179], v[208:211], v[82:85]
	v_mfma_f32_16x16x32_bf16 v[74:77], v[184:187], v[208:211], v[74:77]
	v_mfma_f32_16x16x32_bf16 v[70:73], v[176:179], v[216:219], v[70:73]
	v_mfma_f32_16x16x32_bf16 v[66:69], v[184:187], v[216:219], v[66:69]
	s_setprio 0
	s_barrier
	s_add_i32 s28, s59, s31
	v_lshl_add_u64 v[220:221], v[220:221], 0, s[10:11]
	s_mov_b32 m0, s28
	ds_read_b128 v[188:191], v157 offset:49152
	ds_read_b128 v[192:195], v157 offset:50176
	ds_read_b128 v[196:199], v157 offset:51200
	ds_read_b128 v[200:203], v157 offset:52224
	ds_read_b128 v[204:207], v157 offset:53248
	ds_read_b128 v[208:211], v157 offset:54272
	ds_read_b128 v[212:215], v157 offset:55296
	ds_read_b128 v[216:219], v157 offset:56320
	global_load_lds_dwordx4 v[220:221], off
	s_add_i32 m0, s28, 0x2000
	s_add_u32 s26, s26, 0x80080
	v_lshl_add_u64 v[220:221], v[222:223], 0, s[10:11]
	s_addc_u32 s27, s27, 0
	s_add_i32 s28, s60, s31
	global_load_lds_dwordx4 v[220:221], off
	v_lshl_add_u64 v[220:221], s[26:27], 0, v[134:135]
	s_mov_b32 m0, s28
	s_nop 0
	global_load_lds_dwordx4 v[220:221], off
	v_lshl_add_u64 v[220:221], s[26:27], 0, v[130:131]
	s_add_i32 m0, s28, 0x2000
	s_nop 0
	global_load_lds_dwordx4 v[220:221], off
	v_lshl_add_u64 v[220:221], v[224:225], 0, s[10:11]
	s_mov_b32 m0, s39
	s_nop 0
	global_load_lds_dwordx4 v[220:221], off
	v_lshl_add_u64 v[220:221], v[226:227], 0, s[10:11]
	s_mov_b32 m0, s40
	s_nop 0
	global_load_lds_dwordx4 v[220:221], off
	s_waitcnt vmcnt(8)
	s_waitcnt lgkmcnt(0)
	s_barrier
	s_setprio 1
	s_waitcnt lgkmcnt(0)
	v_mfma_f32_16x16x32_bf16 v[62:65], v[148:151], v[188:191], v[62:65]
	v_mfma_f32_16x16x32_bf16 v[58:61], v[164:167], v[188:191], v[58:61]
	v_mfma_f32_16x16x32_bf16 v[54:57], v[148:151], v[196:199], v[54:57]
	v_mfma_f32_16x16x32_bf16 v[46:49], v[164:167], v[196:199], v[46:49]
	v_mfma_f32_16x16x32_bf16 v[38:41], v[148:151], v[204:207], v[38:41]
	v_mfma_f32_16x16x32_bf16 v[30:33], v[164:167], v[204:207], v[30:33]
	v_mfma_f32_16x16x32_bf16 v[22:25], v[148:151], v[212:215], v[22:25]
	v_mfma_f32_16x16x32_bf16 v[14:17], v[164:167], v[212:215], v[14:17]
	v_mfma_f32_16x16x32_bf16 v[62:65], v[160:163], v[192:195], v[62:65]
	v_mfma_f32_16x16x32_bf16 v[58:61], v[168:171], v[192:195], v[58:61]
	v_mfma_f32_16x16x32_bf16 v[54:57], v[160:163], v[200:203], v[54:57]
	v_mfma_f32_16x16x32_bf16 v[46:49], v[168:171], v[200:203], v[46:49]
	v_mfma_f32_16x16x32_bf16 v[38:41], v[160:163], v[208:211], v[38:41]
	v_mfma_f32_16x16x32_bf16 v[30:33], v[168:171], v[208:211], v[30:33]
	v_mfma_f32_16x16x32_bf16 v[22:25], v[160:163], v[216:219], v[22:25]
	v_mfma_f32_16x16x32_bf16 v[14:17], v[168:171], v[216:219], v[14:17]
	s_setprio 0
	s_setprio 1
	v_mfma_f32_16x16x32_bf16 v[50:53], v[172:175], v[188:191], v[50:53]
	v_mfma_f32_16x16x32_bf16 v[42:45], v[180:183], v[188:191], v[42:45]
	v_mfma_f32_16x16x32_bf16 v[34:37], v[172:175], v[196:199], v[34:37]
	v_mfma_f32_16x16x32_bf16 v[26:29], v[180:183], v[196:199], v[26:29]
	v_mfma_f32_16x16x32_bf16 v[18:21], v[172:175], v[204:207], v[18:21]
	v_mfma_f32_16x16x32_bf16 v[10:13], v[180:183], v[204:207], v[10:13]
	v_mfma_f32_16x16x32_bf16 v[6:9], v[172:175], v[212:215], v[6:9]
	v_mfma_f32_16x16x32_bf16 v[2:5], v[180:183], v[212:215], v[2:5]
	v_mfma_f32_16x16x32_bf16 v[50:53], v[176:179], v[192:195], v[50:53]
	v_mfma_f32_16x16x32_bf16 v[42:45], v[184:187], v[192:195], v[42:45]
	v_mfma_f32_16x16x32_bf16 v[34:37], v[176:179], v[200:203], v[34:37]
	v_mfma_f32_16x16x32_bf16 v[26:29], v[184:187], v[200:203], v[26:29]
	v_mfma_f32_16x16x32_bf16 v[18:21], v[176:179], v[208:211], v[18:21]
	v_mfma_f32_16x16x32_bf16 v[10:13], v[184:187], v[208:211], v[10:13]
	v_mfma_f32_16x16x32_bf16 v[6:9], v[176:179], v[216:219], v[6:9]
	v_mfma_f32_16x16x32_bf16 v[2:5], v[184:187], v[216:219], v[2:5]
	s_setprio 0
	s_barrier
	s_add_i32 s58, s58, 2
	s_add_u32 s24, s24, 0x100
	s_addc_u32 s25, s25, 0
	s_add_u32 s56, s56, 0x100
	s_addc_u32 s57, s57, 0
	s_cmp_gt_u32 s58, 29
	s_cbranch_scc1 .Lpeel_exit_178
.LBB0_178:
	ds_read_b128 v[148:151], v155
	ds_read_b128 v[160:163], v155 offset:1024
	ds_read_b128 v[164:167], v155 offset:2048
	ds_read_b128 v[168:171], v155 offset:3072
	ds_read_b128 v[172:175], v156
	ds_read_b128 v[176:179], v156 offset:1024
	ds_read_b128 v[180:183], v156 offset:2048
	ds_read_b128 v[184:187], v156 offset:3072
	s_add_u32 s26, s24, 0xfff80080
	s_addc_u32 s27, s25, -1
	s_cmp_eq_u32 s58, 28
	s_cselect_b32 s29, s17, s27
	s_cselect_b32 s28, s54, s26
	s_cselect_b32 s27, s15, s57
	s_cselect_b32 s26, s55, s56
	v_lshl_add_u64 v[220:221], s[24:25], 0, v[138:139]
	s_add_i32 m0, s23, 0xc000
	ds_read_b128 v[188:191], v157
	ds_read_b128 v[192:195], v157 offset:1024
	ds_read_b128 v[196:199], v157 offset:2048
	ds_read_b128 v[200:203], v157 offset:3072
	ds_read_b128 v[204:207], v157 offset:4096
	ds_read_b128 v[208:211], v157 offset:5120
	ds_read_b128 v[212:215], v157 offset:6144
	ds_read_b128 v[216:219], v157 offset:7168
	global_load_lds_dwordx4 v[220:221], off
	v_lshl_add_u64 v[220:221], s[24:25], 0, v[140:141]
	s_add_i32 m0, s23, 0xe000
	s_nop 0
	global_load_lds_dwordx4 v[220:221], off
	s_waitcnt vmcnt(8)
	s_waitcnt lgkmcnt(0)
	s_barrier
	s_setprio 1
	s_waitcnt lgkmcnt(0)
	v_mfma_f32_16x16x32_bf16 v[126:129], v[148:151], v[188:191], v[126:129]
	v_mfma_f32_16x16x32_bf16 v[122:125], v[164:167], v[188:191], v[122:125]
	v_mfma_f32_16x16x32_bf16 v[118:121], v[148:151], v[196:199], v[118:121]
	v_mfma_f32_16x16x32_bf16 v[110:113], v[164:167], v[196:199], v[110:113]
	v_mfma_f32_16x16x32_bf16 v[102:105], v[148:151], v[204:207], v[102:105]
	v_mfma_f32_16x16x32_bf16 v[94:97], v[164:167], v[204:207], v[94:97]
	v_mfma_f32_16x16x32_bf16 v[86:89], v[148:151], v[212:215], v[86:89]
	v_mfma_f32_16x16x32_bf16 v[78:81], v[164:167], v[212:215], v[78:81]
	v_mfma_f32_16x16x32_bf16 v[126:129], v[160:163], v[192:195], v[126:129]
	v_mfma_f32_16x16x32_bf16 v[122:125], v[168:171], v[192:195], v[122:125]
	v_mfma_f32_16x16x32_bf16 v[118:121], v[160:163], v[200:203], v[118:121]
	v_mfma_f32_16x16x32_bf16 v[110:113], v[168:171], v[200:203], v[110:113]
	v_mfma_f32_16x16x32_bf16 v[102:105], v[160:163], v[208:211], v[102:105]
	v_mfma_f32_16x16x32_bf16 v[94:97], v[168:171], v[208:211], v[94:97]
	v_mfma_f32_16x16x32_bf16 v[86:89], v[160:163], v[216:219], v[86:89]
	v_mfma_f32_16x16x32_bf16 v[78:81], v[168:171], v[216:219], v[78:81]
	s_setprio 0
	s_setprio 1
	v_mfma_f32_16x16x32_bf16 v[114:117], v[172:175], v[188:191], v[114:117]
	v_mfma_f32_16x16x32_bf16 v[106:109], v[180:183], v[188:191], v[106:109]
	v_mfma_f32_16x16x32_bf16 v[98:101], v[172:175], v[196:199], v[98:101]
	v_mfma_f32_16x16x32_bf16 v[90:93], v[180:183], v[196:199], v[90:93]
	v_mfma_f32_16x16x32_bf16 v[82:85], v[172:175], v[204:207], v[82:85]
	v_mfma_f32_16x16x32_bf16 v[74:77], v[180:183], v[204:207], v[74:77]
	v_mfma_f32_16x16x32_bf16 v[70:73], v[172:175], v[212:215], v[70:73]
	v_mfma_f32_16x16x32_bf16 v[66:69], v[180:183], v[212:215], v[66:69]
	v_mfma_f32_16x16x32_bf16 v[114:117], v[176:179], v[192:195], v[114:117]
	v_mfma_f32_16x16x32_bf16 v[106:109], v[184:187], v[192:195], v[106:109]
	v_mfma_f32_16x16x32_bf16 v[98:101], v[176:179], v[200:203], v[98:101]
	v_mfma_f32_16x16x32_bf16 v[90:93], v[184:187], v[200:203], v[90:93]
	v_mfma_f32_16x16x32_bf16 v[82:85], v[176:179], v[208:211], v[82:85]
	v_mfma_f32_16x16x32_bf16 v[74:77], v[184:187], v[208:211], v[74:77]
	v_mfma_f32_16x16x32_bf16 v[70:73], v[176:179], v[216:219], v[70:73]
	v_mfma_f32_16x16x32_bf16 v[66:69], v[184:187], v[216:219], v[66:69]
	s_setprio 0
	s_barrier
	s_add_i32 s59, s42, s31
	v_lshl_add_u64 v[220:221], s[26:27], 0, v[134:135]
	s_mov_b32 m0, s59
	ds_read_b128 v[188:191], v157 offset:16384
	ds_read_b128 v[192:195], v157 offset:17408
	ds_read_b128 v[196:199], v157 offset:18432
	ds_read_b128 v[200:203], v157 offset:19456
	ds_read_b128 v[204:207], v157 offset:20480
	ds_read_b128 v[208:211], v157 offset:21504
	ds_read_b128 v[212:215], v157 offset:22528
	ds_read_b128 v[216:219], v157 offset:23552
	global_load_lds_dwordx4 v[220:221], off
	s_add_i32 m0, s59, 0x2000
	s_add_u32 s60, s26, 0x80000
	v_lshl_add_u64 v[222:223], s[26:27], 0, v[130:131]
	s_addc_u32 s61, s27, 0
	s_add_i32 s59, s43, s31
	global_load_lds_dwordx4 v[222:223], off
	v_lshl_add_u64 v[224:225], s[60:61], 0, v[134:135]
	s_mov_b32 m0, s59
	v_lshl_add_u64 v[226:227], s[28:29], 0, v[132:133]
	global_load_lds_dwordx4 v[224:225], off
	v_lshl_add_u64 v[224:225], s[60:61], 0, v[130:131]
	s_add_i32 m0, s59, 0x2000
	s_nop 0
	global_load_lds_dwordx4 v[224:225], off
	v_lshl_add_u64 v[224:225], s[28:29], 0, v[136:137]
	s_mov_b32 m0, s23
	s_nop 0
	global_load_lds_dwordx4 v[224:225], off
	s_mov_b32 m0, s35
	s_nop 0
	global_load_lds_dwordx4 v[226:227], off
	s_waitcnt vmcnt(8)
	s_waitcnt lgkmcnt(0)
	s_barrier
	s_setprio 1
	s_waitcnt lgkmcnt(0)
	v_mfma_f32_16x16x32_bf16 v[62:65], v[148:151], v[188:191], v[62:65]
	v_mfma_f32_16x16x32_bf16 v[58:61], v[164:167], v[188:191], v[58:61]
	v_mfma_f32_16x16x32_bf16 v[54:57], v[148:151], v[196:199], v[54:57]
	v_mfma_f32_16x16x32_bf16 v[46:49], v[164:167], v[196:199], v[46:49]
	v_mfma_f32_16x16x32_bf16 v[38:41], v[148:151], v[204:207], v[38:41]
	v_mfma_f32_16x16x32_bf16 v[30:33], v[164:167], v[204:207], v[30:33]
	v_mfma_f32_16x16x32_bf16 v[22:25], v[148:151], v[212:215], v[22:25]
	v_mfma_f32_16x16x32_bf16 v[14:17], v[164:167], v[212:215], v[14:17]
	v_mfma_f32_16x16x32_bf16 v[62:65], v[160:163], v[192:195], v[62:65]
	v_mfma_f32_16x16x32_bf16 v[58:61], v[168:171], v[192:195], v[58:61]
	v_mfma_f32_16x16x32_bf16 v[54:57], v[160:163], v[200:203], v[54:57]
	v_mfma_f32_16x16x32_bf16 v[46:49], v[168:171], v[200:203], v[46:49]
	v_mfma_f32_16x16x32_bf16 v[38:41], v[160:163], v[208:211], v[38:41]
	v_mfma_f32_16x16x32_bf16 v[30:33], v[168:171], v[208:211], v[30:33]
	v_mfma_f32_16x16x32_bf16 v[22:25], v[160:163], v[216:219], v[22:25]
	v_mfma_f32_16x16x32_bf16 v[14:17], v[168:171], v[216:219], v[14:17]
	s_setprio 0
	s_setprio 1
	v_mfma_f32_16x16x32_bf16 v[50:53], v[172:175], v[188:191], v[50:53]
	v_mfma_f32_16x16x32_bf16 v[42:45], v[180:183], v[188:191], v[42:45]
	v_mfma_f32_16x16x32_bf16 v[34:37], v[172:175], v[196:199], v[34:37]
	v_mfma_f32_16x16x32_bf16 v[26:29], v[180:183], v[196:199], v[26:29]
	v_mfma_f32_16x16x32_bf16 v[18:21], v[172:175], v[204:207], v[18:21]
	v_mfma_f32_16x16x32_bf16 v[10:13], v[180:183], v[204:207], v[10:13]
	v_mfma_f32_16x16x32_bf16 v[6:9], v[172:175], v[212:215], v[6:9]
	v_mfma_f32_16x16x32_bf16 v[2:5], v[180:183], v[212:215], v[2:5]
	v_mfma_f32_16x16x32_bf16 v[50:53], v[176:179], v[192:195], v[50:53]
	v_mfma_f32_16x16x32_bf16 v[42:45], v[184:187], v[192:195], v[42:45]
	v_mfma_f32_16x16x32_bf16 v[34:37], v[176:179], v[200:203], v[34:37]
	v_mfma_f32_16x16x32_bf16 v[26:29], v[184:187], v[200:203], v[26:29]
	v_mfma_f32_16x16x32_bf16 v[18:21], v[176:179], v[208:211], v[18:21]
	v_mfma_f32_16x16x32_bf16 v[10:13], v[184:187], v[208:211], v[10:13]
	v_mfma_f32_16x16x32_bf16 v[6:9], v[176:179], v[216:219], v[6:9]
	v_mfma_f32_16x16x32_bf16 v[2:5], v[184:187], v[216:219], v[2:5]
	s_setprio 0
	s_barrier
	s_add_i32 s59, 0, 0x18000
	v_add_u32_e32 v159, s59, v153
	s_add_i32 s60, 0, 0x1c000
	ds_read_b128 v[148:151], v159
	ds_read_b128 v[160:163], v159 offset:1024
	ds_read_b128 v[164:167], v159 offset:2048
	ds_read_b128 v[168:171], v159 offset:3072
	v_add_u32_e32 v159, s60, v153
	ds_read_b128 v[172:175], v159
	ds_read_b128 v[176:179], v159 offset:1024
	ds_read_b128 v[180:183], v159 offset:2048
	ds_read_b128 v[184:187], v159 offset:3072
	s_add_u32 s28, s28, 0x80000
	s_addc_u32 s29, s29, 0
	s_mov_b32 m0, s36
	v_lshl_add_u64 v[228:229], s[28:29], 0, v[136:137]
	ds_read_b128 v[188:191], v157 offset:32768
	ds_read_b128 v[192:195], v157 offset:33792
	ds_read_b128 v[196:199], v157 offset:34816
	ds_read_b128 v[200:203], v157 offset:35840
	ds_read_b128 v[204:207], v157 offset:36864
	ds_read_b128 v[208:211], v157 offset:37888
	ds_read_b128 v[212:215], v157 offset:38912
	ds_read_b128 v[216:219], v157 offset:39936
	global_load_lds_dwordx4 v[228:229], off
	v_lshl_add_u64 v[228:229], s[28:29], 0, v[132:133]
	s_mov_b32 m0, s37
	s_nop 0
	global_load_lds_dwordx4 v[228:229], off
	s_waitcnt vmcnt(8)
	s_waitcnt lgkmcnt(0)
	s_barrier
	s_setprio 1
	s_waitcnt lgkmcnt(0)
	v_mfma_f32_16x16x32_bf16 v[126:129], v[148:151], v[188:191], v[126:129]
	v_mfma_f32_16x16x32_bf16 v[122:125], v[164:167], v[188:191], v[122:125]
	v_mfma_f32_16x16x32_bf16 v[118:121], v[148:151], v[196:199], v[118:121]
	v_mfma_f32_16x16x32_bf16 v[110:113], v[164:167], v[196:199], v[110:113]
	v_mfma_f32_16x16x32_bf16 v[102:105], v[148:151], v[204:207], v[102:105]
	v_mfma_f32_16x16x32_bf16 v[94:97], v[164:167], v[204:207], v[94:97]
	v_mfma_f32_16x16x32_bf16 v[86:89], v[148:151], v[212:215], v[86:89]
	v_mfma_f32_16x16x32_bf16 v[78:81], v[164:167], v[212:215], v[78:81]
	v_mfma_f32_16x16x32_bf16 v[126:129], v[160:163], v[192:195], v[126:129]
	v_mfma_f32_16x16x32_bf16 v[122:125], v[168:171], v[192:195], v[122:125]
	v_mfma_f32_16x16x32_bf16 v[118:121], v[160:163], v[200:203], v[118:121]
	v_mfma_f32_16x16x32_bf16 v[110:113], v[168:171], v[200:203], v[110:113]
	v_mfma_f32_16x16x32_bf16 v[102:105], v[160:163], v[208:211], v[102:105]
	v_mfma_f32_16x16x32_bf16 v[94:97], v[168:171], v[208:211], v[94:97]
	v_mfma_f32_16x16x32_bf16 v[86:89], v[160:163], v[216:219], v[86:89]
	v_mfma_f32_16x16x32_bf16 v[78:81], v[168:171], v[216:219], v[78:81]
	s_setprio 0
	s_setprio 1
	v_mfma_f32_16x16x32_bf16 v[114:117], v[172:175], v[188:191], v[114:117]
	v_mfma_f32_16x16x32_bf16 v[106:109], v[180:183], v[188:191], v[106:109]
	v_mfma_f32_16x16x32_bf16 v[98:101], v[172:175], v[196:199], v[98:101]
	v_mfma_f32_16x16x32_bf16 v[90:93], v[180:183], v[196:199], v[90:93]
	v_mfma_f32_16x16x32_bf16 v[82:85], v[172:175], v[204:207], v[82:85]
	v_mfma_f32_16x16x32_bf16 v[74:77], v[180:183], v[204:207], v[74:77]
	v_mfma_f32_16x16x32_bf16 v[70:73], v[172:175], v[212:215], v[70:73]
	v_mfma_f32_16x16x32_bf16 v[66:69], v[180:183], v[212:215], v[66:69]
	v_mfma_f32_16x16x32_bf16 v[114:117], v[176:179], v[192:195], v[114:117]
	v_mfma_f32_16x16x32_bf16 v[106:109], v[184:187], v[192:195], v[106:109]
	v_mfma_f32_16x16x32_bf16 v[98:101], v[176:179], v[200:203], v[98:101]
	v_mfma_f32_16x16x32_bf16 v[90:93], v[184:187], v[200:203], v[90:93]
	v_mfma_f32_16x16x32_bf16 v[82:85], v[176:179], v[208:211], v[82:85]
	v_mfma_f32_16x16x32_bf16 v[74:77], v[184:187], v[208:211], v[74:77]
	v_mfma_f32_16x16x32_bf16 v[70:73], v[176:179], v[216:219], v[70:73]
	v_mfma_f32_16x16x32_bf16 v[66:69], v[184:187], v[216:219], v[66:69]
	s_setprio 0
	s_barrier
	s_add_i32 s28, s59, s31
	v_lshl_add_u64 v[220:221], v[220:221], 0, s[10:11]
	s_mov_b32 m0, s28
	ds_read_b128 v[188:191], v157 offset:49152
	ds_read_b128 v[192:195], v157 offset:50176
	ds_read_b128 v[196:199], v157 offset:51200
	ds_read_b128 v[200:203], v157 offset:52224
	ds_read_b128 v[204:207], v157 offset:53248
	ds_read_b128 v[208:211], v157 offset:54272
	ds_read_b128 v[212:215], v157 offset:55296
	ds_read_b128 v[216:219], v157 offset:56320
	global_load_lds_dwordx4 v[220:221], off
	s_add_i32 m0, s28, 0x2000
	s_add_u32 s26, s26, 0x80080
	v_lshl_add_u64 v[220:221], v[222:223], 0, s[10:11]
	s_addc_u32 s27, s27, 0
	s_add_i32 s28, s60, s31
	global_load_lds_dwordx4 v[220:221], off
	v_lshl_add_u64 v[220:221], s[26:27], 0, v[134:135]
	s_mov_b32 m0, s28
	s_nop 0
	global_load_lds_dwordx4 v[220:221], off
	v_lshl_add_u64 v[220:221], s[26:27], 0, v[130:131]
	s_add_i32 m0, s28, 0x2000
	s_nop 0
	global_load_lds_dwordx4 v[220:221], off
	v_lshl_add_u64 v[220:221], v[224:225], 0, s[10:11]
	s_mov_b32 m0, s39
	s_nop 0
	global_load_lds_dwordx4 v[220:221], off
	v_lshl_add_u64 v[220:221], v[226:227], 0, s[10:11]
	s_mov_b32 m0, s40
	s_nop 0
	global_load_lds_dwordx4 v[220:221], off
	s_waitcnt vmcnt(8)
	s_waitcnt lgkmcnt(0)
	s_barrier
	s_setprio 1
	s_waitcnt lgkmcnt(0)
	v_mfma_f32_16x16x32_bf16 v[62:65], v[148:151], v[188:191], v[62:65]
	v_mfma_f32_16x16x32_bf16 v[58:61], v[164:167], v[188:191], v[58:61]
	v_mfma_f32_16x16x32_bf16 v[54:57], v[148:151], v[196:199], v[54:57]
	v_mfma_f32_16x16x32_bf16 v[46:49], v[164:167], v[196:199], v[46:49]
	v_mfma_f32_16x16x32_bf16 v[38:41], v[148:151], v[204:207], v[38:41]
	v_mfma_f32_16x16x32_bf16 v[30:33], v[164:167], v[204:207], v[30:33]
	v_mfma_f32_16x16x32_bf16 v[22:25], v[148:151], v[212:215], v[22:25]
	v_mfma_f32_16x16x32_bf16 v[14:17], v[164:167], v[212:215], v[14:17]
	v_mfma_f32_16x16x32_bf16 v[62:65], v[160:163], v[192:195], v[62:65]
	v_mfma_f32_16x16x32_bf16 v[58:61], v[168:171], v[192:195], v[58:61]
	v_mfma_f32_16x16x32_bf16 v[54:57], v[160:163], v[200:203], v[54:57]
	v_mfma_f32_16x16x32_bf16 v[46:49], v[168:171], v[200:203], v[46:49]
	v_mfma_f32_16x16x32_bf16 v[38:41], v[160:163], v[208:211], v[38:41]
	v_mfma_f32_16x16x32_bf16 v[30:33], v[168:171], v[208:211], v[30:33]
	v_mfma_f32_16x16x32_bf16 v[22:25], v[160:163], v[216:219], v[22:25]
	v_mfma_f32_16x16x32_bf16 v[14:17], v[168:171], v[216:219], v[14:17]
	s_setprio 0
	s_setprio 1
	v_mfma_f32_16x16x32_bf16 v[50:53], v[172:175], v[188:191], v[50:53]
	v_mfma_f32_16x16x32_bf16 v[42:45], v[180:183], v[188:191], v[42:45]
	v_mfma_f32_16x16x32_bf16 v[34:37], v[172:175], v[196:199], v[34:37]
	v_mfma_f32_16x16x32_bf16 v[26:29], v[180:183], v[196:199], v[26:29]
	v_mfma_f32_16x16x32_bf16 v[18:21], v[172:175], v[204:207], v[18:21]
	v_mfma_f32_16x16x32_bf16 v[10:13], v[180:183], v[204:207], v[10:13]
	v_mfma_f32_16x16x32_bf16 v[6:9], v[172:175], v[212:215], v[6:9]
	v_mfma_f32_16x16x32_bf16 v[2:5], v[180:183], v[212:215], v[2:5]
	v_mfma_f32_16x16x32_bf16 v[50:53], v[176:179], v[192:195], v[50:53]
	v_mfma_f32_16x16x32_bf16 v[42:45], v[184:187], v[192:195], v[42:45]
	v_mfma_f32_16x16x32_bf16 v[34:37], v[176:179], v[200:203], v[34:37]
	v_mfma_f32_16x16x32_bf16 v[26:29], v[184:187], v[200:203], v[26:29]
	v_mfma_f32_16x16x32_bf16 v[18:21], v[176:179], v[208:211], v[18:21]
	v_mfma_f32_16x16x32_bf16 v[10:13], v[184:187], v[208:211], v[10:13]
	v_mfma_f32_16x16x32_bf16 v[6:9], v[176:179], v[216:219], v[6:9]
	v_mfma_f32_16x16x32_bf16 v[2:5], v[184:187], v[216:219], v[2:5]
	s_setprio 0
	s_barrier
	s_add_i32 s58, s58, 2
	s_add_u32 s24, s24, 0x100
	s_addc_u32 s25, s25, 0
	s_add_u32 s56, s56, 0x100
	s_addc_u32 s57, s57, 0
	s_cmp_gt_u32 s58, 29
	s_cbranch_scc0 .LBB0_178
.Lpeel_exit_178:
	s_and_b64 vcc, exec, s[12:13]
	s_cbranch_vccz .LBB0_181
	s_barrier
.LBB0_181:
	v_lshl_or_b32 v150, s45, 8, v154
	v_lshl_add_u32 v159, s22, 8, v152
	v_ashrrev_i32_e32 v151, 31, v150
	v_mov_b64_e32 v[148:149], s[8:9]
	v_mad_i64_i32 v[160:161], s[24:25], v159, s44, v[148:149]
	v_lshlrev_b64 v[150:151], 1, v[150:151]
	v_lshl_add_u64 v[160:161], v[160:161], 0, v[150:151]
	v_cvt_pk_bf16_f32 v126, v126, v127
	v_cvt_pk_bf16_f32 v127, v128, v129
	v_cvt_pk_bf16_f32 v128, v122, v123
	v_cvt_pk_bf16_f32 v129, v124, v125
	global_store_dwordx4 v[160:161], v[126:129], off
	v_cvt_pk_bf16_f32 v114, v114, v115
	v_cvt_pk_bf16_f32 v115, v116, v117
	v_cvt_pk_bf16_f32 v116, v106, v107
	v_or_b32_e32 v106, 16, v159
	v_mad_i64_i32 v[106:107], s[24:25], v106, s44, v[148:149]
	v_cvt_pk_bf16_f32 v117, v108, v109
	global_store_dwordx4 v[160:161], v[114:117], off offset:256
	s_andn2_b64 vcc, exec, s[4:5]
	s_mov_b64 s[4:5], -1
	v_lshl_add_u64 v[114:115], v[106:107], 0, v[150:151]
	v_cvt_pk_bf16_f32 v106, v118, v119
	v_cvt_pk_bf16_f32 v107, v120, v121
	v_cvt_pk_bf16_f32 v108, v110, v111
	v_cvt_pk_bf16_f32 v109, v112, v113
	global_store_dwordx4 v[114:115], v[106:109], off
	v_cvt_pk_bf16_f32 v98, v98, v99
	v_cvt_pk_bf16_f32 v99, v100, v101
	v_cvt_pk_bf16_f32 v100, v90, v91
	v_or_b32_e32 v90, 32, v159
	v_mad_i64_i32 v[90:91], s[24:25], v90, s44, v[148:149]
	v_cvt_pk_bf16_f32 v101, v92, v93
	global_store_dwordx4 v[114:115], v[98:101], off offset:256
	s_nop 1
	v_lshl_add_u64 v[98:99], v[90:91], 0, v[150:151]
	v_cvt_pk_bf16_f32 v90, v102, v103
	v_cvt_pk_bf16_f32 v91, v104, v105
	v_cvt_pk_bf16_f32 v92, v94, v95
	v_cvt_pk_bf16_f32 v93, v96, v97
	global_store_dwordx4 v[98:99], v[90:93], off
	v_cvt_pk_bf16_f32 v82, v82, v83
	v_cvt_pk_bf16_f32 v83, v84, v85
	v_cvt_pk_bf16_f32 v84, v74, v75
	v_or_b32_e32 v74, 48, v159
	v_mad_i64_i32 v[74:75], s[24:25], v74, s44, v[148:149]
	v_cvt_pk_bf16_f32 v85, v76, v77
	global_store_dwordx4 v[98:99], v[82:85], off offset:256
	s_nop 1
	v_lshl_add_u64 v[82:83], v[74:75], 0, v[150:151]
	v_cvt_pk_bf16_f32 v74, v86, v87
	v_cvt_pk_bf16_f32 v75, v88, v89
	v_cvt_pk_bf16_f32 v76, v78, v79
	v_cvt_pk_bf16_f32 v77, v80, v81
	global_store_dwordx4 v[82:83], v[74:77], off
	v_cvt_pk_bf16_f32 v70, v70, v71
	v_cvt_pk_bf16_f32 v71, v72, v73
	v_cvt_pk_bf16_f32 v72, v66, v67
	v_add_u32_e32 v66, 0x80, v159
	v_mad_i64_i32 v[66:67], s[24:25], v66, s44, v[148:149]
	v_lshl_add_u64 v[66:67], v[66:67], 0, v[150:151]
	v_cvt_pk_bf16_f32 v73, v68, v69
	global_store_dwordx4 v[82:83], v[70:73], off offset:256
	v_cvt_pk_bf16_f32 v62, v62, v63
	v_cvt_pk_bf16_f32 v63, v64, v65
	v_cvt_pk_bf16_f32 v64, v58, v59
	v_cvt_pk_bf16_f32 v65, v60, v61
	global_store_dwordx4 v[66:67], v[62:65], off
	v_cvt_pk_bf16_f32 v50, v50, v51
	v_cvt_pk_bf16_f32 v51, v52, v53
	v_cvt_pk_bf16_f32 v52, v42, v43
	v_add_u32_e32 v42, 0x90, v159
	v_mad_i64_i32 v[42:43], s[24:25], v42, s44, v[148:149]
	v_cvt_pk_bf16_f32 v53, v44, v45
	global_store_dwordx4 v[66:67], v[50:53], off offset:256
	s_nop 1
	v_lshl_add_u64 v[50:51], v[42:43], 0, v[150:151]
	v_cvt_pk_bf16_f32 v42, v54, v55
	v_cvt_pk_bf16_f32 v43, v56, v57
	v_cvt_pk_bf16_f32 v44, v46, v47
	v_cvt_pk_bf16_f32 v45, v48, v49
	global_store_dwordx4 v[50:51], v[42:45], off
	v_cvt_pk_bf16_f32 v34, v34, v35
	v_cvt_pk_bf16_f32 v35, v36, v37
	v_cvt_pk_bf16_f32 v36, v26, v27
	v_add_u32_e32 v26, 0xa0, v159
	v_mad_i64_i32 v[26:27], s[24:25], v26, s44, v[148:149]
	v_cvt_pk_bf16_f32 v37, v28, v29
	global_store_dwordx4 v[50:51], v[34:37], off offset:256
	s_nop 1
	v_lshl_add_u64 v[34:35], v[26:27], 0, v[150:151]
	v_cvt_pk_bf16_f32 v26, v38, v39
	v_cvt_pk_bf16_f32 v27, v40, v41
	v_cvt_pk_bf16_f32 v28, v30, v31
	v_cvt_pk_bf16_f32 v29, v32, v33
	global_store_dwordx4 v[34:35], v[26:29], off
	v_cvt_pk_bf16_f32 v18, v18, v19
	v_cvt_pk_bf16_f32 v19, v20, v21
	v_cvt_pk_bf16_f32 v20, v10, v11
	v_add_u32_e32 v10, 0xb0, v159
	v_mad_i64_i32 v[10:11], s[24:25], v10, s44, v[148:149]
	v_cvt_pk_bf16_f32 v21, v12, v13
	global_store_dwordx4 v[34:35], v[18:21], off offset:256
	s_nop 1
	v_lshl_add_u64 v[18:19], v[10:11], 0, v[150:151]
	v_cvt_pk_bf16_f32 v10, v22, v23
	v_cvt_pk_bf16_f32 v11, v24, v25
	v_cvt_pk_bf16_f32 v12, v14, v15
	v_cvt_pk_bf16_f32 v13, v16, v17
	global_store_dwordx4 v[18:19], v[10:13], off
	v_cvt_pk_bf16_f32 v6, v6, v7
	v_cvt_pk_bf16_f32 v7, v8, v9
	v_cvt_pk_bf16_f32 v8, v2, v3
	v_cvt_pk_bf16_f32 v9, v4, v5
	global_store_dwordx4 v[18:19], v[6:9], off offset:256
	s_cbranch_vccnz .LBB0_174
	s_andn2_b64 vcc, exec, s[6:7]
	s_cbranch_vccnz .LBB0_173
	s_barrier
	s_branch .LBB0_173

.LBB0_383:
	s_ashr_i32 s19, s18, 31
	s_lshl_b64 s[20:21], s[18:19], 20
	s_add_u32 s20, s70, s20
	s_addc_u32 s21, s71, s21
	s_and_b64 s[22:23], s[6:7], exec
	s_cselect_b32 s19, s21, s29
	s_cselect_b32 s25, s20, s28
	s_ashr_i32 s17, s16, 31
	s_lshl_b64 s[22:23], s[16:17], 20
	s_add_u32 s22, s3, s22
	s_addc_u32 s23, s33, s23
	s_and_b64 s[34:35], s[6:7], exec
	s_cselect_b32 s17, s23, s31
	s_cselect_b32 s56, s22, s30
	s_add_u32 s28, s28, 0x80080
	s_addc_u32 s29, s29, 0
	s_add_u32 s57, s30, 0x100
	v_mov_b32_e32 v2, 0
	s_addc_u32 s58, s31, 0
	s_mov_b32 s59, -2
	s_waitcnt lgkmcnt(0)
	ds_read_b128 v[148:151], v155
	ds_read_b128 v[160:163], v155 offset:1024
	ds_read_b128 v[164:167], v155 offset:2048
	ds_read_b128 v[168:171], v155 offset:3072
	ds_read_b128 v[172:175], v156
	ds_read_b128 v[176:179], v156 offset:1024
	ds_read_b128 v[180:183], v156 offset:2048
	ds_read_b128 v[184:187], v156 offset:3072
	s_add_u32 s30, s28, 0xfff80080
	s_addc_u32 s31, s29, -1
	s_cmp_eq_u32 s59, 28
	s_cselect_b32 s35, s19, s31
	s_cselect_b32 s34, s25, s30
	s_cselect_b32 s31, s17, s58
	s_cselect_b32 s30, s56, s57
	v_lshl_add_u64 v[220:221], s[28:29], 0, v[138:139]
	s_add_i32 m0, s27, 0xc000
	ds_read_b128 v[188:191], v157
	ds_read_b128 v[192:195], v157 offset:1024
	ds_read_b128 v[196:199], v157 offset:2048
	ds_read_b128 v[200:203], v157 offset:3072
	ds_read_b128 v[204:207], v157 offset:4096
	ds_read_b128 v[208:211], v157 offset:5120
	ds_read_b128 v[212:215], v157 offset:6144
	ds_read_b128 v[216:219], v157 offset:7168
	global_load_lds_dwordx4 v[220:221], off
	v_lshl_add_u64 v[220:221], s[28:29], 0, v[140:141]
	s_add_i32 m0, s27, 0xe000
	s_nop 0
	global_load_lds_dwordx4 v[220:221], off
	s_waitcnt vmcnt(8)
	s_waitcnt lgkmcnt(0)
	s_barrier
	s_setprio 1
	s_waitcnt lgkmcnt(0)
	v_mfma_f32_16x16x32_bf16 v[126:129], v[148:151], v[188:191], 0
	v_mfma_f32_16x16x32_bf16 v[122:125], v[164:167], v[188:191], 0
	v_mfma_f32_16x16x32_bf16 v[110:113], v[148:151], v[196:199], 0
	v_mfma_f32_16x16x32_bf16 v[106:109], v[164:167], v[196:199], 0
	v_mfma_f32_16x16x32_bf16 v[94:97], v[148:151], v[204:207], 0
	v_mfma_f32_16x16x32_bf16 v[90:93], v[164:167], v[204:207], 0
	v_mfma_f32_16x16x32_bf16 v[78:81], v[148:151], v[212:215], 0
	v_mfma_f32_16x16x32_bf16 v[74:77], v[164:167], v[212:215], 0
	v_mfma_f32_16x16x32_bf16 v[126:129], v[160:163], v[192:195], v[126:129]
	v_mfma_f32_16x16x32_bf16 v[122:125], v[168:171], v[192:195], v[122:125]
	v_mfma_f32_16x16x32_bf16 v[110:113], v[160:163], v[200:203], v[110:113]
	v_mfma_f32_16x16x32_bf16 v[106:109], v[168:171], v[200:203], v[106:109]
	v_mfma_f32_16x16x32_bf16 v[94:97], v[160:163], v[208:211], v[94:97]
	v_mfma_f32_16x16x32_bf16 v[90:93], v[168:171], v[208:211], v[90:93]
	v_mfma_f32_16x16x32_bf16 v[78:81], v[160:163], v[216:219], v[78:81]
	v_mfma_f32_16x16x32_bf16 v[74:77], v[168:171], v[216:219], v[74:77]
	s_setprio 0
	s_setprio 1
	v_mfma_f32_16x16x32_bf16 v[118:121], v[172:175], v[188:191], 0
	v_mfma_f32_16x16x32_bf16 v[114:117], v[180:183], v[188:191], 0
	v_mfma_f32_16x16x32_bf16 v[102:105], v[172:175], v[196:199], 0
	v_mfma_f32_16x16x32_bf16 v[98:101], v[180:183], v[196:199], 0
	v_mfma_f32_16x16x32_bf16 v[86:89], v[172:175], v[204:207], 0
	v_mfma_f32_16x16x32_bf16 v[82:85], v[180:183], v[204:207], 0
	v_mfma_f32_16x16x32_bf16 v[70:73], v[172:175], v[212:215], 0
	v_mfma_f32_16x16x32_bf16 v[66:69], v[180:183], v[212:215], 0
	v_mfma_f32_16x16x32_bf16 v[118:121], v[176:179], v[192:195], v[118:121]
	v_mfma_f32_16x16x32_bf16 v[114:117], v[184:187], v[192:195], v[114:117]
	v_mfma_f32_16x16x32_bf16 v[102:105], v[176:179], v[200:203], v[102:105]
	v_mfma_f32_16x16x32_bf16 v[98:101], v[184:187], v[200:203], v[98:101]
	v_mfma_f32_16x16x32_bf16 v[86:89], v[176:179], v[208:211], v[86:89]
	v_mfma_f32_16x16x32_bf16 v[82:85], v[184:187], v[208:211], v[82:85]
	v_mfma_f32_16x16x32_bf16 v[70:73], v[176:179], v[216:219], v[70:73]
	v_mfma_f32_16x16x32_bf16 v[66:69], v[184:187], v[216:219], v[66:69]
	s_setprio 0
	s_barrier
	s_add_i32 s60, s45, s36
	v_lshl_add_u64 v[220:221], s[30:31], 0, v[132:133]
	s_mov_b32 m0, s60
	ds_read_b128 v[188:191], v157 offset:16384
	ds_read_b128 v[192:195], v157 offset:17408
	ds_read_b128 v[196:199], v157 offset:18432
	ds_read_b128 v[200:203], v157 offset:19456
	ds_read_b128 v[204:207], v157 offset:20480
	ds_read_b128 v[208:211], v157 offset:21504
	ds_read_b128 v[212:215], v157 offset:22528
	ds_read_b128 v[216:219], v157 offset:23552
	global_load_lds_dwordx4 v[220:221], off
	s_add_i32 m0, s60, 0x2000
	s_add_u32 s60, s30, 0x80000
	v_lshl_add_u64 v[222:223], s[30:31], 0, v[136:137]
	s_addc_u32 s61, s31, 0
	s_add_i32 s62, s54, s36
	global_load_lds_dwordx4 v[222:223], off
	v_lshl_add_u64 v[224:225], s[60:61], 0, v[132:133]
	s_mov_b32 m0, s62
	v_lshl_add_u64 v[226:227], s[34:35], 0, v[134:135]
	global_load_lds_dwordx4 v[224:225], off
	v_lshl_add_u64 v[224:225], s[60:61], 0, v[136:137]
	s_add_i32 m0, s62, 0x2000
	s_nop 0
	global_load_lds_dwordx4 v[224:225], off
	v_lshl_add_u64 v[224:225], s[34:35], 0, v[130:131]
	s_mov_b32 m0, s27
	s_nop 0
	global_load_lds_dwordx4 v[224:225], off
	s_mov_b32 m0, s37
	s_nop 0
	global_load_lds_dwordx4 v[226:227], off
	s_waitcnt vmcnt(8)
	s_waitcnt lgkmcnt(0)
	s_barrier
	s_setprio 1
	s_waitcnt lgkmcnt(0)
	v_mfma_f32_16x16x32_bf16 v[62:65], v[148:151], v[188:191], 0
	v_mfma_f32_16x16x32_bf16 v[58:61], v[164:167], v[188:191], 0
	v_mfma_f32_16x16x32_bf16 v[46:49], v[148:151], v[196:199], 0
	v_mfma_f32_16x16x32_bf16 v[42:45], v[164:167], v[196:199], 0
	v_mfma_f32_16x16x32_bf16 v[30:33], v[148:151], v[204:207], 0
	v_mfma_f32_16x16x32_bf16 v[26:29], v[164:167], v[204:207], 0
	v_mfma_f32_16x16x32_bf16 v[14:17], v[148:151], v[212:215], 0
	v_mfma_f32_16x16x32_bf16 v[10:13], v[164:167], v[212:215], 0
	v_mfma_f32_16x16x32_bf16 v[62:65], v[160:163], v[192:195], v[62:65]
	v_mfma_f32_16x16x32_bf16 v[58:61], v[168:171], v[192:195], v[58:61]
	v_mfma_f32_16x16x32_bf16 v[46:49], v[160:163], v[200:203], v[46:49]
	v_mfma_f32_16x16x32_bf16 v[42:45], v[168:171], v[200:203], v[42:45]
	v_mfma_f32_16x16x32_bf16 v[30:33], v[160:163], v[208:211], v[30:33]
	v_mfma_f32_16x16x32_bf16 v[26:29], v[168:171], v[208:211], v[26:29]
	v_mfma_f32_16x16x32_bf16 v[14:17], v[160:163], v[216:219], v[14:17]
	v_mfma_f32_16x16x32_bf16 v[10:13], v[168:171], v[216:219], v[10:13]
	s_setprio 0
	s_setprio 1
	v_mfma_f32_16x16x32_bf16 v[54:57], v[172:175], v[188:191], 0
	v_mfma_f32_16x16x32_bf16 v[50:53], v[180:183], v[188:191], 0
	v_mfma_f32_16x16x32_bf16 v[38:41], v[172:175], v[196:199], 0
	v_mfma_f32_16x16x32_bf16 v[34:37], v[180:183], v[196:199], 0
	v_mfma_f32_16x16x32_bf16 v[22:25], v[172:175], v[204:207], 0
	v_mfma_f32_16x16x32_bf16 v[18:21], v[180:183], v[204:207], 0
	v_mfma_f32_16x16x32_bf16 v[6:9], v[172:175], v[212:215], 0
	v_mfma_f32_16x16x32_bf16 v[2:5], v[180:183], v[212:215], 0
	v_mfma_f32_16x16x32_bf16 v[54:57], v[176:179], v[192:195], v[54:57]
	v_mfma_f32_16x16x32_bf16 v[50:53], v[184:187], v[192:195], v[50:53]
	v_mfma_f32_16x16x32_bf16 v[38:41], v[176:179], v[200:203], v[38:41]
	v_mfma_f32_16x16x32_bf16 v[34:37], v[184:187], v[200:203], v[34:37]
	v_mfma_f32_16x16x32_bf16 v[22:25], v[176:179], v[208:211], v[22:25]
	v_mfma_f32_16x16x32_bf16 v[18:21], v[184:187], v[208:211], v[18:21]
	v_mfma_f32_16x16x32_bf16 v[6:9], v[176:179], v[216:219], v[6:9]
	v_mfma_f32_16x16x32_bf16 v[2:5], v[184:187], v[216:219], v[2:5]
	s_setprio 0
	s_barrier
	s_add_i32 s60, 0, 0x18000
	s_add_i32 s61, 0, 0x1c000
	v_add_u32_e32 v168, s60, v153
	v_add_u32_e32 v184, s61, v153
	ds_read_b128 v[148:151], v168
	ds_read_b128 v[160:163], v168 offset:1024
	ds_read_b128 v[164:167], v168 offset:2048
	ds_read_b128 v[168:171], v168 offset:3072
	ds_read_b128 v[172:175], v184
	ds_read_b128 v[176:179], v184 offset:1024
	ds_read_b128 v[180:183], v184 offset:2048
	ds_read_b128 v[184:187], v184 offset:3072
	s_add_u32 s34, s34, 0x80000
	s_addc_u32 s35, s35, 0
	s_mov_b32 m0, s38
	v_lshl_add_u64 v[228:229], s[34:35], 0, v[130:131]
	ds_read_b128 v[188:191], v157 offset:32768
	ds_read_b128 v[192:195], v157 offset:33792
	ds_read_b128 v[196:199], v157 offset:34816
	ds_read_b128 v[200:203], v157 offset:35840
	ds_read_b128 v[204:207], v157 offset:36864
	ds_read_b128 v[208:211], v157 offset:37888
	ds_read_b128 v[212:215], v157 offset:38912
	ds_read_b128 v[216:219], v157 offset:39936
	global_load_lds_dwordx4 v[228:229], off
	v_lshl_add_u64 v[228:229], s[34:35], 0, v[134:135]
	s_mov_b32 m0, s39
	s_nop 0
	global_load_lds_dwordx4 v[228:229], off
	s_waitcnt vmcnt(8)
	s_waitcnt lgkmcnt(0)
	s_barrier
	s_setprio 1
	s_waitcnt lgkmcnt(0)
	v_mfma_f32_16x16x32_bf16 v[126:129], v[148:151], v[188:191], v[126:129]
	v_mfma_f32_16x16x32_bf16 v[122:125], v[164:167], v[188:191], v[122:125]
	v_mfma_f32_16x16x32_bf16 v[110:113], v[148:151], v[196:199], v[110:113]
	v_mfma_f32_16x16x32_bf16 v[106:109], v[164:167], v[196:199], v[106:109]
	v_mfma_f32_16x16x32_bf16 v[94:97], v[148:151], v[204:207], v[94:97]
	v_mfma_f32_16x16x32_bf16 v[90:93], v[164:167], v[204:207], v[90:93]
	v_mfma_f32_16x16x32_bf16 v[78:81], v[148:151], v[212:215], v[78:81]
	v_mfma_f32_16x16x32_bf16 v[74:77], v[164:167], v[212:215], v[74:77]
	v_mfma_f32_16x16x32_bf16 v[126:129], v[160:163], v[192:195], v[126:129]
	v_mfma_f32_16x16x32_bf16 v[122:125], v[168:171], v[192:195], v[122:125]
	v_mfma_f32_16x16x32_bf16 v[110:113], v[160:163], v[200:203], v[110:113]
	v_mfma_f32_16x16x32_bf16 v[106:109], v[168:171], v[200:203], v[106:109]
	v_mfma_f32_16x16x32_bf16 v[94:97], v[160:163], v[208:211], v[94:97]
	v_mfma_f32_16x16x32_bf16 v[90:93], v[168:171], v[208:211], v[90:93]
	v_mfma_f32_16x16x32_bf16 v[78:81], v[160:163], v[216:219], v[78:81]
	v_mfma_f32_16x16x32_bf16 v[74:77], v[168:171], v[216:219], v[74:77]
	s_setprio 0
	s_setprio 1
	v_mfma_f32_16x16x32_bf16 v[118:121], v[172:175], v[188:191], v[118:121]
	v_mfma_f32_16x16x32_bf16 v[114:117], v[180:183], v[188:191], v[114:117]
	v_mfma_f32_16x16x32_bf16 v[102:105], v[172:175], v[196:199], v[102:105]
	v_mfma_f32_16x16x32_bf16 v[98:101], v[180:183], v[196:199], v[98:101]
	v_mfma_f32_16x16x32_bf16 v[86:89], v[172:175], v[204:207], v[86:89]
	v_mfma_f32_16x16x32_bf16 v[82:85], v[180:183], v[204:207], v[82:85]
	v_mfma_f32_16x16x32_bf16 v[70:73], v[172:175], v[212:215], v[70:73]
	v_mfma_f32_16x16x32_bf16 v[66:69], v[180:183], v[212:215], v[66:69]
	v_mfma_f32_16x16x32_bf16 v[118:121], v[176:179], v[192:195], v[118:121]
	v_mfma_f32_16x16x32_bf16 v[114:117], v[184:187], v[192:195], v[114:117]
	v_mfma_f32_16x16x32_bf16 v[102:105], v[176:179], v[200:203], v[102:105]
	v_mfma_f32_16x16x32_bf16 v[98:101], v[184:187], v[200:203], v[98:101]
	v_mfma_f32_16x16x32_bf16 v[86:89], v[176:179], v[208:211], v[86:89]
	v_mfma_f32_16x16x32_bf16 v[82:85], v[184:187], v[208:211], v[82:85]
	v_mfma_f32_16x16x32_bf16 v[70:73], v[176:179], v[216:219], v[70:73]
	v_mfma_f32_16x16x32_bf16 v[66:69], v[184:187], v[216:219], v[66:69]
	s_setprio 0
	s_barrier
	s_add_i32 s34, s60, s36
	v_lshl_add_u64 v[220:221], v[220:221], 0, s[12:13]
	s_mov_b32 m0, s34
	ds_read_b128 v[188:191], v157 offset:49152
	ds_read_b128 v[192:195], v157 offset:50176
	ds_read_b128 v[196:199], v157 offset:51200
	ds_read_b128 v[200:203], v157 offset:52224
	ds_read_b128 v[204:207], v157 offset:53248
	ds_read_b128 v[208:211], v157 offset:54272
	ds_read_b128 v[212:215], v157 offset:55296
	ds_read_b128 v[216:219], v157 offset:56320
	global_load_lds_dwordx4 v[220:221], off
	s_add_i32 m0, s34, 0x2000
	s_add_u32 s30, s30, 0x80080
	v_lshl_add_u64 v[220:221], v[222:223], 0, s[12:13]
	s_addc_u32 s31, s31, 0
	s_add_i32 s34, s61, s36
	global_load_lds_dwordx4 v[220:221], off
	v_lshl_add_u64 v[220:221], s[30:31], 0, v[132:133]
	s_mov_b32 m0, s34
	s_nop 0
	global_load_lds_dwordx4 v[220:221], off
	v_lshl_add_u64 v[220:221], s[30:31], 0, v[136:137]
	s_add_i32 m0, s34, 0x2000
	s_nop 0
	global_load_lds_dwordx4 v[220:221], off
	v_lshl_add_u64 v[220:221], v[224:225], 0, s[12:13]
	s_mov_b32 m0, s41
	s_nop 0
	global_load_lds_dwordx4 v[220:221], off
	v_lshl_add_u64 v[220:221], v[226:227], 0, s[12:13]
	s_mov_b32 m0, s42
	s_nop 0
	global_load_lds_dwordx4 v[220:221], off
	s_waitcnt vmcnt(8)
	s_waitcnt lgkmcnt(0)
	s_barrier
	s_setprio 1
	s_waitcnt lgkmcnt(0)
	v_mfma_f32_16x16x32_bf16 v[62:65], v[148:151], v[188:191], v[62:65]
	v_mfma_f32_16x16x32_bf16 v[58:61], v[164:167], v[188:191], v[58:61]
	v_mfma_f32_16x16x32_bf16 v[46:49], v[148:151], v[196:199], v[46:49]
	v_mfma_f32_16x16x32_bf16 v[42:45], v[164:167], v[196:199], v[42:45]
	v_mfma_f32_16x16x32_bf16 v[30:33], v[148:151], v[204:207], v[30:33]
	v_mfma_f32_16x16x32_bf16 v[26:29], v[164:167], v[204:207], v[26:29]
	v_mfma_f32_16x16x32_bf16 v[14:17], v[148:151], v[212:215], v[14:17]
	v_mfma_f32_16x16x32_bf16 v[10:13], v[164:167], v[212:215], v[10:13]
	v_mfma_f32_16x16x32_bf16 v[62:65], v[160:163], v[192:195], v[62:65]
	v_mfma_f32_16x16x32_bf16 v[58:61], v[168:171], v[192:195], v[58:61]
	v_mfma_f32_16x16x32_bf16 v[46:49], v[160:163], v[200:203], v[46:49]
	v_mfma_f32_16x16x32_bf16 v[42:45], v[168:171], v[200:203], v[42:45]
	v_mfma_f32_16x16x32_bf16 v[30:33], v[160:163], v[208:211], v[30:33]
	v_mfma_f32_16x16x32_bf16 v[26:29], v[168:171], v[208:211], v[26:29]
	v_mfma_f32_16x16x32_bf16 v[14:17], v[160:163], v[216:219], v[14:17]
	v_mfma_f32_16x16x32_bf16 v[10:13], v[168:171], v[216:219], v[10:13]
	s_setprio 0
	s_setprio 1
	v_mfma_f32_16x16x32_bf16 v[54:57], v[172:175], v[188:191], v[54:57]
	v_mfma_f32_16x16x32_bf16 v[50:53], v[180:183], v[188:191], v[50:53]
	v_mfma_f32_16x16x32_bf16 v[38:41], v[172:175], v[196:199], v[38:41]
	v_mfma_f32_16x16x32_bf16 v[34:37], v[180:183], v[196:199], v[34:37]
	v_mfma_f32_16x16x32_bf16 v[22:25], v[172:175], v[204:207], v[22:25]
	v_mfma_f32_16x16x32_bf16 v[18:21], v[180:183], v[204:207], v[18:21]
	v_mfma_f32_16x16x32_bf16 v[6:9], v[172:175], v[212:215], v[6:9]
	v_mfma_f32_16x16x32_bf16 v[2:5], v[180:183], v[212:215], v[2:5]
	v_mfma_f32_16x16x32_bf16 v[54:57], v[176:179], v[192:195], v[54:57]
	v_mfma_f32_16x16x32_bf16 v[50:53], v[184:187], v[192:195], v[50:53]
	v_mfma_f32_16x16x32_bf16 v[38:41], v[176:179], v[200:203], v[38:41]
	v_mfma_f32_16x16x32_bf16 v[34:37], v[184:187], v[200:203], v[34:37]
	v_mfma_f32_16x16x32_bf16 v[22:25], v[176:179], v[208:211], v[22:25]
	v_mfma_f32_16x16x32_bf16 v[18:21], v[184:187], v[208:211], v[18:21]
	v_mfma_f32_16x16x32_bf16 v[6:9], v[176:179], v[216:219], v[6:9]
	v_mfma_f32_16x16x32_bf16 v[2:5], v[184:187], v[216:219], v[2:5]
	s_setprio 0
	s_barrier
	s_add_i32 s59, s59, 2
	s_add_u32 s28, s28, 0x100
	s_addc_u32 s29, s29, 0
	s_add_u32 s57, s57, 0x100
	s_addc_u32 s58, s58, 0
	s_cmp_gt_u32 s59, 29
	s_cbranch_scc1 .Lpeel_exit_384

.Lpeel_exit_384:
	s_and_b64 vcc, exec, s[14:15]
	s_cbranch_vccz .LBB0_387
	s_barrier

.LBB0_470:
	s_ashr_i32 s19, s18, 31
	s_lshl_b64 s[20:21], s[18:19], 20
	s_add_u32 s20, s50, s20
	s_addc_u32 s21, s51, s21
	s_and_b64 s[22:23], s[4:5], exec
	s_cselect_b32 s19, s21, s27
	s_cselect_b32 s55, s20, s26
	s_ashr_i32 s17, s16, 31
	s_lshl_b64 s[22:23], s[16:17], 20
	s_add_u32 s22, s3, s22
	s_addc_u32 s23, s33, s23
	s_and_b64 s[30:31], s[4:5], exec
	s_cselect_b32 s17, s23, s29
	s_cselect_b32 s56, s22, s28
	s_add_u32 s26, s26, 0x80080
	s_addc_u32 s27, s27, 0
	s_add_u32 s57, s28, 0x100
	v_mov_b32_e32 v10, 0
	s_addc_u32 s58, s29, 0
	s_mov_b32 s59, -2
	ds_read_b128 v[148:151], v160
	ds_read_b128 v[152:155], v160 offset:1024
	ds_read_b128 v[166:169], v160 offset:2048
	ds_read_b128 v[170:173], v160 offset:3072
	ds_read_b128 v[174:177], v161
	ds_read_b128 v[178:181], v161 offset:1024
	ds_read_b128 v[182:185], v161 offset:2048
	ds_read_b128 v[186:189], v161 offset:3072
	s_add_u32 s28, s26, 0xfff80080
	s_addc_u32 s29, s27, -1
	s_cmp_eq_u32 s59, 28
	s_cselect_b32 s31, s19, s29
	s_cselect_b32 s30, s55, s28
	s_cselect_b32 s29, s17, s58
	s_cselect_b32 s28, s56, s57
	v_lshl_add_u64 v[222:223], s[26:27], 0, v[138:139]
	s_add_i32 m0, s25, 0xc000
	ds_read_b128 v[190:193], v162
	ds_read_b128 v[194:197], v162 offset:1024
	ds_read_b128 v[198:201], v162 offset:2048
	ds_read_b128 v[202:205], v162 offset:3072
	ds_read_b128 v[206:209], v162 offset:4096
	ds_read_b128 v[210:213], v162 offset:5120
	ds_read_b128 v[214:217], v162 offset:6144
	ds_read_b128 v[218:221], v162 offset:7168
	global_load_lds_dwordx4 v[222:223], off
	v_lshl_add_u64 v[222:223], s[26:27], 0, v[140:141]
	s_add_i32 m0, s25, 0xe000
	s_nop 0
	global_load_lds_dwordx4 v[222:223], off
	s_waitcnt vmcnt(8)
	s_waitcnt lgkmcnt(0)
	s_barrier
	s_setprio 1
	s_waitcnt lgkmcnt(0)
	v_mfma_f32_16x16x32_bf16 v[118:121], v[148:151], v[190:193], 0
	v_mfma_f32_16x16x32_bf16 v[114:117], v[166:169], v[190:193], 0
	v_mfma_f32_16x16x32_bf16 v[102:105], v[148:151], v[198:201], 0
	v_mfma_f32_16x16x32_bf16 v[98:101], v[166:169], v[198:201], 0
	v_mfma_f32_16x16x32_bf16 v[86:89], v[148:151], v[206:209], 0
	v_mfma_f32_16x16x32_bf16 v[82:85], v[166:169], v[206:209], 0
	v_mfma_f32_16x16x32_bf16 v[74:77], v[148:151], v[214:217], 0
	v_mfma_f32_16x16x32_bf16 v[70:73], v[166:169], v[214:217], 0
	v_mfma_f32_16x16x32_bf16 v[118:121], v[152:155], v[194:197], v[118:121]
	v_mfma_f32_16x16x32_bf16 v[114:117], v[170:173], v[194:197], v[114:117]
	v_mfma_f32_16x16x32_bf16 v[102:105], v[152:155], v[202:205], v[102:105]
	v_mfma_f32_16x16x32_bf16 v[98:101], v[170:173], v[202:205], v[98:101]
	v_mfma_f32_16x16x32_bf16 v[86:89], v[152:155], v[210:213], v[86:89]
	v_mfma_f32_16x16x32_bf16 v[82:85], v[170:173], v[210:213], v[82:85]
	v_mfma_f32_16x16x32_bf16 v[74:77], v[152:155], v[218:221], v[74:77]
	v_mfma_f32_16x16x32_bf16 v[70:73], v[170:173], v[218:221], v[70:73]
	s_setprio 0
	s_setprio 1
	v_mfma_f32_16x16x32_bf16 v[126:129], v[174:177], v[190:193], 0
	v_mfma_f32_16x16x32_bf16 v[122:125], v[182:185], v[190:193], 0
	v_mfma_f32_16x16x32_bf16 v[110:113], v[174:177], v[198:201], 0
	v_mfma_f32_16x16x32_bf16 v[106:109], v[182:185], v[198:201], 0
	v_mfma_f32_16x16x32_bf16 v[94:97], v[174:177], v[206:209], 0
	v_mfma_f32_16x16x32_bf16 v[90:93], v[182:185], v[206:209], 0
	v_mfma_f32_16x16x32_bf16 v[78:81], v[174:177], v[214:217], 0
	v_mfma_f32_16x16x32_bf16 v[66:69], v[182:185], v[214:217], 0
	v_mfma_f32_16x16x32_bf16 v[126:129], v[178:181], v[194:197], v[126:129]
	v_mfma_f32_16x16x32_bf16 v[122:125], v[186:189], v[194:197], v[122:125]
	v_mfma_f32_16x16x32_bf16 v[110:113], v[178:181], v[202:205], v[110:113]
	v_mfma_f32_16x16x32_bf16 v[106:109], v[186:189], v[202:205], v[106:109]
	v_mfma_f32_16x16x32_bf16 v[94:97], v[178:181], v[210:213], v[94:97]
	v_mfma_f32_16x16x32_bf16 v[90:93], v[186:189], v[210:213], v[90:93]
	v_mfma_f32_16x16x32_bf16 v[78:81], v[178:181], v[218:221], v[78:81]
	v_mfma_f32_16x16x32_bf16 v[66:69], v[186:189], v[218:221], v[66:69]
	s_setprio 0
	s_barrier
	s_add_i32 s60, s44, s34
	v_lshl_add_u64 v[222:223], s[28:29], 0, v[134:135]
	s_mov_b32 m0, s60
	ds_read_b128 v[190:193], v162 offset:16384
	ds_read_b128 v[194:197], v162 offset:17408
	ds_read_b128 v[198:201], v162 offset:18432
	ds_read_b128 v[202:205], v162 offset:19456
	ds_read_b128 v[206:209], v162 offset:20480
	ds_read_b128 v[210:213], v162 offset:21504
	ds_read_b128 v[214:217], v162 offset:22528
	ds_read_b128 v[218:221], v162 offset:23552
	global_load_lds_dwordx4 v[222:223], off
	s_add_i32 m0, s60, 0x2000
	s_add_u32 s60, s28, 0x80000
	v_lshl_add_u64 v[224:225], s[28:29], 0, v[130:131]
	s_addc_u32 s61, s29, 0
	s_add_i32 s62, s45, s34
	global_load_lds_dwordx4 v[224:225], off
	v_lshl_add_u64 v[226:227], s[60:61], 0, v[134:135]
	s_mov_b32 m0, s62
	v_lshl_add_u64 v[228:229], s[30:31], 0, v[132:133]
	global_load_lds_dwordx4 v[226:227], off
	v_lshl_add_u64 v[226:227], s[60:61], 0, v[130:131]
	s_add_i32 m0, s62, 0x2000
	s_nop 0
	global_load_lds_dwordx4 v[226:227], off
	v_lshl_add_u64 v[226:227], s[30:31], 0, v[136:137]
	s_mov_b32 m0, s25
	s_nop 0
	global_load_lds_dwordx4 v[226:227], off
	s_mov_b32 m0, s37
	s_nop 0
	global_load_lds_dwordx4 v[228:229], off
	s_waitcnt vmcnt(8)
	s_waitcnt lgkmcnt(0)
	s_barrier
	s_setprio 1
	s_waitcnt lgkmcnt(0)
	v_mfma_f32_16x16x32_bf16 v[58:61], v[148:151], v[190:193], 0
	v_mfma_f32_16x16x32_bf16 v[54:57], v[166:169], v[190:193], 0
	v_mfma_f32_16x16x32_bf16 v[42:45], v[148:151], v[198:201], 0
	v_mfma_f32_16x16x32_bf16 v[38:41], v[166:169], v[198:201], 0
	v_mfma_f32_16x16x32_bf16 v[26:29], v[148:151], v[206:209], 0
	v_mfma_f32_16x16x32_bf16 v[22:25], v[166:169], v[206:209], 0
	v_mfma_f32_16x16x32_bf16 v[6:9], v[148:151], v[214:217], 0
	v_mfma_f32_16x16x32_bf16 v[2:5], v[166:169], v[214:217], 0
	v_mfma_f32_16x16x32_bf16 v[58:61], v[152:155], v[194:197], v[58:61]
	v_mfma_f32_16x16x32_bf16 v[54:57], v[170:173], v[194:197], v[54:57]
	v_mfma_f32_16x16x32_bf16 v[42:45], v[152:155], v[202:205], v[42:45]
	v_mfma_f32_16x16x32_bf16 v[38:41], v[170:173], v[202:205], v[38:41]
	v_mfma_f32_16x16x32_bf16 v[26:29], v[152:155], v[210:213], v[26:29]
	v_mfma_f32_16x16x32_bf16 v[22:25], v[170:173], v[210:213], v[22:25]
	v_mfma_f32_16x16x32_bf16 v[6:9], v[152:155], v[218:221], v[6:9]
	v_mfma_f32_16x16x32_bf16 v[2:5], v[170:173], v[218:221], v[2:5]
	s_setprio 0
	s_setprio 1
	v_mfma_f32_16x16x32_bf16 v[62:65], v[174:177], v[190:193], 0
	v_mfma_f32_16x16x32_bf16 v[50:53], v[182:185], v[190:193], 0
	v_mfma_f32_16x16x32_bf16 v[46:49], v[174:177], v[198:201], 0
	v_mfma_f32_16x16x32_bf16 v[34:37], v[182:185], v[198:201], 0
	v_mfma_f32_16x16x32_bf16 v[30:33], v[174:177], v[206:209], 0
	v_mfma_f32_16x16x32_bf16 v[18:21], v[182:185], v[206:209], 0
	v_mfma_f32_16x16x32_bf16 v[14:17], v[174:177], v[214:217], 0
	v_mfma_f32_16x16x32_bf16 v[10:13], v[182:185], v[214:217], 0
	v_mfma_f32_16x16x32_bf16 v[62:65], v[178:181], v[194:197], v[62:65]
	v_mfma_f32_16x16x32_bf16 v[50:53], v[186:189], v[194:197], v[50:53]
	v_mfma_f32_16x16x32_bf16 v[46:49], v[178:181], v[202:205], v[46:49]
	v_mfma_f32_16x16x32_bf16 v[34:37], v[186:189], v[202:205], v[34:37]
	v_mfma_f32_16x16x32_bf16 v[30:33], v[178:181], v[210:213], v[30:33]
	v_mfma_f32_16x16x32_bf16 v[18:21], v[186:189], v[210:213], v[18:21]
	v_mfma_f32_16x16x32_bf16 v[14:17], v[178:181], v[218:221], v[14:17]
	v_mfma_f32_16x16x32_bf16 v[10:13], v[186:189], v[218:221], v[10:13]
	s_setprio 0
	s_barrier
	s_add_i32 s60, 0, 0x18000
	v_add_u32_e32 v165, s60, v157
	s_add_i32 s61, 0, 0x1c000
	ds_read_b128 v[148:151], v165
	ds_read_b128 v[152:155], v165 offset:1024
	ds_read_b128 v[166:169], v165 offset:2048
	ds_read_b128 v[170:173], v165 offset:3072
	v_add_u32_e32 v165, s61, v157
	ds_read_b128 v[174:177], v165
	ds_read_b128 v[178:181], v165 offset:1024
	ds_read_b128 v[182:185], v165 offset:2048
	ds_read_b128 v[186:189], v165 offset:3072
	s_add_u32 s30, s30, 0x80000
	s_addc_u32 s31, s31, 0
	s_mov_b32 m0, s38
	v_lshl_add_u64 v[230:231], s[30:31], 0, v[136:137]
	ds_read_b128 v[190:193], v162 offset:32768
	ds_read_b128 v[194:197], v162 offset:33792
	ds_read_b128 v[198:201], v162 offset:34816
	ds_read_b128 v[202:205], v162 offset:35840
	ds_read_b128 v[206:209], v162 offset:36864
	ds_read_b128 v[210:213], v162 offset:37888
	ds_read_b128 v[214:217], v162 offset:38912
	ds_read_b128 v[218:221], v162 offset:39936
	global_load_lds_dwordx4 v[230:231], off
	v_lshl_add_u64 v[230:231], s[30:31], 0, v[132:133]
	s_mov_b32 m0, s39
	s_nop 0
	global_load_lds_dwordx4 v[230:231], off
	s_waitcnt vmcnt(8)
	s_waitcnt lgkmcnt(0)
	s_barrier
	s_setprio 1
	s_waitcnt lgkmcnt(0)
	v_mfma_f32_16x16x32_bf16 v[118:121], v[148:151], v[190:193], v[118:121]
	v_mfma_f32_16x16x32_bf16 v[114:117], v[166:169], v[190:193], v[114:117]
	v_mfma_f32_16x16x32_bf16 v[102:105], v[148:151], v[198:201], v[102:105]
	v_mfma_f32_16x16x32_bf16 v[98:101], v[166:169], v[198:201], v[98:101]
	v_mfma_f32_16x16x32_bf16 v[86:89], v[148:151], v[206:209], v[86:89]
	v_mfma_f32_16x16x32_bf16 v[82:85], v[166:169], v[206:209], v[82:85]
	v_mfma_f32_16x16x32_bf16 v[74:77], v[148:151], v[214:217], v[74:77]
	v_mfma_f32_16x16x32_bf16 v[70:73], v[166:169], v[214:217], v[70:73]
	v_mfma_f32_16x16x32_bf16 v[118:121], v[152:155], v[194:197], v[118:121]
	v_mfma_f32_16x16x32_bf16 v[114:117], v[170:173], v[194:197], v[114:117]
	v_mfma_f32_16x16x32_bf16 v[102:105], v[152:155], v[202:205], v[102:105]
	v_mfma_f32_16x16x32_bf16 v[98:101], v[170:173], v[202:205], v[98:101]
	v_mfma_f32_16x16x32_bf16 v[86:89], v[152:155], v[210:213], v[86:89]
	v_mfma_f32_16x16x32_bf16 v[82:85], v[170:173], v[210:213], v[82:85]
	v_mfma_f32_16x16x32_bf16 v[74:77], v[152:155], v[218:221], v[74:77]
	v_mfma_f32_16x16x32_bf16 v[70:73], v[170:173], v[218:221], v[70:73]
	s_setprio 0
	s_setprio 1
	v_mfma_f32_16x16x32_bf16 v[126:129], v[174:177], v[190:193], v[126:129]
	v_mfma_f32_16x16x32_bf16 v[122:125], v[182:185], v[190:193], v[122:125]
	v_mfma_f32_16x16x32_bf16 v[110:113], v[174:177], v[198:201], v[110:113]
	v_mfma_f32_16x16x32_bf16 v[106:109], v[182:185], v[198:201], v[106:109]
	v_mfma_f32_16x16x32_bf16 v[94:97], v[174:177], v[206:209], v[94:97]
	v_mfma_f32_16x16x32_bf16 v[90:93], v[182:185], v[206:209], v[90:93]
	v_mfma_f32_16x16x32_bf16 v[78:81], v[174:177], v[214:217], v[78:81]
	v_mfma_f32_16x16x32_bf16 v[66:69], v[182:185], v[214:217], v[66:69]
	v_mfma_f32_16x16x32_bf16 v[126:129], v[178:181], v[194:197], v[126:129]
	v_mfma_f32_16x16x32_bf16 v[122:125], v[186:189], v[194:197], v[122:125]
	v_mfma_f32_16x16x32_bf16 v[110:113], v[178:181], v[202:205], v[110:113]
	v_mfma_f32_16x16x32_bf16 v[106:109], v[186:189], v[202:205], v[106:109]
	v_mfma_f32_16x16x32_bf16 v[94:97], v[178:181], v[210:213], v[94:97]
	v_mfma_f32_16x16x32_bf16 v[90:93], v[186:189], v[210:213], v[90:93]
	v_mfma_f32_16x16x32_bf16 v[78:81], v[178:181], v[218:221], v[78:81]
	v_mfma_f32_16x16x32_bf16 v[66:69], v[186:189], v[218:221], v[66:69]
	s_setprio 0
	s_barrier
	s_add_i32 s30, s60, s34
	v_lshl_add_u64 v[222:223], v[222:223], 0, s[12:13]
	s_mov_b32 m0, s30
	ds_read_b128 v[190:193], v162 offset:49152
	ds_read_b128 v[194:197], v162 offset:50176
	ds_read_b128 v[198:201], v162 offset:51200
	ds_read_b128 v[202:205], v162 offset:52224
	ds_read_b128 v[206:209], v162 offset:53248
	ds_read_b128 v[210:213], v162 offset:54272
	ds_read_b128 v[214:217], v162 offset:55296
	ds_read_b128 v[218:221], v162 offset:56320
	global_load_lds_dwordx4 v[222:223], off
	s_add_i32 m0, s30, 0x2000
	s_add_u32 s28, s28, 0x80080
	v_lshl_add_u64 v[222:223], v[224:225], 0, s[12:13]
	s_addc_u32 s29, s29, 0
	s_add_i32 s30, s61, s34
	global_load_lds_dwordx4 v[222:223], off
	v_lshl_add_u64 v[222:223], s[28:29], 0, v[134:135]
	s_mov_b32 m0, s30
	s_nop 0
	global_load_lds_dwordx4 v[222:223], off
	v_lshl_add_u64 v[222:223], s[28:29], 0, v[130:131]
	s_add_i32 m0, s30, 0x2000
	s_nop 0
	global_load_lds_dwordx4 v[222:223], off
	v_lshl_add_u64 v[222:223], v[226:227], 0, s[12:13]
	s_mov_b32 m0, s41
	s_nop 0
	global_load_lds_dwordx4 v[222:223], off
	v_lshl_add_u64 v[222:223], v[228:229], 0, s[12:13]
	s_mov_b32 m0, s42
	s_nop 0
	global_load_lds_dwordx4 v[222:223], off
	s_waitcnt vmcnt(8)
	s_waitcnt lgkmcnt(0)
	s_barrier
	s_setprio 1
	s_waitcnt lgkmcnt(0)
	v_mfma_f32_16x16x32_bf16 v[58:61], v[148:151], v[190:193], v[58:61]
	v_mfma_f32_16x16x32_bf16 v[54:57], v[166:169], v[190:193], v[54:57]
	v_mfma_f32_16x16x32_bf16 v[42:45], v[148:151], v[198:201], v[42:45]
	v_mfma_f32_16x16x32_bf16 v[38:41], v[166:169], v[198:201], v[38:41]
	v_mfma_f32_16x16x32_bf16 v[26:29], v[148:151], v[206:209], v[26:29]
	v_mfma_f32_16x16x32_bf16 v[22:25], v[166:169], v[206:209], v[22:25]
	v_mfma_f32_16x16x32_bf16 v[6:9], v[148:151], v[214:217], v[6:9]
	v_mfma_f32_16x16x32_bf16 v[2:5], v[166:169], v[214:217], v[2:5]
	v_mfma_f32_16x16x32_bf16 v[58:61], v[152:155], v[194:197], v[58:61]
	v_mfma_f32_16x16x32_bf16 v[54:57], v[170:173], v[194:197], v[54:57]
	v_mfma_f32_16x16x32_bf16 v[42:45], v[152:155], v[202:205], v[42:45]
	v_mfma_f32_16x16x32_bf16 v[38:41], v[170:173], v[202:205], v[38:41]
	v_mfma_f32_16x16x32_bf16 v[26:29], v[152:155], v[210:213], v[26:29]
	v_mfma_f32_16x16x32_bf16 v[22:25], v[170:173], v[210:213], v[22:25]
	v_mfma_f32_16x16x32_bf16 v[6:9], v[152:155], v[218:221], v[6:9]
	v_mfma_f32_16x16x32_bf16 v[2:5], v[170:173], v[218:221], v[2:5]
	s_setprio 0
	s_setprio 1
	v_mfma_f32_16x16x32_bf16 v[62:65], v[174:177], v[190:193], v[62:65]
	v_mfma_f32_16x16x32_bf16 v[50:53], v[182:185], v[190:193], v[50:53]
	v_mfma_f32_16x16x32_bf16 v[46:49], v[174:177], v[198:201], v[46:49]
	v_mfma_f32_16x16x32_bf16 v[34:37], v[182:185], v[198:201], v[34:37]
	v_mfma_f32_16x16x32_bf16 v[30:33], v[174:177], v[206:209], v[30:33]
	v_mfma_f32_16x16x32_bf16 v[18:21], v[182:185], v[206:209], v[18:21]
	v_mfma_f32_16x16x32_bf16 v[14:17], v[174:177], v[214:217], v[14:17]
	v_mfma_f32_16x16x32_bf16 v[10:13], v[182:185], v[214:217], v[10:13]
	v_mfma_f32_16x16x32_bf16 v[62:65], v[178:181], v[194:197], v[62:65]
	v_mfma_f32_16x16x32_bf16 v[50:53], v[186:189], v[194:197], v[50:53]
	v_mfma_f32_16x16x32_bf16 v[46:49], v[178:181], v[202:205], v[46:49]
	v_mfma_f32_16x16x32_bf16 v[34:37], v[186:189], v[202:205], v[34:37]
	v_mfma_f32_16x16x32_bf16 v[30:33], v[178:181], v[210:213], v[30:33]
	v_mfma_f32_16x16x32_bf16 v[18:21], v[186:189], v[210:213], v[18:21]
	v_mfma_f32_16x16x32_bf16 v[14:17], v[178:181], v[218:221], v[14:17]
	v_mfma_f32_16x16x32_bf16 v[10:13], v[186:189], v[218:221], v[10:13]
	s_setprio 0
	s_barrier
	s_add_i32 s59, s59, 2
	s_add_u32 s26, s26, 0x100
	s_addc_u32 s27, s27, 0
	s_add_u32 s57, s57, 0x100
	s_addc_u32 s58, s58, 0
	s_cmp_gt_u32 s59, 29
	s_cbranch_scc1 .Lpeel_exit_471

.LBB0_555:
	s_add_u32 s20, s20, 0xb0080
	s_addc_u32 s21, s21, 0
	s_add_u32 s49, s22, 0x100
	v_mov_b32_e32 v2, 0
	s_addc_u32 s54, s23, 0
	s_mov_b32 s55, -2
	s_waitcnt lgkmcnt(0)
	ds_read_b128 v[162:165], v155
	ds_read_b128 v[166:169], v155 offset:1024
	ds_read_b128 v[170:173], v155 offset:2048
	ds_read_b128 v[174:177], v155 offset:3072
	ds_read_b128 v[178:181], v156
	ds_read_b128 v[182:185], v156 offset:1024
	ds_read_b128 v[224:227], v156 offset:2048
	ds_read_b128 v[228:231], v156 offset:3072
	s_add_u32 s22, s20, 0xfff50080
	s_addc_u32 s23, s21, -1
	s_cmp_eq_u32 s55, 40
	s_cselect_b32 s25, s1, s23
	s_cselect_b32 s24, s0, s22
	s_cselect_b32 s23, s19, s54
	s_cselect_b32 s22, s18, s49
	v_lshl_add_u64 v[148:149], s[20:21], 0, v[138:139]
	s_add_i32 m0, s30, 0xc000
	ds_read_b128 v[192:195], v157
	ds_read_b128 v[196:199], v157 offset:1024
	ds_read_b128 v[200:203], v157 offset:2048
	ds_read_b128 v[204:207], v157 offset:3072
	ds_read_b128 v[208:211], v157 offset:4096
	ds_read_b128 v[212:215], v157 offset:5120
	ds_read_b128 v[216:219], v157 offset:6144
	ds_read_b128 v[220:223], v157 offset:7168
	global_load_lds_dwordx4 v[148:149], off
	v_lshl_add_u64 v[148:149], s[20:21], 0, v[140:141]
	s_add_i32 m0, s30, 0xe000
	s_nop 0
	global_load_lds_dwordx4 v[148:149], off
	s_waitcnt vmcnt(8)
	s_waitcnt lgkmcnt(0)
	s_barrier
	s_setprio 1
	s_waitcnt lgkmcnt(0)
	s_nop 0
	v_mfma_scale_f32_16x16x128_f8f6f4 v[126:129], v[162:169], v[192:199], 0, v160, v159 op_sel_hi:[0,0,0]
	v_mfma_scale_f32_16x16x128_f8f6f4 v[122:125], v[170:177], v[192:199], 0, v160, v159 op_sel_hi:[0,0,0]
	v_mfma_scale_f32_16x16x128_f8f6f4 v[110:113], v[162:169], v[200:207], 0, v160, v159 op_sel_hi:[0,0,0]
	v_mfma_scale_f32_16x16x128_f8f6f4 v[106:109], v[170:177], v[200:207], 0, v160, v159 op_sel_hi:[0,0,0]
	v_mfma_scale_f32_16x16x128_f8f6f4 v[94:97], v[162:169], v[208:215], 0, v160, v159 op_sel_hi:[0,0,0]
	v_mfma_scale_f32_16x16x128_f8f6f4 v[90:93], v[170:177], v[208:215], 0, v160, v159 op_sel_hi:[0,0,0]
	v_mfma_scale_f32_16x16x128_f8f6f4 v[78:81], v[162:169], v[216:223], 0, v160, v159 op_sel_hi:[0,0,0]
	v_mfma_scale_f32_16x16x128_f8f6f4 v[74:77], v[170:177], v[216:223], 0, v160, v159 op_sel_hi:[0,0,0]
	s_setprio 0
	s_setprio 1
	s_nop 0
	v_mfma_scale_f32_16x16x128_f8f6f4 v[118:121], v[178:185], v[192:199], 0, v160, v159 op_sel_hi:[0,0,0]
	v_mfma_scale_f32_16x16x128_f8f6f4 v[114:117], v[224:231], v[192:199], 0, v160, v159 op_sel_hi:[0,0,0]
	v_mfma_scale_f32_16x16x128_f8f6f4 v[102:105], v[178:185], v[200:207], 0, v160, v159 op_sel_hi:[0,0,0]
	v_mfma_scale_f32_16x16x128_f8f6f4 v[98:101], v[224:231], v[200:207], 0, v160, v159 op_sel_hi:[0,0,0]
	v_mfma_scale_f32_16x16x128_f8f6f4 v[86:89], v[178:185], v[208:215], 0, v160, v159 op_sel_hi:[0,0,0]
	v_mfma_scale_f32_16x16x128_f8f6f4 v[82:85], v[224:231], v[208:215], 0, v160, v159 op_sel_hi:[0,0,0]
	v_mfma_scale_f32_16x16x128_f8f6f4 v[70:73], v[178:185], v[216:223], 0, v160, v159 op_sel_hi:[0,0,0]
	v_mfma_scale_f32_16x16x128_f8f6f4 v[66:69], v[224:231], v[216:223], 0, v160, v159 op_sel_hi:[0,0,0]
	s_setprio 0
	s_barrier
	s_add_i32 s56, s40, s29
	v_lshl_add_u64 v[190:191], s[22:23], 0, v[132:133]
	s_mov_b32 m0, s56
	ds_read_b128 v[192:195], v157 offset:16384
	ds_read_b128 v[196:199], v157 offset:17408
	ds_read_b128 v[200:203], v157 offset:18432
	ds_read_b128 v[204:207], v157 offset:19456
	ds_read_b128 v[208:211], v157 offset:20480
	ds_read_b128 v[212:215], v157 offset:21504
	ds_read_b128 v[216:219], v157 offset:22528
	ds_read_b128 v[220:223], v157 offset:23552
	global_load_lds_dwordx4 v[190:191], off
	s_add_i32 m0, s56, 0x2000
	s_add_u32 s56, s22, 0xb0000
	v_lshl_add_u64 v[232:233], s[22:23], 0, v[136:137]
	s_addc_u32 s57, s23, 0
	s_add_i32 s58, s41, s29
	global_load_lds_dwordx4 v[232:233], off
	v_lshl_add_u64 v[148:149], s[56:57], 0, v[132:133]
	s_mov_b32 m0, s58
	v_lshl_add_u64 v[234:235], s[24:25], 0, v[130:131]
	global_load_lds_dwordx4 v[148:149], off
	v_lshl_add_u64 v[148:149], s[56:57], 0, v[136:137]
	s_add_i32 m0, s58, 0x2000
	v_lshl_add_u64 v[236:237], s[24:25], 0, v[134:135]
	global_load_lds_dwordx4 v[148:149], off
	s_mov_b32 m0, s30
	s_nop 0
	global_load_lds_dwordx4 v[234:235], off
	s_mov_b32 m0, s31
	s_nop 0
	global_load_lds_dwordx4 v[236:237], off
	s_waitcnt vmcnt(8)
	s_waitcnt lgkmcnt(0)
	s_barrier
	s_setprio 1
	s_waitcnt lgkmcnt(0)
	s_nop 0
	v_mfma_scale_f32_16x16x128_f8f6f4 v[62:65], v[162:169], v[192:199], 0, v160, v159 op_sel_hi:[0,0,0]
	v_mfma_scale_f32_16x16x128_f8f6f4 v[58:61], v[170:177], v[192:199], 0, v160, v159 op_sel_hi:[0,0,0]
	v_mfma_scale_f32_16x16x128_f8f6f4 v[46:49], v[162:169], v[200:207], 0, v160, v159 op_sel_hi:[0,0,0]
	v_mfma_scale_f32_16x16x128_f8f6f4 v[42:45], v[170:177], v[200:207], 0, v160, v159 op_sel_hi:[0,0,0]
	v_mfma_scale_f32_16x16x128_f8f6f4 v[30:33], v[162:169], v[208:215], 0, v160, v159 op_sel_hi:[0,0,0]
	v_mfma_scale_f32_16x16x128_f8f6f4 v[26:29], v[170:177], v[208:215], 0, v160, v159 op_sel_hi:[0,0,0]
	v_mfma_scale_f32_16x16x128_f8f6f4 v[14:17], v[162:169], v[216:223], 0, v160, v159 op_sel_hi:[0,0,0]
	v_mfma_scale_f32_16x16x128_f8f6f4 v[10:13], v[170:177], v[216:223], 0, v160, v159 op_sel_hi:[0,0,0]
	s_setprio 0
	s_setprio 1
	s_nop 0
	v_mfma_scale_f32_16x16x128_f8f6f4 v[54:57], v[178:185], v[192:199], 0, v160, v159 op_sel_hi:[0,0,0]
	v_mfma_scale_f32_16x16x128_f8f6f4 v[50:53], v[224:231], v[192:199], 0, v160, v159 op_sel_hi:[0,0,0]
	v_mfma_scale_f32_16x16x128_f8f6f4 v[38:41], v[178:185], v[200:207], 0, v160, v159 op_sel_hi:[0,0,0]
	v_mfma_scale_f32_16x16x128_f8f6f4 v[34:37], v[224:231], v[200:207], 0, v160, v159 op_sel_hi:[0,0,0]
	v_mfma_scale_f32_16x16x128_f8f6f4 v[148:151], v[178:185], v[208:215], 0, v160, v159 op_sel_hi:[0,0,0]
	v_mfma_scale_f32_16x16x128_f8f6f4 v[186:189], v[224:231], v[208:215], 0, v160, v159 op_sel_hi:[0,0,0]
	v_mfma_scale_f32_16x16x128_f8f6f4 v[178:181], v[178:185], v[216:223], 0, v160, v159 op_sel_hi:[0,0,0]
	v_mfma_scale_f32_16x16x128_f8f6f4 v[182:185], v[224:231], v[216:223], 0, v160, v159 op_sel_hi:[0,0,0]
	s_setprio 0
	s_barrier
	s_add_i32 s56, 0, 0x18000
	s_add_i32 s57, 0, 0x1c000
	v_add_u32_e32 v22, s56, v153
	v_add_u32_e32 v174, s57, v153
	s_nop 0
	ds_read_b128 v[2:5], v22
	ds_read_b128 v[6:9], v22 offset:1024
	ds_read_b128 v[18:21], v22 offset:2048
	ds_read_b128 v[22:25], v22 offset:3072
	ds_read_b128 v[162:165], v174
	ds_read_b128 v[166:169], v174 offset:1024
	ds_read_b128 v[170:173], v174 offset:2048
	ds_read_b128 v[174:177], v174 offset:3072
	s_add_u32 s24, s24, 0xb0000
	s_addc_u32 s25, s25, 0
	s_mov_b32 m0, s33
	v_lshl_add_u64 v[224:225], s[24:25], 0, v[130:131]
	ds_read_b128 v[192:195], v157 offset:32768
	ds_read_b128 v[196:199], v157 offset:33792
	ds_read_b128 v[200:203], v157 offset:34816
	ds_read_b128 v[204:207], v157 offset:35840
	ds_read_b128 v[208:211], v157 offset:36864
	ds_read_b128 v[212:215], v157 offset:37888
	ds_read_b128 v[216:219], v157 offset:38912
	ds_read_b128 v[220:223], v157 offset:39936
	global_load_lds_dwordx4 v[224:225], off
	v_lshl_add_u64 v[224:225], s[24:25], 0, v[134:135]
	s_mov_b32 m0, s34
	s_nop 0
	global_load_lds_dwordx4 v[224:225], off
	s_waitcnt vmcnt(8)
	s_waitcnt lgkmcnt(0)
	s_barrier
	s_setprio 1
	s_waitcnt lgkmcnt(0)
	s_nop 0
	v_mfma_scale_f32_16x16x128_f8f6f4 v[126:129], v[2:9], v[192:199], v[126:129], v160, v159 op_sel_hi:[0,0,0]
	v_mfma_scale_f32_16x16x128_f8f6f4 v[122:125], v[18:25], v[192:199], v[122:125], v160, v159 op_sel_hi:[0,0,0]
	v_mfma_scale_f32_16x16x128_f8f6f4 v[110:113], v[2:9], v[200:207], v[110:113], v160, v159 op_sel_hi:[0,0,0]
	v_mfma_scale_f32_16x16x128_f8f6f4 v[106:109], v[18:25], v[200:207], v[106:109], v160, v159 op_sel_hi:[0,0,0]
	v_mfma_scale_f32_16x16x128_f8f6f4 v[94:97], v[2:9], v[208:215], v[94:97], v160, v159 op_sel_hi:[0,0,0]
	v_mfma_scale_f32_16x16x128_f8f6f4 v[90:93], v[18:25], v[208:215], v[90:93], v160, v159 op_sel_hi:[0,0,0]
	v_mfma_scale_f32_16x16x128_f8f6f4 v[78:81], v[2:9], v[216:223], v[78:81], v160, v159 op_sel_hi:[0,0,0]
	v_mfma_scale_f32_16x16x128_f8f6f4 v[74:77], v[18:25], v[216:223], v[74:77], v160, v159 op_sel_hi:[0,0,0]
	s_setprio 0
	s_setprio 1
	s_nop 0
	v_mfma_scale_f32_16x16x128_f8f6f4 v[118:121], v[162:169], v[192:199], v[118:121], v160, v159 op_sel_hi:[0,0,0]
	v_mfma_scale_f32_16x16x128_f8f6f4 v[114:117], v[170:177], v[192:199], v[114:117], v160, v159 op_sel_hi:[0,0,0]
	v_mfma_scale_f32_16x16x128_f8f6f4 v[102:105], v[162:169], v[200:207], v[102:105], v160, v159 op_sel_hi:[0,0,0]
	v_mfma_scale_f32_16x16x128_f8f6f4 v[98:101], v[170:177], v[200:207], v[98:101], v160, v159 op_sel_hi:[0,0,0]
	v_mfma_scale_f32_16x16x128_f8f6f4 v[86:89], v[162:169], v[208:215], v[86:89], v160, v159 op_sel_hi:[0,0,0]
	v_mfma_scale_f32_16x16x128_f8f6f4 v[82:85], v[170:177], v[208:215], v[82:85], v160, v159 op_sel_hi:[0,0,0]
	v_mfma_scale_f32_16x16x128_f8f6f4 v[70:73], v[162:169], v[216:223], v[70:73], v160, v159 op_sel_hi:[0,0,0]
	v_mfma_scale_f32_16x16x128_f8f6f4 v[66:69], v[170:177], v[216:223], v[66:69], v160, v159 op_sel_hi:[0,0,0]
	s_setprio 0
	s_barrier
	s_add_i32 s24, s56, s29
	v_lshl_add_u64 v[190:191], v[190:191], 0, s[14:15]
	s_mov_b32 m0, s24
	ds_read_b128 v[192:195], v157 offset:49152
	ds_read_b128 v[196:199], v157 offset:50176
	ds_read_b128 v[200:203], v157 offset:51200
	ds_read_b128 v[204:207], v157 offset:52224
	ds_read_b128 v[208:211], v157 offset:53248
	ds_read_b128 v[212:215], v157 offset:54272
	ds_read_b128 v[216:219], v157 offset:55296
	ds_read_b128 v[220:223], v157 offset:56320
	global_load_lds_dwordx4 v[190:191], off
	s_add_i32 m0, s24, 0x2000
	s_add_u32 s22, s22, 0xb0080
	v_lshl_add_u64 v[190:191], v[232:233], 0, s[14:15]
	s_addc_u32 s23, s23, 0
	s_add_i32 s24, s57, s29
	global_load_lds_dwordx4 v[190:191], off
	v_lshl_add_u64 v[190:191], s[22:23], 0, v[132:133]
	s_mov_b32 m0, s24
	s_nop 0
	global_load_lds_dwordx4 v[190:191], off
	v_lshl_add_u64 v[190:191], s[22:23], 0, v[136:137]
	s_add_i32 m0, s24, 0x2000
	s_nop 0
	global_load_lds_dwordx4 v[190:191], off
	v_lshl_add_u64 v[190:191], v[234:235], 0, s[14:15]
	s_mov_b32 m0, s36
	s_nop 0
	global_load_lds_dwordx4 v[190:191], off
	v_lshl_add_u64 v[190:191], v[236:237], 0, s[14:15]
	s_mov_b32 m0, s37
	s_nop 0
	global_load_lds_dwordx4 v[190:191], off
	s_waitcnt vmcnt(8)
	s_waitcnt lgkmcnt(0)
	s_barrier
	s_setprio 1
	s_waitcnt lgkmcnt(0)
	s_nop 0
	v_mfma_scale_f32_16x16x128_f8f6f4 v[62:65], v[2:9], v[192:199], v[62:65], v160, v159 op_sel_hi:[0,0,0]
	v_mfma_scale_f32_16x16x128_f8f6f4 v[58:61], v[18:25], v[192:199], v[58:61], v160, v159 op_sel_hi:[0,0,0]
	v_mfma_scale_f32_16x16x128_f8f6f4 v[46:49], v[2:9], v[200:207], v[46:49], v160, v159 op_sel_hi:[0,0,0]
	v_mfma_scale_f32_16x16x128_f8f6f4 v[42:45], v[18:25], v[200:207], v[42:45], v160, v159 op_sel_hi:[0,0,0]
	v_mfma_scale_f32_16x16x128_f8f6f4 v[30:33], v[2:9], v[208:215], v[30:33], v160, v159 op_sel_hi:[0,0,0]
	v_mfma_scale_f32_16x16x128_f8f6f4 v[26:29], v[18:25], v[208:215], v[26:29], v160, v159 op_sel_hi:[0,0,0]
	v_mfma_scale_f32_16x16x128_f8f6f4 v[14:17], v[2:9], v[216:223], v[14:17], v160, v159 op_sel_hi:[0,0,0]
	v_mfma_scale_f32_16x16x128_f8f6f4 v[10:13], v[18:25], v[216:223], v[10:13], v160, v159 op_sel_hi:[0,0,0]
	s_setprio 0
	s_setprio 1
	s_nop 0
	v_mfma_scale_f32_16x16x128_f8f6f4 v[54:57], v[162:169], v[192:199], v[54:57], v160, v159 op_sel_hi:[0,0,0]
	v_mfma_scale_f32_16x16x128_f8f6f4 v[50:53], v[170:177], v[192:199], v[50:53], v160, v159 op_sel_hi:[0,0,0]
	v_mfma_scale_f32_16x16x128_f8f6f4 v[38:41], v[162:169], v[200:207], v[38:41], v160, v159 op_sel_hi:[0,0,0]
	v_mfma_scale_f32_16x16x128_f8f6f4 v[34:37], v[170:177], v[200:207], v[34:37], v160, v159 op_sel_hi:[0,0,0]
	v_mfma_scale_f32_16x16x128_f8f6f4 v[22:25], v[162:169], v[208:215], v[148:151], v160, v159 op_sel_hi:[0,0,0]
	v_mfma_scale_f32_16x16x128_f8f6f4 v[18:21], v[170:177], v[208:215], v[186:189], v160, v159 op_sel_hi:[0,0,0]
	v_mfma_scale_f32_16x16x128_f8f6f4 v[6:9], v[162:169], v[216:223], v[178:181], v160, v159 op_sel_hi:[0,0,0]
	v_mfma_scale_f32_16x16x128_f8f6f4 v[2:5], v[170:177], v[216:223], v[182:185], v160, v159 op_sel_hi:[0,0,0]
	s_setprio 0
	s_barrier
	s_add_i32 s55, s55, 2
	s_add_u32 s20, s20, 0x100
	s_addc_u32 s21, s21, 0
	s_add_u32 s49, s49, 0x100
	s_addc_u32 s54, s54, 0
	s_cmp_gt_u32 s55, 41
	s_cbranch_scc1 .Lpeel_exit_556

.Lpeel_exit_556:
	s_and_b64 vcc, exec, s[16:17]
	s_cbranch_vccz .LBB0_559
	s_barrier

.LBB0_650:
	s_ashr_i32 s27, s26, 31
	s_lshl_b64 s[28:29], s[26:27], 20
	s_add_u32 s28, s50, s28
	s_addc_u32 s29, s51, s29
	s_and_b64 s[30:31], s[4:5], exec
	s_cselect_b32 s27, s29, s35
	s_cselect_b32 s62, s28, s34
	s_ashr_i32 s25, s24, 31
	s_lshl_b64 s[30:31], s[24:25], 20
	s_add_u32 s30, s33, s30
	s_addc_u32 s31, s40, s31
	s_and_b64 s[38:39], s[4:5], exec
	s_cselect_b32 s25, s31, s37
	s_cselect_b32 s63, s30, s36
	s_add_u32 s34, s34, 0x80080
	s_addc_u32 s35, s35, 0
	s_add_u32 s64, s36, 0x100
	v_mov_b32_e32 v2, 0
	s_addc_u32 s65, s37, 0
	s_mov_b32 s66, -2
	ds_read_b128 v[148:151], v157
	ds_read_b128 v[162:165], v157 offset:1024
	ds_read_b128 v[166:169], v157 offset:2048
	ds_read_b128 v[170:173], v157 offset:3072
	ds_read_b128 v[174:177], v159
	ds_read_b128 v[178:181], v159 offset:1024
	ds_read_b128 v[182:185], v159 offset:2048
	ds_read_b128 v[186:189], v159 offset:3072
	s_add_u32 s36, s34, 0xfff80080
	s_addc_u32 s37, s35, -1
	s_cmp_eq_u32 s66, 28
	s_cselect_b32 s39, s27, s37
	s_cselect_b32 s38, s62, s36
	s_cselect_b32 s37, s25, s65
	s_cselect_b32 s36, s63, s64
	v_lshl_add_u64 v[152:153], s[34:35], 0, v[138:139]
	s_add_i32 m0, s42, 0xc000
	ds_read_b128 v[190:193], v160
	ds_read_b128 v[194:197], v160 offset:1024
	ds_read_b128 v[198:201], v160 offset:2048
	ds_read_b128 v[202:205], v160 offset:3072
	ds_read_b128 v[206:209], v160 offset:4096
	ds_read_b128 v[210:213], v160 offset:5120
	ds_read_b128 v[214:217], v160 offset:6144
	ds_read_b128 v[218:221], v160 offset:7168
	global_load_lds_dwordx4 v[152:153], off
	v_lshl_add_u64 v[152:153], s[34:35], 0, v[140:141]
	s_add_i32 m0, s42, 0xe000
	s_nop 0
	global_load_lds_dwordx4 v[152:153], off
	s_waitcnt vmcnt(8)
	s_waitcnt lgkmcnt(0)
	s_barrier
	s_setprio 1
	s_waitcnt lgkmcnt(0)
	v_mfma_f32_16x16x32_bf16 v[126:129], v[148:151], v[190:193], 0
	v_mfma_f32_16x16x32_bf16 v[122:125], v[166:169], v[190:193], 0
	v_mfma_f32_16x16x32_bf16 v[110:113], v[148:151], v[198:201], 0
	v_mfma_f32_16x16x32_bf16 v[106:109], v[166:169], v[198:201], 0
	v_mfma_f32_16x16x32_bf16 v[94:97], v[148:151], v[206:209], 0
	v_mfma_f32_16x16x32_bf16 v[90:93], v[166:169], v[206:209], 0
	v_mfma_f32_16x16x32_bf16 v[78:81], v[148:151], v[214:217], 0
	v_mfma_f32_16x16x32_bf16 v[74:77], v[166:169], v[214:217], 0
	v_mfma_f32_16x16x32_bf16 v[126:129], v[162:165], v[194:197], v[126:129]
	v_mfma_f32_16x16x32_bf16 v[122:125], v[170:173], v[194:197], v[122:125]
	v_mfma_f32_16x16x32_bf16 v[110:113], v[162:165], v[202:205], v[110:113]
	v_mfma_f32_16x16x32_bf16 v[106:109], v[170:173], v[202:205], v[106:109]
	v_mfma_f32_16x16x32_bf16 v[94:97], v[162:165], v[210:213], v[94:97]
	v_mfma_f32_16x16x32_bf16 v[90:93], v[170:173], v[210:213], v[90:93]
	v_mfma_f32_16x16x32_bf16 v[78:81], v[162:165], v[218:221], v[78:81]
	v_mfma_f32_16x16x32_bf16 v[74:77], v[170:173], v[218:221], v[74:77]
	s_setprio 0
	s_setprio 1
	v_mfma_f32_16x16x32_bf16 v[118:121], v[174:177], v[190:193], 0
	v_mfma_f32_16x16x32_bf16 v[114:117], v[182:185], v[190:193], 0
	v_mfma_f32_16x16x32_bf16 v[102:105], v[174:177], v[198:201], 0
	v_mfma_f32_16x16x32_bf16 v[98:101], v[182:185], v[198:201], 0
	v_mfma_f32_16x16x32_bf16 v[86:89], v[174:177], v[206:209], 0
	v_mfma_f32_16x16x32_bf16 v[82:85], v[182:185], v[206:209], 0
	v_mfma_f32_16x16x32_bf16 v[70:73], v[174:177], v[214:217], 0
	v_mfma_f32_16x16x32_bf16 v[66:69], v[182:185], v[214:217], 0
	v_mfma_f32_16x16x32_bf16 v[118:121], v[178:181], v[194:197], v[118:121]
	v_mfma_f32_16x16x32_bf16 v[114:117], v[186:189], v[194:197], v[114:117]
	v_mfma_f32_16x16x32_bf16 v[102:105], v[178:181], v[202:205], v[102:105]
	v_mfma_f32_16x16x32_bf16 v[98:101], v[186:189], v[202:205], v[98:101]
	v_mfma_f32_16x16x32_bf16 v[86:89], v[178:181], v[210:213], v[86:89]
	v_mfma_f32_16x16x32_bf16 v[82:85], v[186:189], v[210:213], v[82:85]
	v_mfma_f32_16x16x32_bf16 v[70:73], v[178:181], v[218:221], v[70:73]
	v_mfma_f32_16x16x32_bf16 v[66:69], v[186:189], v[218:221], v[66:69]
	s_setprio 0
	s_barrier
	s_add_i32 s67, s56, s41
	v_lshl_add_u64 v[152:153], s[36:37], 0, v[132:133]
	s_mov_b32 m0, s67
	ds_read_b128 v[190:193], v160 offset:16384
	ds_read_b128 v[194:197], v160 offset:17408
	ds_read_b128 v[198:201], v160 offset:18432
	ds_read_b128 v[202:205], v160 offset:19456
	ds_read_b128 v[206:209], v160 offset:20480
	ds_read_b128 v[210:213], v160 offset:21504
	ds_read_b128 v[214:217], v160 offset:22528
	ds_read_b128 v[218:221], v160 offset:23552
	global_load_lds_dwordx4 v[152:153], off
	s_add_i32 m0, s67, 0x2000
	s_add_u32 s68, s36, 0x80000
	v_lshl_add_u64 v[222:223], s[36:37], 0, v[136:137]
	s_addc_u32 s69, s37, 0
	s_add_i32 s67, s57, s41
	global_load_lds_dwordx4 v[222:223], off
	v_lshl_add_u64 v[224:225], s[68:69], 0, v[132:133]
	s_mov_b32 m0, s67
	v_lshl_add_u64 v[226:227], s[38:39], 0, v[134:135]
	global_load_lds_dwordx4 v[224:225], off
	v_lshl_add_u64 v[224:225], s[68:69], 0, v[136:137]
	s_add_i32 m0, s67, 0x2000
	s_nop 0
	global_load_lds_dwordx4 v[224:225], off
	v_lshl_add_u64 v[224:225], s[38:39], 0, v[130:131]
	s_mov_b32 m0, s42
	s_nop 0
	global_load_lds_dwordx4 v[224:225], off
	s_mov_b32 m0, s43
	s_nop 0
	global_load_lds_dwordx4 v[226:227], off
	s_waitcnt vmcnt(8)
	s_waitcnt lgkmcnt(0)
	s_barrier
	s_setprio 1
	s_waitcnt lgkmcnt(0)
	v_mfma_f32_16x16x32_bf16 v[62:65], v[148:151], v[190:193], 0
	v_mfma_f32_16x16x32_bf16 v[58:61], v[166:169], v[190:193], 0
	v_mfma_f32_16x16x32_bf16 v[46:49], v[148:151], v[198:201], 0
	v_mfma_f32_16x16x32_bf16 v[42:45], v[166:169], v[198:201], 0
	v_mfma_f32_16x16x32_bf16 v[30:33], v[148:151], v[206:209], 0
	v_mfma_f32_16x16x32_bf16 v[26:29], v[166:169], v[206:209], 0
	v_mfma_f32_16x16x32_bf16 v[14:17], v[148:151], v[214:217], 0
	v_mfma_f32_16x16x32_bf16 v[10:13], v[166:169], v[214:217], 0
	v_mfma_f32_16x16x32_bf16 v[62:65], v[162:165], v[194:197], v[62:65]
	v_mfma_f32_16x16x32_bf16 v[58:61], v[170:173], v[194:197], v[58:61]
	v_mfma_f32_16x16x32_bf16 v[46:49], v[162:165], v[202:205], v[46:49]
	v_mfma_f32_16x16x32_bf16 v[42:45], v[170:173], v[202:205], v[42:45]
	v_mfma_f32_16x16x32_bf16 v[30:33], v[162:165], v[210:213], v[30:33]
	v_mfma_f32_16x16x32_bf16 v[26:29], v[170:173], v[210:213], v[26:29]
	v_mfma_f32_16x16x32_bf16 v[14:17], v[162:165], v[218:221], v[14:17]
	v_mfma_f32_16x16x32_bf16 v[10:13], v[170:173], v[218:221], v[10:13]
	s_setprio 0
	s_setprio 1
	v_mfma_f32_16x16x32_bf16 v[54:57], v[174:177], v[190:193], 0
	v_mfma_f32_16x16x32_bf16 v[50:53], v[182:185], v[190:193], 0
	v_mfma_f32_16x16x32_bf16 v[38:41], v[174:177], v[198:201], 0
	v_mfma_f32_16x16x32_bf16 v[34:37], v[182:185], v[198:201], 0
	v_mfma_f32_16x16x32_bf16 v[22:25], v[174:177], v[206:209], 0
	v_mfma_f32_16x16x32_bf16 v[18:21], v[182:185], v[206:209], 0
	v_mfma_f32_16x16x32_bf16 v[6:9], v[174:177], v[214:217], 0
	v_mfma_f32_16x16x32_bf16 v[2:5], v[182:185], v[214:217], 0
	v_mfma_f32_16x16x32_bf16 v[54:57], v[178:181], v[194:197], v[54:57]
	v_mfma_f32_16x16x32_bf16 v[50:53], v[186:189], v[194:197], v[50:53]
	v_mfma_f32_16x16x32_bf16 v[38:41], v[178:181], v[202:205], v[38:41]
	v_mfma_f32_16x16x32_bf16 v[34:37], v[186:189], v[202:205], v[34:37]
	v_mfma_f32_16x16x32_bf16 v[22:25], v[178:181], v[210:213], v[22:25]
	v_mfma_f32_16x16x32_bf16 v[18:21], v[186:189], v[210:213], v[18:21]
	v_mfma_f32_16x16x32_bf16 v[6:9], v[178:181], v[218:221], v[6:9]
	v_mfma_f32_16x16x32_bf16 v[2:5], v[186:189], v[218:221], v[2:5]
	s_setprio 0
	s_barrier
	s_add_i32 s67, 0, 0x18000
	s_add_i32 s68, 0, 0x1c000
	v_add_u32_e32 v170, s67, v155
	v_add_u32_e32 v186, s68, v155
	ds_read_b128 v[148:151], v170
	ds_read_b128 v[162:165], v170 offset:1024
	ds_read_b128 v[166:169], v170 offset:2048
	ds_read_b128 v[170:173], v170 offset:3072
	ds_read_b128 v[174:177], v186
	ds_read_b128 v[178:181], v186 offset:1024
	ds_read_b128 v[182:185], v186 offset:2048
	ds_read_b128 v[186:189], v186 offset:3072
	s_add_u32 s38, s38, 0x80000
	s_addc_u32 s39, s39, 0
	s_mov_b32 m0, s44
	v_lshl_add_u64 v[228:229], s[38:39], 0, v[130:131]
	ds_read_b128 v[190:193], v160 offset:32768
	ds_read_b128 v[194:197], v160 offset:33792
	ds_read_b128 v[198:201], v160 offset:34816
	ds_read_b128 v[202:205], v160 offset:35840
	ds_read_b128 v[206:209], v160 offset:36864
	ds_read_b128 v[210:213], v160 offset:37888
	ds_read_b128 v[214:217], v160 offset:38912
	ds_read_b128 v[218:221], v160 offset:39936
	global_load_lds_dwordx4 v[228:229], off
	v_lshl_add_u64 v[228:229], s[38:39], 0, v[134:135]
	s_mov_b32 m0, s45
	s_nop 0
	global_load_lds_dwordx4 v[228:229], off
	s_waitcnt vmcnt(8)
	s_waitcnt lgkmcnt(0)
	s_barrier
	s_setprio 1
	s_waitcnt lgkmcnt(0)
	v_mfma_f32_16x16x32_bf16 v[126:129], v[148:151], v[190:193], v[126:129]
	v_mfma_f32_16x16x32_bf16 v[122:125], v[166:169], v[190:193], v[122:125]
	v_mfma_f32_16x16x32_bf16 v[110:113], v[148:151], v[198:201], v[110:113]
	v_mfma_f32_16x16x32_bf16 v[106:109], v[166:169], v[198:201], v[106:109]
	v_mfma_f32_16x16x32_bf16 v[94:97], v[148:151], v[206:209], v[94:97]
	v_mfma_f32_16x16x32_bf16 v[90:93], v[166:169], v[206:209], v[90:93]
	v_mfma_f32_16x16x32_bf16 v[78:81], v[148:151], v[214:217], v[78:81]
	v_mfma_f32_16x16x32_bf16 v[74:77], v[166:169], v[214:217], v[74:77]
	v_mfma_f32_16x16x32_bf16 v[126:129], v[162:165], v[194:197], v[126:129]
	v_mfma_f32_16x16x32_bf16 v[122:125], v[170:173], v[194:197], v[122:125]
	v_mfma_f32_16x16x32_bf16 v[110:113], v[162:165], v[202:205], v[110:113]
	v_mfma_f32_16x16x32_bf16 v[106:109], v[170:173], v[202:205], v[106:109]
	v_mfma_f32_16x16x32_bf16 v[94:97], v[162:165], v[210:213], v[94:97]
	v_mfma_f32_16x16x32_bf16 v[90:93], v[170:173], v[210:213], v[90:93]
	v_mfma_f32_16x16x32_bf16 v[78:81], v[162:165], v[218:221], v[78:81]
	v_mfma_f32_16x16x32_bf16 v[74:77], v[170:173], v[218:221], v[74:77]
	s_setprio 0
	s_setprio 1
	v_mfma_f32_16x16x32_bf16 v[118:121], v[174:177], v[190:193], v[118:121]
	v_mfma_f32_16x16x32_bf16 v[114:117], v[182:185], v[190:193], v[114:117]
	v_mfma_f32_16x16x32_bf16 v[102:105], v[174:177], v[198:201], v[102:105]
	v_mfma_f32_16x16x32_bf16 v[98:101], v[182:185], v[198:201], v[98:101]
	v_mfma_f32_16x16x32_bf16 v[86:89], v[174:177], v[206:209], v[86:89]
	v_mfma_f32_16x16x32_bf16 v[82:85], v[182:185], v[206:209], v[82:85]
	v_mfma_f32_16x16x32_bf16 v[70:73], v[174:177], v[214:217], v[70:73]
	v_mfma_f32_16x16x32_bf16 v[66:69], v[182:185], v[214:217], v[66:69]
	v_mfma_f32_16x16x32_bf16 v[118:121], v[178:181], v[194:197], v[118:121]
	v_mfma_f32_16x16x32_bf16 v[114:117], v[186:189], v[194:197], v[114:117]
	v_mfma_f32_16x16x32_bf16 v[102:105], v[178:181], v[202:205], v[102:105]
	v_mfma_f32_16x16x32_bf16 v[98:101], v[186:189], v[202:205], v[98:101]
	v_mfma_f32_16x16x32_bf16 v[86:89], v[178:181], v[210:213], v[86:89]
	v_mfma_f32_16x16x32_bf16 v[82:85], v[186:189], v[210:213], v[82:85]
	v_mfma_f32_16x16x32_bf16 v[70:73], v[178:181], v[218:221], v[70:73]
	v_mfma_f32_16x16x32_bf16 v[66:69], v[186:189], v[218:221], v[66:69]
	s_setprio 0
	s_barrier
	s_add_i32 s38, s67, s41
	v_lshl_add_u64 v[152:153], v[152:153], 0, s[14:15]
	s_mov_b32 m0, s38
	ds_read_b128 v[190:193], v160 offset:49152
	ds_read_b128 v[194:197], v160 offset:50176
	ds_read_b128 v[198:201], v160 offset:51200
	ds_read_b128 v[202:205], v160 offset:52224
	ds_read_b128 v[206:209], v160 offset:53248
	ds_read_b128 v[210:213], v160 offset:54272
	ds_read_b128 v[214:217], v160 offset:55296
	ds_read_b128 v[218:221], v160 offset:56320
	global_load_lds_dwordx4 v[152:153], off
	s_add_i32 m0, s38, 0x2000
	s_add_u32 s36, s36, 0x80080
	v_lshl_add_u64 v[152:153], v[222:223], 0, s[14:15]
	s_addc_u32 s37, s37, 0
	s_add_i32 s38, s68, s41
	global_load_lds_dwordx4 v[152:153], off
	v_lshl_add_u64 v[152:153], s[36:37], 0, v[132:133]
	s_mov_b32 m0, s38
	s_nop 0
	global_load_lds_dwordx4 v[152:153], off
	v_lshl_add_u64 v[152:153], s[36:37], 0, v[136:137]
	s_add_i32 m0, s38, 0x2000
	s_nop 0
	global_load_lds_dwordx4 v[152:153], off
	v_lshl_add_u64 v[152:153], v[224:225], 0, s[14:15]
	s_mov_b32 m0, s49
	s_nop 0
	global_load_lds_dwordx4 v[152:153], off
	v_lshl_add_u64 v[152:153], v[226:227], 0, s[14:15]
	s_mov_b32 m0, s54
	s_nop 0
	global_load_lds_dwordx4 v[152:153], off
	s_waitcnt vmcnt(8)
	s_waitcnt lgkmcnt(0)
	s_barrier
	s_setprio 1
	s_waitcnt lgkmcnt(0)
	v_mfma_f32_16x16x32_bf16 v[62:65], v[148:151], v[190:193], v[62:65]
	v_mfma_f32_16x16x32_bf16 v[58:61], v[166:169], v[190:193], v[58:61]
	v_mfma_f32_16x16x32_bf16 v[46:49], v[148:151], v[198:201], v[46:49]
	v_mfma_f32_16x16x32_bf16 v[42:45], v[166:169], v[198:201], v[42:45]
	v_mfma_f32_16x16x32_bf16 v[30:33], v[148:151], v[206:209], v[30:33]
	v_mfma_f32_16x16x32_bf16 v[26:29], v[166:169], v[206:209], v[26:29]
	v_mfma_f32_16x16x32_bf16 v[14:17], v[148:151], v[214:217], v[14:17]
	v_mfma_f32_16x16x32_bf16 v[10:13], v[166:169], v[214:217], v[10:13]
	v_mfma_f32_16x16x32_bf16 v[62:65], v[162:165], v[194:197], v[62:65]
	v_mfma_f32_16x16x32_bf16 v[58:61], v[170:173], v[194:197], v[58:61]
	v_mfma_f32_16x16x32_bf16 v[46:49], v[162:165], v[202:205], v[46:49]
	v_mfma_f32_16x16x32_bf16 v[42:45], v[170:173], v[202:205], v[42:45]
	v_mfma_f32_16x16x32_bf16 v[30:33], v[162:165], v[210:213], v[30:33]
	v_mfma_f32_16x16x32_bf16 v[26:29], v[170:173], v[210:213], v[26:29]
	v_mfma_f32_16x16x32_bf16 v[14:17], v[162:165], v[218:221], v[14:17]
	v_mfma_f32_16x16x32_bf16 v[10:13], v[170:173], v[218:221], v[10:13]
	s_setprio 0
	s_setprio 1
	v_mfma_f32_16x16x32_bf16 v[54:57], v[174:177], v[190:193], v[54:57]
	v_mfma_f32_16x16x32_bf16 v[50:53], v[182:185], v[190:193], v[50:53]
	v_mfma_f32_16x16x32_bf16 v[38:41], v[174:177], v[198:201], v[38:41]
	v_mfma_f32_16x16x32_bf16 v[34:37], v[182:185], v[198:201], v[34:37]
	v_mfma_f32_16x16x32_bf16 v[22:25], v[174:177], v[206:209], v[22:25]
	v_mfma_f32_16x16x32_bf16 v[18:21], v[182:185], v[206:209], v[18:21]
	v_mfma_f32_16x16x32_bf16 v[6:9], v[174:177], v[214:217], v[6:9]
	v_mfma_f32_16x16x32_bf16 v[2:5], v[182:185], v[214:217], v[2:5]
	v_mfma_f32_16x16x32_bf16 v[54:57], v[178:181], v[194:197], v[54:57]
	v_mfma_f32_16x16x32_bf16 v[50:53], v[186:189], v[194:197], v[50:53]
	v_mfma_f32_16x16x32_bf16 v[38:41], v[178:181], v[202:205], v[38:41]
	v_mfma_f32_16x16x32_bf16 v[34:37], v[186:189], v[202:205], v[34:37]
	v_mfma_f32_16x16x32_bf16 v[22:25], v[178:181], v[210:213], v[22:25]
	v_mfma_f32_16x16x32_bf16 v[18:21], v[186:189], v[210:213], v[18:21]
	v_mfma_f32_16x16x32_bf16 v[6:9], v[178:181], v[218:221], v[6:9]
	v_mfma_f32_16x16x32_bf16 v[2:5], v[186:189], v[218:221], v[2:5]
	s_setprio 0
	s_barrier
	s_add_i32 s66, s66, 2
	s_add_u32 s34, s34, 0x100
	s_addc_u32 s35, s35, 0
	s_add_u32 s64, s64, 0x100
	s_addc_u32 s65, s65, 0
	s_cmp_gt_u32 s66, 29
	s_cbranch_scc1 .Lpeel_exit_651

.LBB0_847:
	s_ashr_i32 s23, s22, 31
	s_lshl_b64 s[24:25], s[22:23], 20
	s_add_u32 s24, s70, s24
	s_addc_u32 s25, s71, s25
	s_and_b64 s[26:27], s[4:5], exec
	s_cselect_b32 s23, s25, s35
	s_cselect_b32 s58, s24, s34
	s_ashr_i32 s21, s20, 31
	s_lshl_b64 s[26:27], s[20:21], 20
	s_add_u32 s26, s33, s26
	s_addc_u32 s27, s40, s27
	s_and_b64 s[38:39], s[4:5], exec
	s_cselect_b32 s21, s27, s37
	s_cselect_b32 s59, s26, s36
	s_add_u32 s34, s34, 0x80080
	s_addc_u32 s35, s35, 0
	s_add_u32 s60, s36, 0x100
	v_mov_b32_e32 v2, 0
	s_addc_u32 s61, s37, 0
	s_mov_b32 s62, -2
	ds_read_b128 v[148:151], v157
	ds_read_b128 v[162:165], v157 offset:1024
	ds_read_b128 v[166:169], v157 offset:2048
	ds_read_b128 v[170:173], v157 offset:3072
	ds_read_b128 v[174:177], v159
	ds_read_b128 v[178:181], v159 offset:1024
	ds_read_b128 v[182:185], v159 offset:2048
	ds_read_b128 v[186:189], v159 offset:3072
	s_add_u32 s36, s34, 0xfff80080
	s_addc_u32 s37, s35, -1
	s_cmp_eq_u32 s62, 28
	s_cselect_b32 s39, s23, s37
	s_cselect_b32 s38, s58, s36
	s_cselect_b32 s37, s21, s61
	s_cselect_b32 s36, s59, s60
	v_lshl_add_u64 v[152:153], s[34:35], 0, v[138:139]
	s_add_i32 m0, s31, 0xc000
	ds_read_b128 v[190:193], v160
	ds_read_b128 v[194:197], v160 offset:1024
	ds_read_b128 v[198:201], v160 offset:2048
	ds_read_b128 v[202:205], v160 offset:3072
	ds_read_b128 v[206:209], v160 offset:4096
	ds_read_b128 v[210:213], v160 offset:5120
	ds_read_b128 v[214:217], v160 offset:6144
	ds_read_b128 v[218:221], v160 offset:7168
	global_load_lds_dwordx4 v[152:153], off
	v_lshl_add_u64 v[152:153], s[34:35], 0, v[140:141]
	s_add_i32 m0, s31, 0xe000
	s_nop 0
	global_load_lds_dwordx4 v[152:153], off
	s_waitcnt vmcnt(8)
	s_waitcnt lgkmcnt(0)
	s_barrier
	s_setprio 1
	s_waitcnt lgkmcnt(0)
	v_mfma_f32_16x16x32_bf16 v[126:129], v[148:151], v[190:193], 0
	v_mfma_f32_16x16x32_bf16 v[122:125], v[166:169], v[190:193], 0
	v_mfma_f32_16x16x32_bf16 v[110:113], v[148:151], v[198:201], 0
	v_mfma_f32_16x16x32_bf16 v[106:109], v[166:169], v[198:201], 0
	v_mfma_f32_16x16x32_bf16 v[94:97], v[148:151], v[206:209], 0
	v_mfma_f32_16x16x32_bf16 v[90:93], v[166:169], v[206:209], 0
	v_mfma_f32_16x16x32_bf16 v[78:81], v[148:151], v[214:217], 0
	v_mfma_f32_16x16x32_bf16 v[74:77], v[166:169], v[214:217], 0
	v_mfma_f32_16x16x32_bf16 v[126:129], v[162:165], v[194:197], v[126:129]
	v_mfma_f32_16x16x32_bf16 v[122:125], v[170:173], v[194:197], v[122:125]
	v_mfma_f32_16x16x32_bf16 v[110:113], v[162:165], v[202:205], v[110:113]
	v_mfma_f32_16x16x32_bf16 v[106:109], v[170:173], v[202:205], v[106:109]
	v_mfma_f32_16x16x32_bf16 v[94:97], v[162:165], v[210:213], v[94:97]
	v_mfma_f32_16x16x32_bf16 v[90:93], v[170:173], v[210:213], v[90:93]
	v_mfma_f32_16x16x32_bf16 v[78:81], v[162:165], v[218:221], v[78:81]
	v_mfma_f32_16x16x32_bf16 v[74:77], v[170:173], v[218:221], v[74:77]
	s_setprio 0
	s_setprio 1
	v_mfma_f32_16x16x32_bf16 v[118:121], v[174:177], v[190:193], 0
	v_mfma_f32_16x16x32_bf16 v[114:117], v[182:185], v[190:193], 0
	v_mfma_f32_16x16x32_bf16 v[102:105], v[174:177], v[198:201], 0
	v_mfma_f32_16x16x32_bf16 v[98:101], v[182:185], v[198:201], 0
	v_mfma_f32_16x16x32_bf16 v[86:89], v[174:177], v[206:209], 0
	v_mfma_f32_16x16x32_bf16 v[82:85], v[182:185], v[206:209], 0
	v_mfma_f32_16x16x32_bf16 v[70:73], v[174:177], v[214:217], 0
	v_mfma_f32_16x16x32_bf16 v[66:69], v[182:185], v[214:217], 0
	v_mfma_f32_16x16x32_bf16 v[118:121], v[178:181], v[194:197], v[118:121]
	v_mfma_f32_16x16x32_bf16 v[114:117], v[186:189], v[194:197], v[114:117]
	v_mfma_f32_16x16x32_bf16 v[102:105], v[178:181], v[202:205], v[102:105]
	v_mfma_f32_16x16x32_bf16 v[98:101], v[186:189], v[202:205], v[98:101]
	v_mfma_f32_16x16x32_bf16 v[86:89], v[178:181], v[210:213], v[86:89]
	v_mfma_f32_16x16x32_bf16 v[82:85], v[186:189], v[210:213], v[82:85]
	v_mfma_f32_16x16x32_bf16 v[70:73], v[178:181], v[218:221], v[70:73]
	v_mfma_f32_16x16x32_bf16 v[66:69], v[186:189], v[218:221], v[66:69]
	s_setprio 0
	s_barrier
	s_add_i32 s63, s55, s41
	v_lshl_add_u64 v[152:153], s[36:37], 0, v[132:133]
	s_mov_b32 m0, s63
	ds_read_b128 v[190:193], v160 offset:16384
	ds_read_b128 v[194:197], v160 offset:17408
	ds_read_b128 v[198:201], v160 offset:18432
	ds_read_b128 v[202:205], v160 offset:19456
	ds_read_b128 v[206:209], v160 offset:20480
	ds_read_b128 v[210:213], v160 offset:21504
	ds_read_b128 v[214:217], v160 offset:22528
	ds_read_b128 v[218:221], v160 offset:23552
	global_load_lds_dwordx4 v[152:153], off
	s_add_i32 m0, s63, 0x2000
	s_add_u32 s64, s36, 0x80000
	v_lshl_add_u64 v[222:223], s[36:37], 0, v[136:137]
	s_addc_u32 s65, s37, 0
	s_add_i32 s63, s56, s41
	global_load_lds_dwordx4 v[222:223], off
	v_lshl_add_u64 v[224:225], s[64:65], 0, v[132:133]
	s_mov_b32 m0, s63
	v_lshl_add_u64 v[226:227], s[38:39], 0, v[134:135]
	global_load_lds_dwordx4 v[224:225], off
	v_lshl_add_u64 v[224:225], s[64:65], 0, v[136:137]
	s_add_i32 m0, s63, 0x2000
	s_nop 0
	global_load_lds_dwordx4 v[224:225], off
	v_lshl_add_u64 v[224:225], s[38:39], 0, v[130:131]
	s_mov_b32 m0, s31
	s_nop 0
	global_load_lds_dwordx4 v[224:225], off
	s_mov_b32 m0, s42
	s_nop 0
	global_load_lds_dwordx4 v[226:227], off
	s_waitcnt vmcnt(8)
	s_waitcnt lgkmcnt(0)
	s_barrier
	s_setprio 1
	s_waitcnt lgkmcnt(0)
	v_mfma_f32_16x16x32_bf16 v[62:65], v[148:151], v[190:193], 0
	v_mfma_f32_16x16x32_bf16 v[58:61], v[166:169], v[190:193], 0
	v_mfma_f32_16x16x32_bf16 v[46:49], v[148:151], v[198:201], 0
	v_mfma_f32_16x16x32_bf16 v[42:45], v[166:169], v[198:201], 0
	v_mfma_f32_16x16x32_bf16 v[30:33], v[148:151], v[206:209], 0
	v_mfma_f32_16x16x32_bf16 v[26:29], v[166:169], v[206:209], 0
	v_mfma_f32_16x16x32_bf16 v[14:17], v[148:151], v[214:217], 0
	v_mfma_f32_16x16x32_bf16 v[10:13], v[166:169], v[214:217], 0
	v_mfma_f32_16x16x32_bf16 v[62:65], v[162:165], v[194:197], v[62:65]
	v_mfma_f32_16x16x32_bf16 v[58:61], v[170:173], v[194:197], v[58:61]
	v_mfma_f32_16x16x32_bf16 v[46:49], v[162:165], v[202:205], v[46:49]
	v_mfma_f32_16x16x32_bf16 v[42:45], v[170:173], v[202:205], v[42:45]
	v_mfma_f32_16x16x32_bf16 v[30:33], v[162:165], v[210:213], v[30:33]
	v_mfma_f32_16x16x32_bf16 v[26:29], v[170:173], v[210:213], v[26:29]
	v_mfma_f32_16x16x32_bf16 v[14:17], v[162:165], v[218:221], v[14:17]
	v_mfma_f32_16x16x32_bf16 v[10:13], v[170:173], v[218:221], v[10:13]
	s_setprio 0
	s_setprio 1
	v_mfma_f32_16x16x32_bf16 v[54:57], v[174:177], v[190:193], 0
	v_mfma_f32_16x16x32_bf16 v[50:53], v[182:185], v[190:193], 0
	v_mfma_f32_16x16x32_bf16 v[38:41], v[174:177], v[198:201], 0
	v_mfma_f32_16x16x32_bf16 v[34:37], v[182:185], v[198:201], 0
	v_mfma_f32_16x16x32_bf16 v[22:25], v[174:177], v[206:209], 0
	v_mfma_f32_16x16x32_bf16 v[18:21], v[182:185], v[206:209], 0
	v_mfma_f32_16x16x32_bf16 v[6:9], v[174:177], v[214:217], 0
	v_mfma_f32_16x16x32_bf16 v[2:5], v[182:185], v[214:217], 0
	v_mfma_f32_16x16x32_bf16 v[54:57], v[178:181], v[194:197], v[54:57]
	v_mfma_f32_16x16x32_bf16 v[50:53], v[186:189], v[194:197], v[50:53]
	v_mfma_f32_16x16x32_bf16 v[38:41], v[178:181], v[202:205], v[38:41]
	v_mfma_f32_16x16x32_bf16 v[34:37], v[186:189], v[202:205], v[34:37]
	v_mfma_f32_16x16x32_bf16 v[22:25], v[178:181], v[210:213], v[22:25]
	v_mfma_f32_16x16x32_bf16 v[18:21], v[186:189], v[210:213], v[18:21]
	v_mfma_f32_16x16x32_bf16 v[6:9], v[178:181], v[218:221], v[6:9]
	v_mfma_f32_16x16x32_bf16 v[2:5], v[186:189], v[218:221], v[2:5]
	s_setprio 0
	s_barrier
	s_add_i32 s63, 0, 0x18000
	v_add_u32_e32 v161, s63, v155
	s_add_i32 s64, 0, 0x1c000
	ds_read_b128 v[148:151], v161
	ds_read_b128 v[162:165], v161 offset:1024
	ds_read_b128 v[166:169], v161 offset:2048
	ds_read_b128 v[170:173], v161 offset:3072
	v_add_u32_e32 v161, s64, v155
	ds_read_b128 v[174:177], v161
	ds_read_b128 v[178:181], v161 offset:1024
	ds_read_b128 v[182:185], v161 offset:2048
	ds_read_b128 v[186:189], v161 offset:3072
	s_add_u32 s38, s38, 0x80000
	s_addc_u32 s39, s39, 0
	s_mov_b32 m0, s43
	v_lshl_add_u64 v[228:229], s[38:39], 0, v[130:131]
	ds_read_b128 v[190:193], v160 offset:32768
	ds_read_b128 v[194:197], v160 offset:33792
	ds_read_b128 v[198:201], v160 offset:34816
	ds_read_b128 v[202:205], v160 offset:35840
	ds_read_b128 v[206:209], v160 offset:36864
	ds_read_b128 v[210:213], v160 offset:37888
	ds_read_b128 v[214:217], v160 offset:38912
	ds_read_b128 v[218:221], v160 offset:39936
	global_load_lds_dwordx4 v[228:229], off
	v_lshl_add_u64 v[228:229], s[38:39], 0, v[134:135]
	s_mov_b32 m0, s44
	s_nop 0
	global_load_lds_dwordx4 v[228:229], off
	s_waitcnt vmcnt(8)
	s_waitcnt lgkmcnt(0)
	s_barrier
	s_setprio 1
	s_waitcnt lgkmcnt(0)
	v_mfma_f32_16x16x32_bf16 v[126:129], v[148:151], v[190:193], v[126:129]
	v_mfma_f32_16x16x32_bf16 v[122:125], v[166:169], v[190:193], v[122:125]
	v_mfma_f32_16x16x32_bf16 v[110:113], v[148:151], v[198:201], v[110:113]
	v_mfma_f32_16x16x32_bf16 v[106:109], v[166:169], v[198:201], v[106:109]
	v_mfma_f32_16x16x32_bf16 v[94:97], v[148:151], v[206:209], v[94:97]
	v_mfma_f32_16x16x32_bf16 v[90:93], v[166:169], v[206:209], v[90:93]
	v_mfma_f32_16x16x32_bf16 v[78:81], v[148:151], v[214:217], v[78:81]
	v_mfma_f32_16x16x32_bf16 v[74:77], v[166:169], v[214:217], v[74:77]
	v_mfma_f32_16x16x32_bf16 v[126:129], v[162:165], v[194:197], v[126:129]
	v_mfma_f32_16x16x32_bf16 v[122:125], v[170:173], v[194:197], v[122:125]
	v_mfma_f32_16x16x32_bf16 v[110:113], v[162:165], v[202:205], v[110:113]
	v_mfma_f32_16x16x32_bf16 v[106:109], v[170:173], v[202:205], v[106:109]
	v_mfma_f32_16x16x32_bf16 v[94:97], v[162:165], v[210:213], v[94:97]
	v_mfma_f32_16x16x32_bf16 v[90:93], v[170:173], v[210:213], v[90:93]
	v_mfma_f32_16x16x32_bf16 v[78:81], v[162:165], v[218:221], v[78:81]
	v_mfma_f32_16x16x32_bf16 v[74:77], v[170:173], v[218:221], v[74:77]
	s_setprio 0
	s_setprio 1
	v_mfma_f32_16x16x32_bf16 v[118:121], v[174:177], v[190:193], v[118:121]
	v_mfma_f32_16x16x32_bf16 v[114:117], v[182:185], v[190:193], v[114:117]
	v_mfma_f32_16x16x32_bf16 v[102:105], v[174:177], v[198:201], v[102:105]
	v_mfma_f32_16x16x32_bf16 v[98:101], v[182:185], v[198:201], v[98:101]
	v_mfma_f32_16x16x32_bf16 v[86:89], v[174:177], v[206:209], v[86:89]
	v_mfma_f32_16x16x32_bf16 v[82:85], v[182:185], v[206:209], v[82:85]
	v_mfma_f32_16x16x32_bf16 v[70:73], v[174:177], v[214:217], v[70:73]
	v_mfma_f32_16x16x32_bf16 v[66:69], v[182:185], v[214:217], v[66:69]
	v_mfma_f32_16x16x32_bf16 v[118:121], v[178:181], v[194:197], v[118:121]
	v_mfma_f32_16x16x32_bf16 v[114:117], v[186:189], v[194:197], v[114:117]
	v_mfma_f32_16x16x32_bf16 v[102:105], v[178:181], v[202:205], v[102:105]
	v_mfma_f32_16x16x32_bf16 v[98:101], v[186:189], v[202:205], v[98:101]
	v_mfma_f32_16x16x32_bf16 v[86:89], v[178:181], v[210:213], v[86:89]
	v_mfma_f32_16x16x32_bf16 v[82:85], v[186:189], v[210:213], v[82:85]
	v_mfma_f32_16x16x32_bf16 v[70:73], v[178:181], v[218:221], v[70:73]
	v_mfma_f32_16x16x32_bf16 v[66:69], v[186:189], v[218:221], v[66:69]
	s_setprio 0
	s_barrier
	s_add_i32 s38, s63, s41
	v_lshl_add_u64 v[152:153], v[152:153], 0, s[8:9]
	s_mov_b32 m0, s38
	ds_read_b128 v[190:193], v160 offset:49152
	ds_read_b128 v[194:197], v160 offset:50176
	ds_read_b128 v[198:201], v160 offset:51200
	ds_read_b128 v[202:205], v160 offset:52224
	ds_read_b128 v[206:209], v160 offset:53248
	ds_read_b128 v[210:213], v160 offset:54272
	ds_read_b128 v[214:217], v160 offset:55296
	ds_read_b128 v[218:221], v160 offset:56320
	global_load_lds_dwordx4 v[152:153], off
	s_add_i32 m0, s38, 0x2000
	s_add_u32 s36, s36, 0x80080
	v_lshl_add_u64 v[152:153], v[222:223], 0, s[8:9]
	s_addc_u32 s37, s37, 0
	s_add_i32 s38, s64, s41
	global_load_lds_dwordx4 v[152:153], off
	v_lshl_add_u64 v[152:153], s[36:37], 0, v[132:133]
	s_mov_b32 m0, s38
	s_nop 0
	global_load_lds_dwordx4 v[152:153], off
	v_lshl_add_u64 v[152:153], s[36:37], 0, v[136:137]
	s_add_i32 m0, s38, 0x2000
	s_nop 0
	global_load_lds_dwordx4 v[152:153], off
	v_lshl_add_u64 v[152:153], v[224:225], 0, s[8:9]
	s_mov_b32 m0, s48
	s_nop 0
	global_load_lds_dwordx4 v[152:153], off
	v_lshl_add_u64 v[152:153], v[226:227], 0, s[8:9]
	s_mov_b32 m0, s49
	s_nop 0
	global_load_lds_dwordx4 v[152:153], off
	s_waitcnt vmcnt(8)
	s_waitcnt lgkmcnt(0)
	s_barrier
	s_setprio 1
	s_waitcnt lgkmcnt(0)
	v_mfma_f32_16x16x32_bf16 v[62:65], v[148:151], v[190:193], v[62:65]
	v_mfma_f32_16x16x32_bf16 v[58:61], v[166:169], v[190:193], v[58:61]
	v_mfma_f32_16x16x32_bf16 v[46:49], v[148:151], v[198:201], v[46:49]
	v_mfma_f32_16x16x32_bf16 v[42:45], v[166:169], v[198:201], v[42:45]
	v_mfma_f32_16x16x32_bf16 v[30:33], v[148:151], v[206:209], v[30:33]
	v_mfma_f32_16x16x32_bf16 v[26:29], v[166:169], v[206:209], v[26:29]
	v_mfma_f32_16x16x32_bf16 v[14:17], v[148:151], v[214:217], v[14:17]
	v_mfma_f32_16x16x32_bf16 v[10:13], v[166:169], v[214:217], v[10:13]
	v_mfma_f32_16x16x32_bf16 v[62:65], v[162:165], v[194:197], v[62:65]
	v_mfma_f32_16x16x32_bf16 v[58:61], v[170:173], v[194:197], v[58:61]
	v_mfma_f32_16x16x32_bf16 v[46:49], v[162:165], v[202:205], v[46:49]
	v_mfma_f32_16x16x32_bf16 v[42:45], v[170:173], v[202:205], v[42:45]
	v_mfma_f32_16x16x32_bf16 v[30:33], v[162:165], v[210:213], v[30:33]
	v_mfma_f32_16x16x32_bf16 v[26:29], v[170:173], v[210:213], v[26:29]
	v_mfma_f32_16x16x32_bf16 v[14:17], v[162:165], v[218:221], v[14:17]
	v_mfma_f32_16x16x32_bf16 v[10:13], v[170:173], v[218:221], v[10:13]
	s_setprio 0
	s_setprio 1
	v_mfma_f32_16x16x32_bf16 v[54:57], v[174:177], v[190:193], v[54:57]
	v_mfma_f32_16x16x32_bf16 v[50:53], v[182:185], v[190:193], v[50:53]
	v_mfma_f32_16x16x32_bf16 v[38:41], v[174:177], v[198:201], v[38:41]
	v_mfma_f32_16x16x32_bf16 v[34:37], v[182:185], v[198:201], v[34:37]
	v_mfma_f32_16x16x32_bf16 v[22:25], v[174:177], v[206:209], v[22:25]
	v_mfma_f32_16x16x32_bf16 v[18:21], v[182:185], v[206:209], v[18:21]
	v_mfma_f32_16x16x32_bf16 v[6:9], v[174:177], v[214:217], v[6:9]
	v_mfma_f32_16x16x32_bf16 v[2:5], v[182:185], v[214:217], v[2:5]
	v_mfma_f32_16x16x32_bf16 v[54:57], v[178:181], v[194:197], v[54:57]
	v_mfma_f32_16x16x32_bf16 v[50:53], v[186:189], v[194:197], v[50:53]
	v_mfma_f32_16x16x32_bf16 v[38:41], v[178:181], v[202:205], v[38:41]
	v_mfma_f32_16x16x32_bf16 v[34:37], v[186:189], v[202:205], v[34:37]
	v_mfma_f32_16x16x32_bf16 v[22:25], v[178:181], v[210:213], v[22:25]
	v_mfma_f32_16x16x32_bf16 v[18:21], v[186:189], v[210:213], v[18:21]
	v_mfma_f32_16x16x32_bf16 v[6:9], v[178:181], v[218:221], v[6:9]
	v_mfma_f32_16x16x32_bf16 v[2:5], v[186:189], v[218:221], v[2:5]
	s_setprio 0
	s_barrier
	s_add_i32 s62, s62, 2
	s_add_u32 s34, s34, 0x100
	s_addc_u32 s35, s35, 0
	s_add_u32 s60, s60, 0x100
	s_addc_u32 s61, s61, 0
	s_cmp_gt_u32 s62, 29
	s_cbranch_scc1 .Lpeel_exit_848

.Lpeel_exit_848:
	s_and_b64 vcc, exec, s[10:11]
	s_cbranch_vccz .LBB0_851
	s_barrier

.LBB0_1083:
	s_lshl_b64 s[20:21], s[16:17], 19
	s_add_u32 s20, s15, s20
	s_addc_u32 s21, s33, s21
	s_and_b64 s[22:23], exec, s[2:3]
	s_cselect_b32 s17, s21, s27
	s_cselect_b32 s59, s20, s26
	s_ashr_i32 s19, s18, 31
	s_lshl_b64 s[22:23], s[18:19], 19
	s_add_u32 s22, s36, s22
	s_addc_u32 s23, s37, s23
	s_and_b64 s[34:35], exec, s[2:3]
	s_cselect_b32 s19, s23, s31
	s_cselect_b32 s60, s22, s30
	s_add_u32 s26, s26, 0x40080
	s_addc_u32 s27, s27, 0
	s_add_u32 s61, s30, 0x100
	v_mov_b32_e32 v2, 0
	s_addc_u32 s62, s31, 0
	s_mov_b32 s63, -2
	ds_read_b128 v[164:167], v152
	ds_read_b128 v[168:171], v152 offset:1024
	ds_read_b128 v[172:175], v152 offset:2048
	ds_read_b128 v[176:179], v152 offset:3072
	ds_read_b128 v[180:183], v153
	ds_read_b128 v[184:187], v153 offset:1024
	ds_read_b128 v[224:227], v153 offset:2048
	ds_read_b128 v[228:231], v153 offset:3072
	s_add_u32 s30, s26, 0xfffc0080
	s_addc_u32 s31, s27, -1
	s_cmp_eq_u32 s63, 12
	s_cselect_b32 s35, s17, s31
	s_cselect_b32 s34, s59, s30
	s_cselect_b32 s31, s19, s62
	s_cselect_b32 s30, s60, s61
	v_lshl_add_u64 v[148:149], s[26:27], 0, v[142:143]
	s_add_i32 m0, s25, 0xc000
	ds_read_b128 v[192:195], v154
	ds_read_b128 v[196:199], v154 offset:1024
	ds_read_b128 v[200:203], v154 offset:2048
	ds_read_b128 v[204:207], v154 offset:3072
	ds_read_b128 v[208:211], v154 offset:4096
	ds_read_b128 v[212:215], v154 offset:5120
	ds_read_b128 v[216:219], v154 offset:6144
	ds_read_b128 v[220:223], v154 offset:7168
	global_load_lds_dwordx4 v[148:149], off
	v_lshl_add_u64 v[148:149], s[26:27], 0, v[144:145]
	s_add_i32 m0, s25, 0xe000
	s_nop 0
	global_load_lds_dwordx4 v[148:149], off
	s_waitcnt vmcnt(8)
	s_waitcnt lgkmcnt(0)
	s_barrier
	s_setprio 1
	s_waitcnt lgkmcnt(0)
	s_nop 0
	v_mfma_scale_f32_16x16x128_f8f6f4 v[126:129], v[164:171], v[192:199], 0, v156, v155 op_sel_hi:[0,0,0]
	v_mfma_scale_f32_16x16x128_f8f6f4 v[122:125], v[172:179], v[192:199], 0, v156, v155 op_sel_hi:[0,0,0]
	v_mfma_scale_f32_16x16x128_f8f6f4 v[110:113], v[164:171], v[200:207], 0, v156, v155 op_sel_hi:[0,0,0]
	v_mfma_scale_f32_16x16x128_f8f6f4 v[106:109], v[172:179], v[200:207], 0, v156, v155 op_sel_hi:[0,0,0]
	v_mfma_scale_f32_16x16x128_f8f6f4 v[94:97], v[164:171], v[208:215], 0, v156, v155 op_sel_hi:[0,0,0]
	v_mfma_scale_f32_16x16x128_f8f6f4 v[90:93], v[172:179], v[208:215], 0, v156, v155 op_sel_hi:[0,0,0]
	v_mfma_scale_f32_16x16x128_f8f6f4 v[78:81], v[164:171], v[216:223], 0, v156, v155 op_sel_hi:[0,0,0]
	v_mfma_scale_f32_16x16x128_f8f6f4 v[74:77], v[172:179], v[216:223], 0, v156, v155 op_sel_hi:[0,0,0]
	s_setprio 0
	s_setprio 1
	s_nop 0
	v_mfma_scale_f32_16x16x128_f8f6f4 v[118:121], v[180:187], v[192:199], 0, v156, v155 op_sel_hi:[0,0,0]
	v_mfma_scale_f32_16x16x128_f8f6f4 v[114:117], v[224:231], v[192:199], 0, v156, v155 op_sel_hi:[0,0,0]
	v_mfma_scale_f32_16x16x128_f8f6f4 v[102:105], v[180:187], v[200:207], 0, v156, v155 op_sel_hi:[0,0,0]
	v_mfma_scale_f32_16x16x128_f8f6f4 v[98:101], v[224:231], v[200:207], 0, v156, v155 op_sel_hi:[0,0,0]
	v_mfma_scale_f32_16x16x128_f8f6f4 v[86:89], v[180:187], v[208:215], 0, v156, v155 op_sel_hi:[0,0,0]
	v_mfma_scale_f32_16x16x128_f8f6f4 v[82:85], v[224:231], v[208:215], 0, v156, v155 op_sel_hi:[0,0,0]
	v_mfma_scale_f32_16x16x128_f8f6f4 v[70:73], v[180:187], v[216:223], 0, v156, v155 op_sel_hi:[0,0,0]
	v_mfma_scale_f32_16x16x128_f8f6f4 v[66:69], v[224:231], v[216:223], 0, v156, v155 op_sel_hi:[0,0,0]
	s_setprio 0
	s_barrier
	s_add_i32 s64, s53, s40
	v_lshl_add_u64 v[188:189], s[30:31], 0, v[132:133]
	s_mov_b32 m0, s64
	ds_read_b128 v[192:195], v154 offset:16384
	ds_read_b128 v[196:199], v154 offset:17408
	ds_read_b128 v[200:203], v154 offset:18432
	ds_read_b128 v[204:207], v154 offset:19456
	ds_read_b128 v[208:211], v154 offset:20480
	ds_read_b128 v[212:215], v154 offset:21504
	ds_read_b128 v[216:219], v154 offset:22528
	ds_read_b128 v[220:223], v154 offset:23552
	global_load_lds_dwordx4 v[188:189], off
	s_add_i32 m0, s64, 0x2000
	s_add_u32 s64, s30, 0x40000
	v_lshl_add_u64 v[190:191], s[30:31], 0, v[140:141]
	s_addc_u32 s65, s31, 0
	s_add_i32 s66, s54, s40
	global_load_lds_dwordx4 v[190:191], off
	v_lshl_add_u64 v[148:149], s[64:65], 0, v[132:133]
	s_mov_b32 m0, s66
	v_lshl_add_u64 v[232:233], s[34:35], 0, v[138:139]
	global_load_lds_dwordx4 v[148:149], off
	v_lshl_add_u64 v[148:149], s[64:65], 0, v[140:141]
	s_add_i32 m0, s66, 0x2000
	v_lshl_add_u64 v[234:235], s[34:35], 0, v[136:137]
	global_load_lds_dwordx4 v[148:149], off
	s_mov_b32 m0, s25
	s_nop 0
	global_load_lds_dwordx4 v[232:233], off
	s_mov_b32 m0, s44
	s_nop 0
	global_load_lds_dwordx4 v[234:235], off
	s_waitcnt vmcnt(8)
	s_waitcnt lgkmcnt(0)
	s_barrier
	s_setprio 1
	s_waitcnt lgkmcnt(0)
	s_nop 0
	v_mfma_scale_f32_16x16x128_f8f6f4 v[62:65], v[164:171], v[192:199], 0, v156, v155 op_sel_hi:[0,0,0]
	v_mfma_scale_f32_16x16x128_f8f6f4 v[58:61], v[172:179], v[192:199], 0, v156, v155 op_sel_hi:[0,0,0]
	v_mfma_scale_f32_16x16x128_f8f6f4 v[46:49], v[164:171], v[200:207], 0, v156, v155 op_sel_hi:[0,0,0]
	v_mfma_scale_f32_16x16x128_f8f6f4 v[42:45], v[172:179], v[200:207], 0, v156, v155 op_sel_hi:[0,0,0]
	v_mfma_scale_f32_16x16x128_f8f6f4 v[30:33], v[164:171], v[208:215], 0, v156, v155 op_sel_hi:[0,0,0]
	v_mfma_scale_f32_16x16x128_f8f6f4 v[26:29], v[172:179], v[208:215], 0, v156, v155 op_sel_hi:[0,0,0]
	v_mfma_scale_f32_16x16x128_f8f6f4 v[14:17], v[164:171], v[216:223], 0, v156, v155 op_sel_hi:[0,0,0]
	v_mfma_scale_f32_16x16x128_f8f6f4 v[10:13], v[172:179], v[216:223], 0, v156, v155 op_sel_hi:[0,0,0]
	s_setprio 0
	s_setprio 1
	s_nop 0
	v_mfma_scale_f32_16x16x128_f8f6f4 v[54:57], v[180:187], v[192:199], 0, v156, v155 op_sel_hi:[0,0,0]
	v_mfma_scale_f32_16x16x128_f8f6f4 v[50:53], v[224:231], v[192:199], 0, v156, v155 op_sel_hi:[0,0,0]
	v_mfma_scale_f32_16x16x128_f8f6f4 v[38:41], v[180:187], v[200:207], 0, v156, v155 op_sel_hi:[0,0,0]
	v_mfma_scale_f32_16x16x128_f8f6f4 v[34:37], v[224:231], v[200:207], 0, v156, v155 op_sel_hi:[0,0,0]
	v_mfma_scale_f32_16x16x128_f8f6f4 v[148:151], v[180:187], v[208:215], 0, v156, v155 op_sel_hi:[0,0,0]
	v_mfma_scale_f32_16x16x128_f8f6f4 v[158:161], v[224:231], v[208:215], 0, v156, v155 op_sel_hi:[0,0,0]
	v_mfma_scale_f32_16x16x128_f8f6f4 v[180:183], v[180:187], v[216:223], 0, v156, v155 op_sel_hi:[0,0,0]
	v_mfma_scale_f32_16x16x128_f8f6f4 v[184:187], v[224:231], v[216:223], 0, v156, v155 op_sel_hi:[0,0,0]
	s_setprio 0
	s_barrier
	s_add_i32 s64, 0, 0x18000
	s_add_i32 s65, 0, 0x1c000
	v_add_u32_e32 v22, s64, v135
	v_add_u32_e32 v162, s65, v135
	s_nop 0
	ds_read_b128 v[2:5], v22
	ds_read_b128 v[6:9], v22 offset:1024
	ds_read_b128 v[18:21], v22 offset:2048
	ds_read_b128 v[22:25], v22 offset:3072
	ds_read_b128 v[164:167], v162
	ds_read_b128 v[168:171], v162 offset:1024
	ds_read_b128 v[172:175], v162 offset:2048
	ds_read_b128 v[176:179], v162 offset:3072
	s_add_u32 s34, s34, 0x40000
	s_addc_u32 s35, s35, 0
	s_mov_b32 m0, s45
	v_lshl_add_u64 v[224:225], s[34:35], 0, v[138:139]
	ds_read_b128 v[192:195], v154 offset:32768
	ds_read_b128 v[196:199], v154 offset:33792
	ds_read_b128 v[200:203], v154 offset:34816
	ds_read_b128 v[204:207], v154 offset:35840
	ds_read_b128 v[208:211], v154 offset:36864
	ds_read_b128 v[212:215], v154 offset:37888
	ds_read_b128 v[216:219], v154 offset:38912
	ds_read_b128 v[220:223], v154 offset:39936
	global_load_lds_dwordx4 v[224:225], off
	v_lshl_add_u64 v[224:225], s[34:35], 0, v[136:137]
	s_mov_b32 m0, s48
	s_nop 0
	global_load_lds_dwordx4 v[224:225], off
	s_waitcnt vmcnt(8)
	s_waitcnt lgkmcnt(0)
	s_barrier
	s_setprio 1
	s_waitcnt lgkmcnt(0)
	s_nop 0
	v_mfma_scale_f32_16x16x128_f8f6f4 v[126:129], v[2:9], v[192:199], v[126:129], v156, v155 op_sel_hi:[0,0,0]
	v_mfma_scale_f32_16x16x128_f8f6f4 v[122:125], v[18:25], v[192:199], v[122:125], v156, v155 op_sel_hi:[0,0,0]
	v_mfma_scale_f32_16x16x128_f8f6f4 v[110:113], v[2:9], v[200:207], v[110:113], v156, v155 op_sel_hi:[0,0,0]
	v_mfma_scale_f32_16x16x128_f8f6f4 v[106:109], v[18:25], v[200:207], v[106:109], v156, v155 op_sel_hi:[0,0,0]
	v_mfma_scale_f32_16x16x128_f8f6f4 v[94:97], v[2:9], v[208:215], v[94:97], v156, v155 op_sel_hi:[0,0,0]
	v_mfma_scale_f32_16x16x128_f8f6f4 v[90:93], v[18:25], v[208:215], v[90:93], v156, v155 op_sel_hi:[0,0,0]
	v_mfma_scale_f32_16x16x128_f8f6f4 v[78:81], v[2:9], v[216:223], v[78:81], v156, v155 op_sel_hi:[0,0,0]
	v_mfma_scale_f32_16x16x128_f8f6f4 v[74:77], v[18:25], v[216:223], v[74:77], v156, v155 op_sel_hi:[0,0,0]
	s_setprio 0
	s_setprio 1
	s_nop 0
	v_mfma_scale_f32_16x16x128_f8f6f4 v[118:121], v[164:171], v[192:199], v[118:121], v156, v155 op_sel_hi:[0,0,0]
	v_mfma_scale_f32_16x16x128_f8f6f4 v[114:117], v[172:179], v[192:199], v[114:117], v156, v155 op_sel_hi:[0,0,0]
	v_mfma_scale_f32_16x16x128_f8f6f4 v[102:105], v[164:171], v[200:207], v[102:105], v156, v155 op_sel_hi:[0,0,0]
	v_mfma_scale_f32_16x16x128_f8f6f4 v[98:101], v[172:179], v[200:207], v[98:101], v156, v155 op_sel_hi:[0,0,0]
	v_mfma_scale_f32_16x16x128_f8f6f4 v[86:89], v[164:171], v[208:215], v[86:89], v156, v155 op_sel_hi:[0,0,0]
	v_mfma_scale_f32_16x16x128_f8f6f4 v[82:85], v[172:179], v[208:215], v[82:85], v156, v155 op_sel_hi:[0,0,0]
	v_mfma_scale_f32_16x16x128_f8f6f4 v[70:73], v[164:171], v[216:223], v[70:73], v156, v155 op_sel_hi:[0,0,0]
	v_mfma_scale_f32_16x16x128_f8f6f4 v[66:69], v[172:179], v[216:223], v[66:69], v156, v155 op_sel_hi:[0,0,0]
	s_setprio 0
	s_barrier
	s_add_i32 s34, s64, s40
	v_lshl_add_u64 v[188:189], v[188:189], 0, s[8:9]
	s_mov_b32 m0, s34
	ds_read_b128 v[192:195], v154 offset:49152
	ds_read_b128 v[196:199], v154 offset:50176
	ds_read_b128 v[200:203], v154 offset:51200
	ds_read_b128 v[204:207], v154 offset:52224
	ds_read_b128 v[208:211], v154 offset:53248
	ds_read_b128 v[212:215], v154 offset:54272
	ds_read_b128 v[216:219], v154 offset:55296
	ds_read_b128 v[220:223], v154 offset:56320
	global_load_lds_dwordx4 v[188:189], off
	s_add_i32 m0, s34, 0x2000
	s_add_u32 s30, s30, 0x40080
	v_lshl_add_u64 v[188:189], v[190:191], 0, s[8:9]
	s_addc_u32 s31, s31, 0
	s_add_i32 s34, s65, s40
	global_load_lds_dwordx4 v[188:189], off
	v_lshl_add_u64 v[188:189], s[30:31], 0, v[132:133]
	s_mov_b32 m0, s34
	s_nop 0
	global_load_lds_dwordx4 v[188:189], off
	v_lshl_add_u64 v[188:189], s[30:31], 0, v[140:141]
	s_add_i32 m0, s34, 0x2000
	s_nop 0
	global_load_lds_dwordx4 v[188:189], off
	v_lshl_add_u64 v[188:189], v[232:233], 0, s[8:9]
	s_mov_b32 m0, s50
	s_nop 0
	global_load_lds_dwordx4 v[188:189], off
	v_lshl_add_u64 v[188:189], v[234:235], 0, s[8:9]
	s_mov_b32 m0, s51
	s_nop 0
	global_load_lds_dwordx4 v[188:189], off
	s_waitcnt vmcnt(8)
	s_waitcnt lgkmcnt(0)
	s_barrier
	s_setprio 1
	s_waitcnt lgkmcnt(0)
	s_nop 0
	v_mfma_scale_f32_16x16x128_f8f6f4 v[62:65], v[2:9], v[192:199], v[62:65], v156, v155 op_sel_hi:[0,0,0]
	v_mfma_scale_f32_16x16x128_f8f6f4 v[58:61], v[18:25], v[192:199], v[58:61], v156, v155 op_sel_hi:[0,0,0]
	v_mfma_scale_f32_16x16x128_f8f6f4 v[46:49], v[2:9], v[200:207], v[46:49], v156, v155 op_sel_hi:[0,0,0]
	v_mfma_scale_f32_16x16x128_f8f6f4 v[42:45], v[18:25], v[200:207], v[42:45], v156, v155 op_sel_hi:[0,0,0]
	v_mfma_scale_f32_16x16x128_f8f6f4 v[30:33], v[2:9], v[208:215], v[30:33], v156, v155 op_sel_hi:[0,0,0]
	v_mfma_scale_f32_16x16x128_f8f6f4 v[26:29], v[18:25], v[208:215], v[26:29], v156, v155 op_sel_hi:[0,0,0]
	v_mfma_scale_f32_16x16x128_f8f6f4 v[14:17], v[2:9], v[216:223], v[14:17], v156, v155 op_sel_hi:[0,0,0]
	v_mfma_scale_f32_16x16x128_f8f6f4 v[10:13], v[18:25], v[216:223], v[10:13], v156, v155 op_sel_hi:[0,0,0]
	s_setprio 0
	s_setprio 1
	s_nop 0
	v_mfma_scale_f32_16x16x128_f8f6f4 v[54:57], v[164:171], v[192:199], v[54:57], v156, v155 op_sel_hi:[0,0,0]
	v_mfma_scale_f32_16x16x128_f8f6f4 v[50:53], v[172:179], v[192:199], v[50:53], v156, v155 op_sel_hi:[0,0,0]
	v_mfma_scale_f32_16x16x128_f8f6f4 v[38:41], v[164:171], v[200:207], v[38:41], v156, v155 op_sel_hi:[0,0,0]
	v_mfma_scale_f32_16x16x128_f8f6f4 v[34:37], v[172:179], v[200:207], v[34:37], v156, v155 op_sel_hi:[0,0,0]
	v_mfma_scale_f32_16x16x128_f8f6f4 v[22:25], v[164:171], v[208:215], v[148:151], v156, v155 op_sel_hi:[0,0,0]
	v_mfma_scale_f32_16x16x128_f8f6f4 v[18:21], v[172:179], v[208:215], v[158:161], v156, v155 op_sel_hi:[0,0,0]
	v_mfma_scale_f32_16x16x128_f8f6f4 v[6:9], v[164:171], v[216:223], v[180:183], v156, v155 op_sel_hi:[0,0,0]
	v_mfma_scale_f32_16x16x128_f8f6f4 v[2:5], v[172:179], v[216:223], v[184:187], v156, v155 op_sel_hi:[0,0,0]
	s_setprio 0
	s_barrier
	s_add_i32 s63, s63, 2
	s_add_u32 s26, s26, 0x100
	s_addc_u32 s27, s27, 0
	s_add_u32 s61, s61, 0x100
	s_addc_u32 s62, s62, 0
	s_cmp_gt_u32 s63, 13
	s_cbranch_scc1 .Lpeel_exit_1084

.LBB0_1158:
	s_add_u32 s36, s36, 0xe0080
	s_addc_u32 s37, s37, 0
	s_add_u32 s1, s38, 0x100
	v_mov_b32_e32 v2, 0
	s_addc_u32 s68, s39, 0
	s_mov_b32 s69, -2
	ds_read_b128 v[166:169], v160
	ds_read_b128 v[170:173], v160 offset:1024
	ds_read_b128 v[174:177], v160 offset:2048
	ds_read_b128 v[178:181], v160 offset:3072
	ds_read_b128 v[182:185], v161
	ds_read_b128 v[186:189], v161 offset:1024
	ds_read_b128 v[224:227], v161 offset:2048
	ds_read_b128 v[228:231], v161 offset:3072
	s_add_u32 s38, s36, 0xfff20080
	s_addc_u32 s39, s37, -1
	s_cmp_eq_u32 s69, 52
	s_cselect_b32 s41, s31, s39
	s_cselect_b32 s40, s30, s38
	s_cselect_b32 s39, s35, s68
	s_cselect_b32 s38, s34, s1
	s_mov_b32 m0, s64
	v_lshl_add_u64 v[144:145], s[36:37], 0, v[140:141]
	ds_read_b128 v[192:195], v162
	ds_read_b128 v[196:199], v162 offset:1024
	ds_read_b128 v[200:203], v162 offset:2048
	ds_read_b128 v[204:207], v162 offset:3072
	ds_read_b128 v[208:211], v162 offset:4096
	ds_read_b128 v[212:215], v162 offset:5120
	ds_read_b128 v[216:219], v162 offset:6144
	ds_read_b128 v[220:223], v162 offset:7168
	global_load_lds_dwordx4 v[144:145], off
	v_lshl_add_u64 v[144:145], s[36:37], 0, v[142:143]
	s_mov_b32 m0, s65
	s_nop 0
	global_load_lds_dwordx4 v[144:145], off
	s_waitcnt vmcnt(8)
	s_waitcnt lgkmcnt(0)
	s_barrier
	s_setprio 1
	s_waitcnt lgkmcnt(0)
	s_nop 0
	v_mfma_scale_f32_16x16x128_f8f6f4 v[126:129], v[166:173], v[192:199], 0, v165, v164 op_sel_hi:[0,0,0]
	v_mfma_scale_f32_16x16x128_f8f6f4 v[122:125], v[174:181], v[192:199], 0, v165, v164 op_sel_hi:[0,0,0]
	v_mfma_scale_f32_16x16x128_f8f6f4 v[110:113], v[166:173], v[200:207], 0, v165, v164 op_sel_hi:[0,0,0]
	v_mfma_scale_f32_16x16x128_f8f6f4 v[106:109], v[174:181], v[200:207], 0, v165, v164 op_sel_hi:[0,0,0]
	v_mfma_scale_f32_16x16x128_f8f6f4 v[94:97], v[166:173], v[208:215], 0, v165, v164 op_sel_hi:[0,0,0]
	v_mfma_scale_f32_16x16x128_f8f6f4 v[90:93], v[174:181], v[208:215], 0, v165, v164 op_sel_hi:[0,0,0]
	v_mfma_scale_f32_16x16x128_f8f6f4 v[86:89], v[166:173], v[216:223], 0, v165, v164 op_sel_hi:[0,0,0]
	v_mfma_scale_f32_16x16x128_f8f6f4 v[78:81], v[174:181], v[216:223], 0, v165, v164 op_sel_hi:[0,0,0]
	s_setprio 0
	s_setprio 1
	s_nop 0
	v_mfma_scale_f32_16x16x128_f8f6f4 v[118:121], v[182:189], v[192:199], 0, v165, v164 op_sel_hi:[0,0,0]
	v_mfma_scale_f32_16x16x128_f8f6f4 v[114:117], v[224:231], v[192:199], 0, v165, v164 op_sel_hi:[0,0,0]
	v_mfma_scale_f32_16x16x128_f8f6f4 v[102:105], v[182:189], v[200:207], 0, v165, v164 op_sel_hi:[0,0,0]
	v_mfma_scale_f32_16x16x128_f8f6f4 v[98:101], v[224:231], v[200:207], 0, v165, v164 op_sel_hi:[0,0,0]
	v_mfma_scale_f32_16x16x128_f8f6f4 v[82:85], v[182:189], v[208:215], 0, v165, v164 op_sel_hi:[0,0,0]
	v_mfma_scale_f32_16x16x128_f8f6f4 v[74:77], v[224:231], v[208:215], 0, v165, v164 op_sel_hi:[0,0,0]
	v_mfma_scale_f32_16x16x128_f8f6f4 v[70:73], v[182:189], v[216:223], 0, v165, v164 op_sel_hi:[0,0,0]
	v_mfma_scale_f32_16x16x128_f8f6f4 v[66:69], v[224:231], v[216:223], 0, v165, v164 op_sel_hi:[0,0,0]
	s_setprio 0
	s_barrier
	s_add_i32 s70, s58, s50
	v_lshl_add_u64 v[144:145], s[38:39], 0, v[130:131]
	s_mov_b32 m0, s70
	ds_read_b128 v[192:195], v162 offset:16384
	ds_read_b128 v[196:199], v162 offset:17408
	ds_read_b128 v[200:203], v162 offset:18432
	ds_read_b128 v[204:207], v162 offset:19456
	ds_read_b128 v[208:211], v162 offset:20480
	ds_read_b128 v[212:215], v162 offset:21504
	ds_read_b128 v[216:219], v162 offset:22528
	ds_read_b128 v[220:223], v162 offset:23552
	global_load_lds_dwordx4 v[144:145], off
	s_add_i32 m0, s70, 0x2000
	s_add_u32 s70, s38, 0xe0000
	v_lshl_add_u64 v[148:149], s[38:39], 0, v[138:139]
	s_addc_u32 s71, s39, 0
	s_add_i32 s72, s59, s50
	global_load_lds_dwordx4 v[148:149], off
	v_lshl_add_u64 v[190:191], s[70:71], 0, v[130:131]
	s_mov_b32 m0, s72
	v_lshl_add_u64 v[240:241], s[40:41], 0, v[132:133]
	global_load_lds_dwordx4 v[190:191], off
	v_lshl_add_u64 v[190:191], s[70:71], 0, v[138:139]
	s_add_i32 m0, s72, 0x2000
	s_nop 0
	global_load_lds_dwordx4 v[190:191], off
	v_lshl_add_u64 v[190:191], s[40:41], 0, v[136:137]
	s_mov_b32 m0, s51
	s_nop 0
	global_load_lds_dwordx4 v[190:191], off
	s_mov_b32 m0, s52
	s_nop 0
	global_load_lds_dwordx4 v[240:241], off
	s_waitcnt vmcnt(8)
	s_waitcnt lgkmcnt(0)
	s_barrier
	s_setprio 1
	s_waitcnt lgkmcnt(0)
	s_nop 0
	v_mfma_scale_f32_16x16x128_f8f6f4 v[62:65], v[166:173], v[192:199], 0, v165, v164 op_sel_hi:[0,0,0]
	v_mfma_scale_f32_16x16x128_f8f6f4 v[58:61], v[174:181], v[192:199], 0, v165, v164 op_sel_hi:[0,0,0]
	v_mfma_scale_f32_16x16x128_f8f6f4 v[46:49], v[166:173], v[200:207], 0, v165, v164 op_sel_hi:[0,0,0]
	v_mfma_scale_f32_16x16x128_f8f6f4 v[42:45], v[174:181], v[200:207], 0, v165, v164 op_sel_hi:[0,0,0]
	v_mfma_scale_f32_16x16x128_f8f6f4 v[30:33], v[166:173], v[208:215], 0, v165, v164 op_sel_hi:[0,0,0]
	v_mfma_scale_f32_16x16x128_f8f6f4 v[26:29], v[174:181], v[208:215], 0, v165, v164 op_sel_hi:[0,0,0]
	v_mfma_scale_f32_16x16x128_f8f6f4 v[14:17], v[166:173], v[216:223], 0, v165, v164 op_sel_hi:[0,0,0]
	v_mfma_scale_f32_16x16x128_f8f6f4 v[10:13], v[174:181], v[216:223], 0, v165, v164 op_sel_hi:[0,0,0]
	s_setprio 0
	s_setprio 1
	s_nop 0
	v_mfma_scale_f32_16x16x128_f8f6f4 v[54:57], v[182:189], v[192:199], 0, v165, v164 op_sel_hi:[0,0,0]
	v_mfma_scale_f32_16x16x128_f8f6f4 v[50:53], v[224:231], v[192:199], 0, v165, v164 op_sel_hi:[0,0,0]
	v_mfma_scale_f32_16x16x128_f8f6f4 v[38:41], v[182:189], v[200:207], 0, v165, v164 op_sel_hi:[0,0,0]
	v_mfma_scale_f32_16x16x128_f8f6f4 v[34:37], v[224:231], v[200:207], 0, v165, v164 op_sel_hi:[0,0,0]
	v_mfma_scale_f32_16x16x128_f8f6f4 v[232:235], v[182:189], v[208:215], 0, v165, v164 op_sel_hi:[0,0,0]
	v_mfma_scale_f32_16x16x128_f8f6f4 v[236:239], v[224:231], v[208:215], 0, v165, v164 op_sel_hi:[0,0,0]
	v_mfma_scale_f32_16x16x128_f8f6f4 v[182:185], v[182:189], v[216:223], 0, v165, v164 op_sel_hi:[0,0,0]
	v_mfma_scale_f32_16x16x128_f8f6f4 v[186:189], v[224:231], v[216:223], 0, v165, v164 op_sel_hi:[0,0,0]
	s_setprio 0
	s_barrier
	s_add_i32 s70, 0, 0x18000
	s_add_i32 s71, 0, 0x1c000
	v_add_u32_e32 v22, s70, v158
	v_add_u32_e32 v178, s71, v158
	s_nop 0
	ds_read_b128 v[2:5], v22
	ds_read_b128 v[6:9], v22 offset:1024
	ds_read_b128 v[18:21], v22 offset:2048
	ds_read_b128 v[22:25], v22 offset:3072
	ds_read_b128 v[166:169], v178
	ds_read_b128 v[170:173], v178 offset:1024
	ds_read_b128 v[174:177], v178 offset:2048
	ds_read_b128 v[178:181], v178 offset:3072
	s_add_u32 s40, s40, 0xe0000
	s_addc_u32 s41, s41, 0
	s_mov_b32 m0, s53
	v_lshl_add_u64 v[224:225], s[40:41], 0, v[136:137]
	ds_read_b128 v[192:195], v162 offset:32768
	ds_read_b128 v[196:199], v162 offset:33792
	ds_read_b128 v[200:203], v162 offset:34816
	ds_read_b128 v[204:207], v162 offset:35840
	ds_read_b128 v[208:211], v162 offset:36864
	ds_read_b128 v[212:215], v162 offset:37888
	ds_read_b128 v[216:219], v162 offset:38912
	ds_read_b128 v[220:223], v162 offset:39936
	global_load_lds_dwordx4 v[224:225], off
	v_lshl_add_u64 v[224:225], s[40:41], 0, v[132:133]
	s_mov_b32 m0, s54
	s_nop 0
	global_load_lds_dwordx4 v[224:225], off
	s_waitcnt vmcnt(8)
	s_waitcnt lgkmcnt(0)
	s_barrier
	s_setprio 1
	s_waitcnt lgkmcnt(0)
	s_nop 0
	v_mfma_scale_f32_16x16x128_f8f6f4 v[126:129], v[2:9], v[192:199], v[126:129], v165, v164 op_sel_hi:[0,0,0]
	v_mfma_scale_f32_16x16x128_f8f6f4 v[122:125], v[18:25], v[192:199], v[122:125], v165, v164 op_sel_hi:[0,0,0]
	v_mfma_scale_f32_16x16x128_f8f6f4 v[110:113], v[2:9], v[200:207], v[110:113], v165, v164 op_sel_hi:[0,0,0]
	v_mfma_scale_f32_16x16x128_f8f6f4 v[106:109], v[18:25], v[200:207], v[106:109], v165, v164 op_sel_hi:[0,0,0]
	v_mfma_scale_f32_16x16x128_f8f6f4 v[94:97], v[2:9], v[208:215], v[94:97], v165, v164 op_sel_hi:[0,0,0]
	v_mfma_scale_f32_16x16x128_f8f6f4 v[90:93], v[18:25], v[208:215], v[90:93], v165, v164 op_sel_hi:[0,0,0]
	v_mfma_scale_f32_16x16x128_f8f6f4 v[86:89], v[2:9], v[216:223], v[86:89], v165, v164 op_sel_hi:[0,0,0]
	v_mfma_scale_f32_16x16x128_f8f6f4 v[78:81], v[18:25], v[216:223], v[78:81], v165, v164 op_sel_hi:[0,0,0]
	s_setprio 0
	s_setprio 1
	s_nop 0
	v_mfma_scale_f32_16x16x128_f8f6f4 v[118:121], v[166:173], v[192:199], v[118:121], v165, v164 op_sel_hi:[0,0,0]
	v_mfma_scale_f32_16x16x128_f8f6f4 v[114:117], v[174:181], v[192:199], v[114:117], v165, v164 op_sel_hi:[0,0,0]
	v_mfma_scale_f32_16x16x128_f8f6f4 v[102:105], v[166:173], v[200:207], v[102:105], v165, v164 op_sel_hi:[0,0,0]
	v_mfma_scale_f32_16x16x128_f8f6f4 v[98:101], v[174:181], v[200:207], v[98:101], v165, v164 op_sel_hi:[0,0,0]
	v_mfma_scale_f32_16x16x128_f8f6f4 v[82:85], v[166:173], v[208:215], v[82:85], v165, v164 op_sel_hi:[0,0,0]
	v_mfma_scale_f32_16x16x128_f8f6f4 v[74:77], v[174:181], v[208:215], v[74:77], v165, v164 op_sel_hi:[0,0,0]
	v_mfma_scale_f32_16x16x128_f8f6f4 v[70:73], v[166:173], v[216:223], v[70:73], v165, v164 op_sel_hi:[0,0,0]
	v_mfma_scale_f32_16x16x128_f8f6f4 v[66:69], v[174:181], v[216:223], v[66:69], v165, v164 op_sel_hi:[0,0,0]
	s_setprio 0
	s_barrier
	s_add_i32 s40, s70, s50
	v_lshl_add_u64 v[144:145], v[144:145], 0, s[14:15]
	s_mov_b32 m0, s40
	ds_read_b128 v[192:195], v162 offset:49152
	ds_read_b128 v[196:199], v162 offset:50176
	ds_read_b128 v[200:203], v162 offset:51200
	ds_read_b128 v[204:207], v162 offset:52224
	ds_read_b128 v[208:211], v162 offset:53248
	ds_read_b128 v[212:215], v162 offset:54272
	ds_read_b128 v[216:219], v162 offset:55296
	ds_read_b128 v[220:223], v162 offset:56320
	global_load_lds_dwordx4 v[144:145], off
	s_add_i32 m0, s40, 0x2000
	s_add_u32 s38, s38, 0xe0080
	v_lshl_add_u64 v[144:145], v[148:149], 0, s[14:15]
	s_addc_u32 s39, s39, 0
	s_add_i32 s40, s71, s50
	global_load_lds_dwordx4 v[144:145], off
	v_lshl_add_u64 v[144:145], s[38:39], 0, v[130:131]
	s_mov_b32 m0, s40
	s_nop 0
	global_load_lds_dwordx4 v[144:145], off
	v_lshl_add_u64 v[144:145], s[38:39], 0, v[138:139]
	s_add_i32 m0, s40, 0x2000
	s_nop 0
	global_load_lds_dwordx4 v[144:145], off
	v_lshl_add_u64 v[144:145], v[190:191], 0, s[14:15]
	s_mov_b32 m0, s56
	s_nop 0
	global_load_lds_dwordx4 v[144:145], off
	v_lshl_add_u64 v[144:145], v[240:241], 0, s[14:15]
	s_mov_b32 m0, s57
	s_nop 0
	global_load_lds_dwordx4 v[144:145], off
	s_waitcnt vmcnt(8)
	s_waitcnt lgkmcnt(0)
	s_barrier
	s_setprio 1
	s_waitcnt lgkmcnt(0)
	s_nop 0
	v_mfma_scale_f32_16x16x128_f8f6f4 v[62:65], v[2:9], v[192:199], v[62:65], v165, v164 op_sel_hi:[0,0,0]
	v_mfma_scale_f32_16x16x128_f8f6f4 v[58:61], v[18:25], v[192:199], v[58:61], v165, v164 op_sel_hi:[0,0,0]
	v_mfma_scale_f32_16x16x128_f8f6f4 v[46:49], v[2:9], v[200:207], v[46:49], v165, v164 op_sel_hi:[0,0,0]
	v_mfma_scale_f32_16x16x128_f8f6f4 v[42:45], v[18:25], v[200:207], v[42:45], v165, v164 op_sel_hi:[0,0,0]
	v_mfma_scale_f32_16x16x128_f8f6f4 v[30:33], v[2:9], v[208:215], v[30:33], v165, v164 op_sel_hi:[0,0,0]
	v_mfma_scale_f32_16x16x128_f8f6f4 v[26:29], v[18:25], v[208:215], v[26:29], v165, v164 op_sel_hi:[0,0,0]
	v_mfma_scale_f32_16x16x128_f8f6f4 v[14:17], v[2:9], v[216:223], v[14:17], v165, v164 op_sel_hi:[0,0,0]
	v_mfma_scale_f32_16x16x128_f8f6f4 v[10:13], v[18:25], v[216:223], v[10:13], v165, v164 op_sel_hi:[0,0,0]
	s_setprio 0
	s_setprio 1
	s_nop 0
	v_mfma_scale_f32_16x16x128_f8f6f4 v[54:57], v[166:173], v[192:199], v[54:57], v165, v164 op_sel_hi:[0,0,0]
	v_mfma_scale_f32_16x16x128_f8f6f4 v[50:53], v[174:181], v[192:199], v[50:53], v165, v164 op_sel_hi:[0,0,0]
	v_mfma_scale_f32_16x16x128_f8f6f4 v[38:41], v[166:173], v[200:207], v[38:41], v165, v164 op_sel_hi:[0,0,0]
	v_mfma_scale_f32_16x16x128_f8f6f4 v[34:37], v[174:181], v[200:207], v[34:37], v165, v164 op_sel_hi:[0,0,0]
	v_mfma_scale_f32_16x16x128_f8f6f4 v[22:25], v[166:173], v[208:215], v[232:235], v165, v164 op_sel_hi:[0,0,0]
	v_mfma_scale_f32_16x16x128_f8f6f4 v[18:21], v[174:181], v[208:215], v[236:239], v165, v164 op_sel_hi:[0,0,0]
	v_mfma_scale_f32_16x16x128_f8f6f4 v[6:9], v[166:173], v[216:223], v[182:185], v165, v164 op_sel_hi:[0,0,0]
	v_mfma_scale_f32_16x16x128_f8f6f4 v[2:5], v[174:181], v[216:223], v[186:189], v165, v164 op_sel_hi:[0,0,0]
	s_setprio 0
	s_barrier
	s_add_i32 s69, s69, 2
	s_add_u32 s36, s36, 0x100
	s_addc_u32 s37, s37, 0
	s_add_u32 s1, s1, 0x100
	s_addc_u32 s68, s68, 0
	s_cmp_gt_u32 s69, 53
	s_cbranch_scc1 .Lpeel_exit_1159

.LBB0_1178:
	v_mov_b32_e32 v123, 0
	s_andn2_b64 vcc, exec, s[10:11]
	v_mov_b32_e32 v122, v123
	v_pk_mov_b32 v[0:1], v[122:123], v[122:123]
	v_pk_mov_b32 v[2:3], v[122:123], v[122:123]
	v_pk_mov_b32 v[4:5], v[122:123], v[122:123]
	v_pk_mov_b32 v[6:7], v[122:123], v[122:123]
	v_pk_mov_b32 v[8:9], v[122:123], v[122:123]
	v_pk_mov_b32 v[10:11], v[122:123], v[122:123]
	v_pk_mov_b32 v[12:13], v[122:123], v[122:123]
	v_pk_mov_b32 v[14:15], v[122:123], v[122:123]
	v_pk_mov_b32 v[16:17], v[122:123], v[122:123]
	v_pk_mov_b32 v[18:19], v[122:123], v[122:123]
	v_pk_mov_b32 v[20:21], v[122:123], v[122:123]
	v_pk_mov_b32 v[22:23], v[122:123], v[122:123]
	v_pk_mov_b32 v[24:25], v[122:123], v[122:123]
	v_pk_mov_b32 v[26:27], v[122:123], v[122:123]
	v_pk_mov_b32 v[28:29], v[122:123], v[122:123]
	v_pk_mov_b32 v[30:31], v[122:123], v[122:123]
	v_pk_mov_b32 v[32:33], v[122:123], v[122:123]
	v_pk_mov_b32 v[34:35], v[122:123], v[122:123]
	v_pk_mov_b32 v[36:37], v[122:123], v[122:123]
	v_pk_mov_b32 v[38:39], v[122:123], v[122:123]
	v_pk_mov_b32 v[40:41], v[122:123], v[122:123]
	v_pk_mov_b32 v[42:43], v[122:123], v[122:123]
	v_pk_mov_b32 v[44:45], v[122:123], v[122:123]
	v_pk_mov_b32 v[46:47], v[122:123], v[122:123]
	v_pk_mov_b32 v[48:49], v[122:123], v[122:123]
	v_pk_mov_b32 v[50:51], v[122:123], v[122:123]
	v_pk_mov_b32 v[52:53], v[122:123], v[122:123]
	v_pk_mov_b32 v[54:55], v[122:123], v[122:123]
	v_pk_mov_b32 v[56:57], v[122:123], v[122:123]
	v_pk_mov_b32 v[58:59], v[122:123], v[122:123]
	v_pk_mov_b32 v[60:61], v[122:123], v[122:123]
	v_pk_mov_b32 v[62:63], v[122:123], v[122:123]
	v_pk_mov_b32 v[64:65], v[122:123], v[122:123]
	v_pk_mov_b32 v[66:67], v[122:123], v[122:123]
	v_pk_mov_b32 v[68:69], v[122:123], v[122:123]
	v_pk_mov_b32 v[70:71], v[122:123], v[122:123]
	v_pk_mov_b32 v[72:73], v[122:123], v[122:123]
	v_pk_mov_b32 v[74:75], v[122:123], v[122:123]
	v_pk_mov_b32 v[76:77], v[122:123], v[122:123]
	v_pk_mov_b32 v[78:79], v[122:123], v[122:123]
	v_pk_mov_b32 v[80:81], v[122:123], v[122:123]
	v_pk_mov_b32 v[82:83], v[122:123], v[122:123]
	v_pk_mov_b32 v[84:85], v[122:123], v[122:123]
	v_pk_mov_b32 v[86:87], v[122:123], v[122:123]
	v_pk_mov_b32 v[88:89], v[122:123], v[122:123]
	v_pk_mov_b32 v[90:91], v[122:123], v[122:123]
	v_pk_mov_b32 v[92:93], v[122:123], v[122:123]
	v_pk_mov_b32 v[94:95], v[122:123], v[122:123]
	v_pk_mov_b32 v[96:97], v[122:123], v[122:123]
	v_pk_mov_b32 v[98:99], v[122:123], v[122:123]
	v_pk_mov_b32 v[100:101], v[122:123], v[122:123]
	v_pk_mov_b32 v[102:103], v[122:123], v[122:123]
	v_pk_mov_b32 v[104:105], v[122:123], v[122:123]
	v_pk_mov_b32 v[106:107], v[122:123], v[122:123]
	v_pk_mov_b32 v[108:109], v[122:123], v[122:123]
	v_pk_mov_b32 v[110:111], v[122:123], v[122:123]
	v_pk_mov_b32 v[112:113], v[122:123], v[122:123]
	v_pk_mov_b32 v[114:115], v[122:123], v[122:123]
	v_pk_mov_b32 v[116:117], v[122:123], v[122:123]
	v_pk_mov_b32 v[118:119], v[122:123], v[122:123]
	v_pk_mov_b32 v[120:121], v[122:123], v[122:123]
	v_pk_mov_b32 v[124:125], v[122:123], v[122:123]
	v_pk_mov_b32 v[126:127], v[122:123], v[122:123]
	s_cbranch_vccnz .LBB0_1181
	s_add_u32 s22, s22, 0xe0080
	s_addc_u32 s23, s23, 0
	s_add_u32 s68, s24, 0x100
	v_mov_b32_e32 v0, 0
	s_addc_u32 s69, s25, 0
	s_mov_b32 s24, 0
	ds_read_b128 v[158:161], v152
	ds_read_b128 v[162:165], v152 offset:1024
	ds_read_b128 v[166:169], v152 offset:2048
	ds_read_b128 v[170:173], v152 offset:3072
	ds_read_b128 v[174:177], v153
	ds_read_b128 v[178:181], v153 offset:1024
	ds_read_b128 v[182:185], v153 offset:2048
	ds_read_b128 v[186:189], v153 offset:3072
	s_add_i32 s70, s24, 2
	s_add_u32 s25, s22, 0xfff20080
	s_addc_u32 s26, s23, -1
	s_cmp_eq_u32 s58, s24
	s_cselect_b32 s24, s18, s68
	s_cselect_b32 s27, s17, s26
	s_cselect_b32 s26, s16, s25
	s_cselect_b32 s25, s19, s69
	v_lshl_add_u64 v[140:141], s[22:23], 0, v[136:137]
	s_add_i32 m0, s21, 0xc000
	ds_read_b128 v[192:195], v154
	ds_read_b128 v[196:199], v154 offset:1024
	ds_read_b128 v[200:203], v154 offset:2048
	ds_read_b128 v[204:207], v154 offset:3072
	ds_read_b128 v[208:211], v154 offset:4096
	ds_read_b128 v[212:215], v154 offset:5120
	ds_read_b128 v[216:219], v154 offset:6144
	ds_read_b128 v[220:223], v154 offset:7168
	global_load_lds_dwordx4 v[140:141], off
	v_lshl_add_u64 v[140:141], s[22:23], 0, v[138:139]
	s_add_i32 m0, s21, 0xe000
	s_nop 0
	global_load_lds_dwordx4 v[140:141], off
	s_waitcnt vmcnt(8)
	s_waitcnt lgkmcnt(0)
	s_barrier
	s_setprio 1
	s_waitcnt lgkmcnt(0)
	s_nop 0
	v_mfma_scale_f32_16x16x128_f8f6f4 v[120:123], v[158:165], v[192:199], 0, v156, v155 op_sel_hi:[0,0,0]
	v_mfma_scale_f32_16x16x128_f8f6f4 v[124:127], v[166:173], v[192:199], 0, v156, v155 op_sel_hi:[0,0,0]
	v_mfma_scale_f32_16x16x128_f8f6f4 v[108:111], v[158:165], v[200:207], 0, v156, v155 op_sel_hi:[0,0,0]
	v_mfma_scale_f32_16x16x128_f8f6f4 v[104:107], v[166:173], v[200:207], 0, v156, v155 op_sel_hi:[0,0,0]
	v_mfma_scale_f32_16x16x128_f8f6f4 v[92:95], v[158:165], v[208:215], 0, v156, v155 op_sel_hi:[0,0,0]
	v_mfma_scale_f32_16x16x128_f8f6f4 v[88:91], v[166:173], v[208:215], 0, v156, v155 op_sel_hi:[0,0,0]
	v_mfma_scale_f32_16x16x128_f8f6f4 v[76:79], v[158:165], v[216:223], 0, v156, v155 op_sel_hi:[0,0,0]
	v_mfma_scale_f32_16x16x128_f8f6f4 v[72:75], v[166:173], v[216:223], 0, v156, v155 op_sel_hi:[0,0,0]
	s_setprio 0
	s_setprio 1
	s_nop 0
	v_mfma_scale_f32_16x16x128_f8f6f4 v[116:119], v[174:181], v[192:199], 0, v156, v155 op_sel_hi:[0,0,0]
	v_mfma_scale_f32_16x16x128_f8f6f4 v[112:115], v[182:189], v[192:199], 0, v156, v155 op_sel_hi:[0,0,0]
	v_mfma_scale_f32_16x16x128_f8f6f4 v[100:103], v[174:181], v[200:207], 0, v156, v155 op_sel_hi:[0,0,0]
	v_mfma_scale_f32_16x16x128_f8f6f4 v[96:99], v[182:189], v[200:207], 0, v156, v155 op_sel_hi:[0,0,0]
	v_mfma_scale_f32_16x16x128_f8f6f4 v[84:87], v[174:181], v[208:215], 0, v156, v155 op_sel_hi:[0,0,0]
	v_mfma_scale_f32_16x16x128_f8f6f4 v[80:83], v[182:189], v[208:215], 0, v156, v155 op_sel_hi:[0,0,0]
	v_mfma_scale_f32_16x16x128_f8f6f4 v[68:71], v[174:181], v[216:223], 0, v156, v155 op_sel_hi:[0,0,0]
	v_mfma_scale_f32_16x16x128_f8f6f4 v[64:67], v[182:189], v[216:223], 0, v156, v155 op_sel_hi:[0,0,0]
	s_setprio 0
	s_barrier
	s_add_i32 s71, s62, s38
	v_lshl_add_u64 v[144:145], s[24:25], 0, v[128:129]
	s_mov_b32 m0, s71
	ds_read_b128 v[192:195], v154 offset:16384
	ds_read_b128 v[196:199], v154 offset:17408
	ds_read_b128 v[200:203], v154 offset:18432
	ds_read_b128 v[204:207], v154 offset:19456
	ds_read_b128 v[208:211], v154 offset:20480
	ds_read_b128 v[212:215], v154 offset:21504
	ds_read_b128 v[216:219], v154 offset:22528
	ds_read_b128 v[220:223], v154 offset:23552
	global_load_lds_dwordx4 v[144:145], off
	s_add_i32 m0, s71, 0x2000
	s_add_u32 s72, s24, 0xe0000
	v_lshl_add_u64 v[148:149], s[24:25], 0, v[134:135]
	s_addc_u32 s73, s25, 0
	s_add_i32 s71, s63, s38
	global_load_lds_dwordx4 v[148:149], off
	v_lshl_add_u64 v[140:141], s[72:73], 0, v[128:129]
	s_mov_b32 m0, s71
	v_lshl_add_u64 v[190:191], s[26:27], 0, v[132:133]
	global_load_lds_dwordx4 v[140:141], off
	v_lshl_add_u64 v[140:141], s[72:73], 0, v[134:135]
	s_add_i32 m0, s71, 0x2000
	v_lshl_add_u64 v[228:229], s[26:27], 0, v[130:131]
	global_load_lds_dwordx4 v[140:141], off
	s_mov_b32 m0, s21
	s_nop 0
	global_load_lds_dwordx4 v[190:191], off
	s_mov_b32 m0, s39
	s_nop 0
	global_load_lds_dwordx4 v[228:229], off
	s_waitcnt vmcnt(8)
	s_waitcnt lgkmcnt(0)
	s_barrier
	s_setprio 1
	s_waitcnt lgkmcnt(0)
	s_nop 0
	v_mfma_scale_f32_16x16x128_f8f6f4 v[60:63], v[158:165], v[192:199], 0, v156, v155 op_sel_hi:[0,0,0]
	v_mfma_scale_f32_16x16x128_f8f6f4 v[56:59], v[166:173], v[192:199], 0, v156, v155 op_sel_hi:[0,0,0]
	v_mfma_scale_f32_16x16x128_f8f6f4 v[44:47], v[158:165], v[200:207], 0, v156, v155 op_sel_hi:[0,0,0]
	v_mfma_scale_f32_16x16x128_f8f6f4 v[40:43], v[166:173], v[200:207], 0, v156, v155 op_sel_hi:[0,0,0]
	v_mfma_scale_f32_16x16x128_f8f6f4 v[28:31], v[158:165], v[208:215], 0, v156, v155 op_sel_hi:[0,0,0]
	v_mfma_scale_f32_16x16x128_f8f6f4 v[24:27], v[166:173], v[208:215], 0, v156, v155 op_sel_hi:[0,0,0]
	v_mfma_scale_f32_16x16x128_f8f6f4 v[12:15], v[158:165], v[216:223], 0, v156, v155 op_sel_hi:[0,0,0]
	v_mfma_scale_f32_16x16x128_f8f6f4 v[8:11], v[166:173], v[216:223], 0, v156, v155 op_sel_hi:[0,0,0]
	s_setprio 0
	s_setprio 1
	s_nop 0
	v_mfma_scale_f32_16x16x128_f8f6f4 v[52:55], v[174:181], v[192:199], 0, v156, v155 op_sel_hi:[0,0,0]
	v_mfma_scale_f32_16x16x128_f8f6f4 v[48:51], v[182:189], v[192:199], 0, v156, v155 op_sel_hi:[0,0,0]
	v_mfma_scale_f32_16x16x128_f8f6f4 v[36:39], v[174:181], v[200:207], 0, v156, v155 op_sel_hi:[0,0,0]
	v_mfma_scale_f32_16x16x128_f8f6f4 v[32:35], v[182:189], v[200:207], 0, v156, v155 op_sel_hi:[0,0,0]
	v_mfma_scale_f32_16x16x128_f8f6f4 v[140:143], v[174:181], v[208:215], 0, v156, v155 op_sel_hi:[0,0,0]
	v_mfma_scale_f32_16x16x128_f8f6f4 v[224:227], v[182:189], v[208:215], 0, v156, v155 op_sel_hi:[0,0,0]
	v_mfma_scale_f32_16x16x128_f8f6f4 v[174:177], v[174:181], v[216:223], 0, v156, v155 op_sel_hi:[0,0,0]
	v_mfma_scale_f32_16x16x128_f8f6f4 v[178:181], v[182:189], v[216:223], 0, v156, v155 op_sel_hi:[0,0,0]
	s_setprio 0
	s_barrier
	s_add_i32 s71, 0, 0x18000
	s_add_i32 s72, 0, 0x1c000
	v_add_u32_e32 v20, s71, v150
	v_add_u32_e32 v157, s72, v150
	s_nop 0
	ds_read_b128 v[0:3], v20
	ds_read_b128 v[4:7], v20 offset:1024
	ds_read_b128 v[16:19], v20 offset:2048
	ds_read_b128 v[20:23], v20 offset:3072
	ds_read_b128 v[158:161], v157
	ds_read_b128 v[162:165], v157 offset:1024
	ds_read_b128 v[166:169], v157 offset:2048
	ds_read_b128 v[170:173], v157 offset:3072
	s_add_u32 s26, s26, 0xe0000
	s_addc_u32 s27, s27, 0
	s_mov_b32 m0, s40
	v_lshl_add_u64 v[182:183], s[26:27], 0, v[132:133]
	ds_read_b128 v[192:195], v154 offset:32768
	ds_read_b128 v[196:199], v154 offset:33792
	ds_read_b128 v[200:203], v154 offset:34816
	ds_read_b128 v[204:207], v154 offset:35840
	ds_read_b128 v[208:211], v154 offset:36864
	ds_read_b128 v[212:215], v154 offset:37888
	ds_read_b128 v[216:219], v154 offset:38912
	ds_read_b128 v[220:223], v154 offset:39936
	global_load_lds_dwordx4 v[182:183], off
	v_lshl_add_u64 v[182:183], s[26:27], 0, v[130:131]
	s_mov_b32 m0, s41
	s_nop 0
	global_load_lds_dwordx4 v[182:183], off
	s_waitcnt vmcnt(8)
	s_waitcnt lgkmcnt(0)
	s_barrier
	s_setprio 1
	s_waitcnt lgkmcnt(0)
	s_nop 0
	v_mfma_scale_f32_16x16x128_f8f6f4 v[120:123], v[0:7], v[192:199], v[120:123], v156, v155 op_sel_hi:[0,0,0]
	v_mfma_scale_f32_16x16x128_f8f6f4 v[124:127], v[16:23], v[192:199], v[124:127], v156, v155 op_sel_hi:[0,0,0]
	v_mfma_scale_f32_16x16x128_f8f6f4 v[108:111], v[0:7], v[200:207], v[108:111], v156, v155 op_sel_hi:[0,0,0]
	v_mfma_scale_f32_16x16x128_f8f6f4 v[104:107], v[16:23], v[200:207], v[104:107], v156, v155 op_sel_hi:[0,0,0]
	v_mfma_scale_f32_16x16x128_f8f6f4 v[92:95], v[0:7], v[208:215], v[92:95], v156, v155 op_sel_hi:[0,0,0]
	v_mfma_scale_f32_16x16x128_f8f6f4 v[88:91], v[16:23], v[208:215], v[88:91], v156, v155 op_sel_hi:[0,0,0]
	v_mfma_scale_f32_16x16x128_f8f6f4 v[76:79], v[0:7], v[216:223], v[76:79], v156, v155 op_sel_hi:[0,0,0]
	v_mfma_scale_f32_16x16x128_f8f6f4 v[72:75], v[16:23], v[216:223], v[72:75], v156, v155 op_sel_hi:[0,0,0]
	s_setprio 0
	s_setprio 1
	s_nop 0
	v_mfma_scale_f32_16x16x128_f8f6f4 v[116:119], v[158:165], v[192:199], v[116:119], v156, v155 op_sel_hi:[0,0,0]
	v_mfma_scale_f32_16x16x128_f8f6f4 v[112:115], v[166:173], v[192:199], v[112:115], v156, v155 op_sel_hi:[0,0,0]
	v_mfma_scale_f32_16x16x128_f8f6f4 v[100:103], v[158:165], v[200:207], v[100:103], v156, v155 op_sel_hi:[0,0,0]
	v_mfma_scale_f32_16x16x128_f8f6f4 v[96:99], v[166:173], v[200:207], v[96:99], v156, v155 op_sel_hi:[0,0,0]
	v_mfma_scale_f32_16x16x128_f8f6f4 v[84:87], v[158:165], v[208:215], v[84:87], v156, v155 op_sel_hi:[0,0,0]
	v_mfma_scale_f32_16x16x128_f8f6f4 v[80:83], v[166:173], v[208:215], v[80:83], v156, v155 op_sel_hi:[0,0,0]
	v_mfma_scale_f32_16x16x128_f8f6f4 v[68:71], v[158:165], v[216:223], v[68:71], v156, v155 op_sel_hi:[0,0,0]
	v_mfma_scale_f32_16x16x128_f8f6f4 v[64:67], v[166:173], v[216:223], v[64:67], v156, v155 op_sel_hi:[0,0,0]
	s_setprio 0
	s_barrier
	s_add_i32 s26, s71, s38
	v_lshl_add_u64 v[144:145], v[144:145], 0, s[8:9]
	s_mov_b32 m0, s26
	ds_read_b128 v[192:195], v154 offset:49152
	ds_read_b128 v[196:199], v154 offset:50176
	ds_read_b128 v[200:203], v154 offset:51200
	ds_read_b128 v[204:207], v154 offset:52224
	ds_read_b128 v[208:211], v154 offset:53248
	ds_read_b128 v[212:215], v154 offset:54272
	ds_read_b128 v[216:219], v154 offset:55296
	ds_read_b128 v[220:223], v154 offset:56320
	global_load_lds_dwordx4 v[144:145], off
	s_add_i32 m0, s26, 0x2000
	s_add_u32 s24, s24, 0xe0080
	v_lshl_add_u64 v[144:145], v[148:149], 0, s[8:9]
	s_addc_u32 s25, s25, 0
	s_add_i32 s26, s72, s38
	global_load_lds_dwordx4 v[144:145], off
	v_lshl_add_u64 v[144:145], s[24:25], 0, v[128:129]
	s_mov_b32 m0, s26
	s_nop 0
	global_load_lds_dwordx4 v[144:145], off
	v_lshl_add_u64 v[144:145], s[24:25], 0, v[134:135]
	s_add_i32 m0, s26, 0x2000
	s_nop 0
	global_load_lds_dwordx4 v[144:145], off
	v_lshl_add_u64 v[144:145], v[190:191], 0, s[8:9]
	s_mov_b32 m0, s55
	s_nop 0
	global_load_lds_dwordx4 v[144:145], off
	v_lshl_add_u64 v[144:145], v[228:229], 0, s[8:9]
	s_mov_b32 m0, s56
	s_nop 0
	global_load_lds_dwordx4 v[144:145], off
	s_waitcnt vmcnt(8)
	s_waitcnt lgkmcnt(0)
	s_barrier
	s_setprio 1
	s_waitcnt lgkmcnt(0)
	s_nop 0
	v_mfma_scale_f32_16x16x128_f8f6f4 v[60:63], v[0:7], v[192:199], v[60:63], v156, v155 op_sel_hi:[0,0,0]
	v_mfma_scale_f32_16x16x128_f8f6f4 v[56:59], v[16:23], v[192:199], v[56:59], v156, v155 op_sel_hi:[0,0,0]
	v_mfma_scale_f32_16x16x128_f8f6f4 v[44:47], v[0:7], v[200:207], v[44:47], v156, v155 op_sel_hi:[0,0,0]
	v_mfma_scale_f32_16x16x128_f8f6f4 v[40:43], v[16:23], v[200:207], v[40:43], v156, v155 op_sel_hi:[0,0,0]
	v_mfma_scale_f32_16x16x128_f8f6f4 v[28:31], v[0:7], v[208:215], v[28:31], v156, v155 op_sel_hi:[0,0,0]
	v_mfma_scale_f32_16x16x128_f8f6f4 v[24:27], v[16:23], v[208:215], v[24:27], v156, v155 op_sel_hi:[0,0,0]
	v_mfma_scale_f32_16x16x128_f8f6f4 v[12:15], v[0:7], v[216:223], v[12:15], v156, v155 op_sel_hi:[0,0,0]
	v_mfma_scale_f32_16x16x128_f8f6f4 v[8:11], v[16:23], v[216:223], v[8:11], v156, v155 op_sel_hi:[0,0,0]
	s_setprio 0
	s_setprio 1
	s_nop 0
	v_mfma_scale_f32_16x16x128_f8f6f4 v[52:55], v[158:165], v[192:199], v[52:55], v156, v155 op_sel_hi:[0,0,0]
	v_mfma_scale_f32_16x16x128_f8f6f4 v[48:51], v[166:173], v[192:199], v[48:51], v156, v155 op_sel_hi:[0,0,0]
	v_mfma_scale_f32_16x16x128_f8f6f4 v[36:39], v[158:165], v[200:207], v[36:39], v156, v155 op_sel_hi:[0,0,0]
	v_mfma_scale_f32_16x16x128_f8f6f4 v[32:35], v[166:173], v[200:207], v[32:35], v156, v155 op_sel_hi:[0,0,0]
	v_mfma_scale_f32_16x16x128_f8f6f4 v[20:23], v[158:165], v[208:215], v[140:143], v156, v155 op_sel_hi:[0,0,0]
	v_mfma_scale_f32_16x16x128_f8f6f4 v[16:19], v[166:173], v[208:215], v[224:227], v156, v155 op_sel_hi:[0,0,0]
	v_mfma_scale_f32_16x16x128_f8f6f4 v[4:7], v[158:165], v[216:223], v[174:177], v156, v155 op_sel_hi:[0,0,0]
	v_mfma_scale_f32_16x16x128_f8f6f4 v[0:3], v[166:173], v[216:223], v[178:181], v156, v155 op_sel_hi:[0,0,0]
	s_setprio 0
	s_barrier
	s_add_u32 s22, s22, 0x100
	s_addc_u32 s23, s23, 0
	s_add_u32 s68, s68, 0x100
	s_addc_u32 s69, s69, 0
	s_cmp_ge_i32 s70, s54
	s_mov_b32 s24, s70
	s_cbranch_scc1 .Lpeel_exit_1180

.Lpeel_exit_1180:
.LBB0_1181:
	s_and_b64 vcc, exec, s[12:13]
	s_cbranch_vccz .LBB0_1183
	s_barrier
